# converter assignment v2: W_UP1 stays in P0 (warm for P1), tails convert UP2 / DN1(next) / IN(next); P0 of layers 1-3 does UP1 + late weights only
# baseline (speedup 1.0000x reference)
; #define LAS __attribute__((address_space(3)))
; #define IN(k) in_range(lo, hi, (k))
; __global__ void __launch_bounds__(NWAVES * 64, 2) mk_fwd(Args args) {
;     ...
;         if (EN(0) && IN(pb + 0)) {
;             PH_LOCALS
;             LAS float* scr = (LAS float*)(lds + RING_OFF + wave * 16640);   static_assert(8 * 16640 <= LDSCTL_OFF, "converter scratch below the LDS control words");
;             constexpr int I_UP = (D / 64) * (NUP / 64), I_DN = (DFF / 64) * (D / 64), I_IN = (D / 64) * (DINP / 64), I_GLU = 16 * 16, I_L = 4 * 16, I_V1 = 16 * 4, I_V2 = 4 * 16,
;                           I_BS5 = 16 * 32, I_BAT = 8 * 32, I_BRW = 16 * 32, I_OUT = 32 * 32;
;             constexpr int NITEMS = 2 * I_UP + 2 * I_DN + I_IN + I_GLU + 3 * I_L + I_V1 + I_V2 + I_BS5 + I_BAT + I_BRW + I_OUT;
;             const int lv = l > 0 ? l - 1 : 0;
;     ...
;             for (int it = gw; it < NITEMS; it += NGW) {
;                 ConvItem ca; CONV_DESC(ca, it);
;                 float va[64];
;                 conv_load(ca, lane, va);
;                 conv_store(ca, scr, lane, va);
;             }
.LBB0_25:
	s_mul_i32 s6, s58, 15
	s_add_i32 s2, s6, 1
	s_cmp_gt_i32 s77, s2
	s_cselect_b64 s[0:1], -1, 0
	s_add_i32 s3, s6, 16
	s_cmp_lt_i32 s76, s3
	s_cselect_b64 s[4:5], -1, 0
	s_and_b64 s[0:1], s[0:1], s[4:5]
	s_andn2_b64 vcc, exec, s[0:1]
	s_cbranch_vccnz .LBB0_24
	v_writelane_b32 v254, s6, 36
	v_writelane_b32 v254, s3, 37
	s_mov_b32 s3, s2
	s_cmp_gt_i32 s76, s3
	s_cselect_b64 s[0:1], -1, 0
	s_cmp_ge_i32 s3, s77
	s_cselect_b64 s[4:5], -1, 0
	s_or_b64 s[0:1], s[0:1], s[4:5]
	v_writelane_b32 v254, s58, 38
	s_and_b64 vcc, exec, s[0:1]
	s_cbranch_vccnz .LBB0_92
	v_readlane_b32 s98, v254, 38
	s_nop 3
	s_cmp_lt_u32 s98, 1
	s_movk_i32 s99, 0x1580
	s_cselect_b32 s99, 0x69c0, s99
	v_readlane_b32 s0, v254, 8
	v_readlane_b32 s4, v254, 10
	v_readlane_b32 s1, v254, 9
	v_mbcnt_lo_u32_b32 v11, -1, 0
	v_mbcnt_hi_u32_b32 v11, -1, v11
	s_load_dword s6, s[0:1], 0x0
	s_mov_b32 s3, s84
	s_waitcnt lgkmcnt(0)
	s_lshl_b32 s3, s3, 3
	v_readlane_b32 s0, v254, 0
	s_add_i32 s3, s3, s4
	v_readlane_b32 s1, v254, 1
	s_cmp_ge_i32 s3, s99
	s_cbranch_scc1 .Lmy_p0_second
	s_load_dwordx2 s[8:9], s[0:1], 0x138
	v_readlane_b32 s14, v254, 38
	s_mulk_i32 s4, 0x4100
	s_add_i32 s7, s4, 0
	v_sub_u32_e64 v0, s14, 1 clamp
	s_lshl_b32 s33, s6, 3
	v_readfirstlane_b32 s4, v0
	s_lshl_b32 s96, s4, 16
	s_waitcnt lgkmcnt(0)
	s_add_u32 s4, s8, 0x22800000
	s_addc_u32 s5, s9, 0
	v_writelane_b32 v254, s4, 39
	s_mov_b32 s15, s97
	v_and_b32_e32 v0, 7, v11
	v_writelane_b32 v254, s5, 40
	s_add_u32 s4, s8, 0x22780000
	s_addc_u32 s5, s9, 0
	v_writelane_b32 v254, s4, 41
	v_ashrrev_i32_e32 v13, 3, v11
	v_lshlrev_b32_e32 v10, 3, v0
	v_writelane_b32 v254, s5, 42
	s_lshl_b32 s4, s14, 18
	s_add_u32 s10, s8, 0x22700000
	s_addc_u32 s11, s9, 0
	v_writelane_b32 v254, s10, 43
	s_mov_b32 s5, s97
	v_mul_u32_u24_e32 v0, 0x820, v0
	v_writelane_b32 v254, s11, 44
	s_mul_i32 s10, s14, 0x18000
	s_mov_b32 s11, s97
	v_writelane_b32 v254, s10, 45
	v_lshlrev_b32_e32 v1, 2, v13
	v_lshl_add_u32 v12, v11, 2, s7
	v_writelane_b32 v254, s11, 46
	s_add_u32 s10, s8, 0x22680000
	s_addc_u32 s11, s9, 0
	v_writelane_b32 v254, s10, 47
	v_add3_u32 v14, s7, v0, v1
	s_mov_b32 s41, s97
	v_writelane_b32 v254, s11, 48
	s_add_u32 s10, s8, 0x22600000
	s_addc_u32 s11, s9, 0
	v_writelane_b32 v254, s10, 49
	s_nop 1
	v_writelane_b32 v254, s11, 50
	s_lshl_b32 s10, s14, 20
	s_mov_b32 s11, s97
	v_writelane_b32 v254, s10, 51
	s_nop 1
	v_writelane_b32 v254, s11, 52
	s_add_u32 s10, s8, 0x22400000
	s_addc_u32 s11, s9, 0
	v_writelane_b32 v254, s10, 53
	s_nop 1
	v_writelane_b32 v254, s11, 54
	s_lshl_b32 s10, s14, 21
	s_mov_b32 s11, s97
	v_writelane_b32 v254, s10, 55
	s_nop 1
	v_writelane_b32 v254, s11, 56
	s_add_u32 s10, s8, 0x22e80000
	s_addc_u32 s11, s9, 0
	v_writelane_b32 v254, s10, 57
	s_nop 1
	v_writelane_b32 v254, s11, 58
	s_add_u32 s10, s8, 0x27b80000
	s_addc_u32 s11, s9, 0
	v_writelane_b32 v254, s10, 59
	s_nop 1
	v_writelane_b32 v254, s11, 60
	s_add_u32 s10, s8, 0x22880000
	s_addc_u32 s11, s9, 0
	v_writelane_b32 v254, s10, 61
	s_nop 1
	v_writelane_b32 v254, s11, 62
	s_lshl_b32 s10, s14, 22
	s_add_u32 s12, s8, 0x23280000
	s_addc_u32 s13, s9, 0
	v_writelane_b32 v254, s12, 63
	s_mov_b32 s11, s97
	s_nop 0
	v_writelane_b32 v255, s13, 0
	s_mul_i32 s12, s14, 0xac0000
	s_mov_b32 s13, s97
	v_writelane_b32 v255, s12, 1
	s_nop 1
	v_writelane_b32 v255, s13, 2
	s_add_u32 s12, s8, 0x26580000
	s_addc_u32 s13, s9, 0
	v_writelane_b32 v255, s12, 3
	s_nop 1
	v_writelane_b32 v255, s13, 4
	s_add_u32 s12, s8, 0x1d200000
	s_addc_u32 s13, s9, 0
	s_lshl_b32 s40, s14, 11
	v_writelane_b32 v255, s12, 5
	s_add_u32 s16, s8, 0x1e800000
	s_addc_u32 s17, s9, 0
	v_writelane_b32 v255, s13, 6
	v_writelane_b32 v255, s16, 7
	s_mul_i32 s12, s14, 0x1de0000
	s_mul_i32 s14, s14, 0x1580000
	v_writelane_b32 v255, s17, 8
	v_writelane_b32 v255, s14, 9
	s_mov_b32 s13, s97
	s_nop 0
	v_writelane_b32 v255, s15, 10
	s_add_u32 s14, s8, 0x23a80000
	s_addc_u32 s15, s9, 0
	v_writelane_b32 v255, s14, 11
	s_add_u32 s8, s8, 0x1a700000
	s_addc_u32 s9, s9, 0
	v_writelane_b32 v255, s15, 12
	v_writelane_b32 v255, s8, 13
	s_lshl_b64 s[4:5], s[4:5], 2
	s_lshl_b32 s7, s3, 4
	v_writelane_b32 v255, s9, 14
	v_writelane_b32 v255, s4, 15
	s_add_i32 s72, s7, 0xc00
	s_lshl_b32 s7, s3, 1
	v_writelane_b32 v255, s5, 16
	s_lshl_b64 s[4:5], s[10:11], 2
	v_writelane_b32 v255, s4, 17
	s_lshl_b32 s66, s3, 6
	s_lshl_b32 s67, s6, 9
	v_writelane_b32 v255, s5, 18
	s_lshl_b64 s[4:5], s[12:13], 2
	v_writelane_b32 v255, s4, 19
	s_lshl_b32 s68, s3, 5
	s_lshl_b32 s69, s6, 8
	v_writelane_b32 v255, s5, 20
	v_writelane_b32 v255, s80, 21
	s_lshl_b32 s70, s3, 2
	s_lshl_b32 s71, s6, 5
	v_writelane_b32 v255, s81, 22
	v_writelane_b32 v255, s82, 23
	s_lshl_b32 s73, s6, 7
	s_add_i32 s74, s7, 0x13500
	s_lshl_b32 s75, s6, 4
	v_writelane_b32 v255, s83, 24
	s_branch .LBB0_31

; __device__ __forceinline__ void conv_load(const ConvItem& ci, int lane, float (&v)[64]) {
;     ...
;     for (int i = 0; i < 64; ++i) { const int k = ci.k0 + i, kk = k < kmax ? k : kmax; v[i] = __builtin_nontemporal_load(base + (size_t)kk * ci.ldw); }
; #pragma unroll
;     for (int i = 0; i < 64; ++i) v[i] = (okc && (ci.k0 + i) < ci.Ksrc) ? v[i] : 0.f;
.LBB0_30:
	s_cmp_lt_i32 s58, s76
	s_cselect_b64 s[4:5], -1, 0
	s_and_b64 s[4:5], vcc, s[4:5]
	s_cmp_lt_i32 s64, s76
	s_waitcnt vmcnt(62)
	v_cndmask_b32_e64 v21, 0, v21, s[4:5]
	s_cselect_b64 s[4:5], -1, 0
	s_and_b64 s[4:5], vcc, s[4:5]
	s_cmp_lt_i32 s65, s76
	v_cndmask_b32_e64 v20, 0, v20, s[4:5]
	s_cselect_b64 s[4:5], -1, 0
	s_and_b64 s[4:5], vcc, s[4:5]
	s_cmp_lt_i32 s78, s76
	s_waitcnt vmcnt(61)
	v_cndmask_b32_e64 v19, 0, v19, s[4:5]
	s_cselect_b64 s[4:5], -1, 0
	s_and_b64 s[4:5], vcc, s[4:5]
	s_cmp_lt_i32 s79, s76
	s_waitcnt vmcnt(60)
	v_cndmask_b32_e64 v18, 0, v18, s[4:5]
	s_cselect_b64 s[4:5], -1, 0
	s_and_b64 s[4:5], vcc, s[4:5]
	s_cmp_lt_i32 s80, s76
	s_waitcnt vmcnt(59)
	v_cndmask_b32_e64 v17, 0, v17, s[4:5]
	s_cselect_b64 s[4:5], -1, 0
	s_and_b64 s[4:5], vcc, s[4:5]
	s_cmp_lt_i32 s81, s76
	s_waitcnt vmcnt(58)
	v_cndmask_b32_e64 v16, 0, v16, s[4:5]
	s_cselect_b64 s[4:5], -1, 0
	s_and_b64 s[4:5], vcc, s[4:5]
	s_cmp_lt_i32 s82, s76
	s_waitcnt vmcnt(57)
	v_cndmask_b32_e64 v15, 0, v15, s[4:5]
	s_cselect_b64 s[4:5], -1, 0
	s_and_b64 s[4:5], vcc, s[4:5]
	s_cmp_lt_i32 s83, s76
	s_waitcnt vmcnt(56)
	v_cndmask_b32_e64 v8, 0, v8, s[4:5]
	s_cselect_b64 s[4:5], -1, 0
	s_and_b64 s[4:5], vcc, s[4:5]
	s_cmp_lt_i32 s85, s76
	s_waitcnt vmcnt(55)
	v_cndmask_b32_e64 v29, 0, v29, s[4:5]
	s_cselect_b64 s[4:5], -1, 0
	s_and_b64 s[4:5], vcc, s[4:5]
	s_cmp_lt_i32 s86, s76
	s_waitcnt vmcnt(54)
	v_cndmask_b32_e64 v28, 0, v28, s[4:5]
	s_cselect_b64 s[4:5], -1, 0
	s_and_b64 s[4:5], vcc, s[4:5]
	s_cmp_lt_i32 s87, s76
	s_waitcnt vmcnt(53)
	v_cndmask_b32_e64 v27, 0, v27, s[4:5]
	s_cselect_b64 s[4:5], -1, 0
	s_and_b64 s[4:5], vcc, s[4:5]
	s_cmp_lt_i32 s88, s76
	s_waitcnt vmcnt(52)
	v_cndmask_b32_e64 v26, 0, v26, s[4:5]
	s_cselect_b64 s[4:5], -1, 0
	s_and_b64 s[4:5], vcc, s[4:5]
	s_cmp_lt_i32 s89, s76
	s_waitcnt vmcnt(51)
	v_cndmask_b32_e64 v25, 0, v25, s[4:5]
	s_cselect_b64 s[4:5], -1, 0
	s_and_b64 s[4:5], vcc, s[4:5]
	s_cmp_lt_i32 s90, s76
	s_waitcnt vmcnt(50)
	v_cndmask_b32_e64 v24, 0, v24, s[4:5]
	s_cselect_b64 s[4:5], -1, 0
	s_and_b64 s[4:5], vcc, s[4:5]
	s_cmp_lt_i32 s92, s76
	s_waitcnt vmcnt(49)
	v_cndmask_b32_e64 v23, 0, v23, s[4:5]
	s_cselect_b64 s[4:5], -1, 0
	s_and_b64 s[4:5], vcc, s[4:5]
	s_cmp_lt_i32 s93, s76
	s_waitcnt vmcnt(48)
	v_cndmask_b32_e64 v22, 0, v22, s[4:5]
	s_cselect_b64 s[4:5], -1, 0
	s_and_b64 s[4:5], vcc, s[4:5]
	s_cmp_lt_i32 s94, s76
	s_waitcnt vmcnt(47)
	v_cndmask_b32_e64 v37, 0, v37, s[4:5]
	s_cselect_b64 s[4:5], -1, 0
	s_and_b64 s[4:5], vcc, s[4:5]
	s_cmp_lt_i32 s95, s76
	s_waitcnt vmcnt(46)
	v_cndmask_b32_e64 v36, 0, v36, s[4:5]
	s_cselect_b64 s[4:5], -1, 0
	s_and_b64 s[4:5], vcc, s[4:5]
	s_cmp_lt_i32 s50, s76
	s_waitcnt vmcnt(45)
	v_cndmask_b32_e64 v35, 0, v35, s[4:5]
	s_cselect_b64 s[4:5], -1, 0
	s_and_b64 s[4:5], vcc, s[4:5]
	s_cmp_lt_i32 s51, s76
	s_waitcnt vmcnt(44)
	v_cndmask_b32_e64 v34, 0, v34, s[4:5]
	s_cselect_b64 s[4:5], -1, 0
	s_and_b64 s[4:5], vcc, s[4:5]
	s_cmp_lt_i32 s52, s76
	s_waitcnt vmcnt(43)
	v_cndmask_b32_e64 v33, 0, v33, s[4:5]
	s_cselect_b64 s[4:5], -1, 0
	s_and_b64 s[4:5], vcc, s[4:5]
	s_cmp_lt_i32 s53, s76
	s_waitcnt vmcnt(42)
	v_cndmask_b32_e64 v32, 0, v32, s[4:5]
	s_cselect_b64 s[4:5], -1, 0
	s_and_b64 s[4:5], vcc, s[4:5]
	s_cmp_lt_i32 s6, s76
	s_waitcnt vmcnt(41)
	v_cndmask_b32_e64 v31, 0, v31, s[4:5]
	s_cselect_b64 s[4:5], -1, 0
	s_and_b64 s[4:5], vcc, s[4:5]
	s_cmp_lt_i32 s7, s76
	s_waitcnt vmcnt(40)
	v_cndmask_b32_e64 v30, 0, v30, s[4:5]
	s_cselect_b64 s[4:5], -1, 0
	s_and_b64 s[4:5], vcc, s[4:5]
	s_cmp_lt_i32 s8, s76
	s_waitcnt vmcnt(39)
	v_cndmask_b32_e64 v45, 0, v45, s[4:5]
	s_cselect_b64 s[4:5], -1, 0
	s_and_b64 s[4:5], vcc, s[4:5]
	s_cmp_lt_i32 s9, s76
	s_waitcnt vmcnt(38)
	v_cndmask_b32_e64 v44, 0, v44, s[4:5]
	s_cselect_b64 s[4:5], -1, 0
	s_and_b64 s[4:5], vcc, s[4:5]
	s_cmp_lt_i32 s10, s76
	s_waitcnt vmcnt(37)
	v_cndmask_b32_e64 v43, 0, v43, s[4:5]
	s_cselect_b64 s[4:5], -1, 0
	s_and_b64 s[4:5], vcc, s[4:5]
	s_cmp_lt_i32 s11, s76
	s_waitcnt vmcnt(36)
	v_cndmask_b32_e64 v42, 0, v42, s[4:5]
	s_cselect_b64 s[4:5], -1, 0
	s_and_b64 s[4:5], vcc, s[4:5]
	s_cmp_lt_i32 s14, s76
	s_waitcnt vmcnt(35)
	v_cndmask_b32_e64 v41, 0, v41, s[4:5]
	s_cselect_b64 s[4:5], -1, 0
	s_and_b64 s[4:5], vcc, s[4:5]
	s_cmp_lt_i32 s15, s76
	s_waitcnt vmcnt(34)
	v_cndmask_b32_e64 v40, 0, v40, s[4:5]
	s_cselect_b64 s[4:5], -1, 0
	s_and_b64 s[4:5], vcc, s[4:5]
	s_cmp_lt_i32 s16, s76
	s_waitcnt vmcnt(33)
	v_cndmask_b32_e64 v39, 0, v39, s[4:5]
	s_cselect_b64 s[4:5], -1, 0
	s_and_b64 s[4:5], vcc, s[4:5]
	s_cmp_lt_i32 s17, s76
	s_waitcnt vmcnt(32)
	v_cndmask_b32_e64 v38, 0, v38, s[4:5]
	s_cselect_b64 s[4:5], -1, 0
	s_and_b64 s[4:5], vcc, s[4:5]
	s_cmp_lt_i32 s12, s76
	s_waitcnt vmcnt(31)
	v_cndmask_b32_e64 v53, 0, v53, s[4:5]
	s_cselect_b64 s[4:5], -1, 0
	s_and_b64 s[4:5], vcc, s[4:5]
	s_cmp_lt_i32 s13, s76
	s_waitcnt vmcnt(30)
	v_cndmask_b32_e64 v52, 0, v52, s[4:5]
	s_cselect_b64 s[4:5], -1, 0
	s_and_b64 s[4:5], vcc, s[4:5]
	s_cmp_lt_i32 s20, s76
	s_waitcnt vmcnt(29)
	v_cndmask_b32_e64 v51, 0, v51, s[4:5]
	s_cselect_b64 s[4:5], -1, 0
	s_and_b64 s[4:5], vcc, s[4:5]
	s_cmp_lt_i32 s21, s76
	s_waitcnt vmcnt(28)
	v_cndmask_b32_e64 v50, 0, v50, s[4:5]
	s_cselect_b64 s[4:5], -1, 0
	s_and_b64 s[4:5], vcc, s[4:5]
	s_cmp_lt_i32 s24, s76
	s_waitcnt vmcnt(27)
	v_cndmask_b32_e64 v49, 0, v49, s[4:5]
	s_cselect_b64 s[4:5], -1, 0
	s_and_b64 s[4:5], vcc, s[4:5]
	s_cmp_lt_i32 s25, s76
	s_waitcnt vmcnt(26)
	v_cndmask_b32_e64 v48, 0, v48, s[4:5]
	s_cselect_b64 s[4:5], -1, 0
	s_and_b64 s[4:5], vcc, s[4:5]
	s_cmp_lt_i32 s26, s76
	s_waitcnt vmcnt(25)
	v_cndmask_b32_e64 v47, 0, v47, s[4:5]
	s_cselect_b64 s[4:5], -1, 0
	s_and_b64 s[4:5], vcc, s[4:5]
	s_cmp_lt_i32 s27, s76
	s_waitcnt vmcnt(24)
; #define LAS __attribute__((address_space(3)))
; #define LDS_WAIT() asm volatile("s_waitcnt lgkmcnt(0)" ::: "memory")
; __device__ __forceinline__ void conv_load(const ConvItem& ci, int lane, float (&v)[64]) {
;     ...
;     for (int i = 0; i < 64; ++i) v[i] = (okc && (ci.k0 + i) < ci.Ksrc) ? v[i] : 0.f;
; }
; __device__ __forceinline__ void conv_store(const ConvItem& ci, LAS float* scr, int lane, const float (&v)[64]) {
;     const int c = lane & 7;
;     f32x4 s0 = {1.f, 1.f, 1.f, 1.f}, s1 = s0;
;     if (ci.ks) { const int kb = ci.k0 + 8 * c < ci.Ksrc - 8 ? ci.k0 + 8 * c : ci.Ksrc - 8; s0 = *(const f32x4*)(ci.ks + kb); s1 = *(const f32x4*)(ci.ks + kb + 4); }
; #pragma unroll
;     for (int i = 0; i < 64; ++i) scr[i * 65 + lane] = v[i];
;     LDS_WAIT(); asm volatile("" ::: "memory");
	v_cndmask_b32_e64 v46, 0, v46, s[4:5]
	s_cselect_b64 s[4:5], -1, 0
	s_and_b64 s[4:5], vcc, s[4:5]
	s_cmp_lt_i32 s18, s76
	s_waitcnt vmcnt(23)
	v_cndmask_b32_e64 v61, 0, v61, s[4:5]
	s_cselect_b64 s[4:5], -1, 0
	s_and_b64 s[4:5], vcc, s[4:5]
	s_cmp_lt_i32 s19, s76
	s_waitcnt vmcnt(22)
	v_cndmask_b32_e64 v60, 0, v60, s[4:5]
	s_cselect_b64 s[4:5], -1, 0
	s_and_b64 s[4:5], vcc, s[4:5]
	s_cmp_lt_i32 s28, s76
	s_waitcnt vmcnt(21)
	v_cndmask_b32_e64 v59, 0, v59, s[4:5]
	s_cselect_b64 s[4:5], -1, 0
	s_and_b64 s[4:5], vcc, s[4:5]
	s_cmp_lt_i32 s29, s76
	s_waitcnt vmcnt(20)
	v_cndmask_b32_e64 v58, 0, v58, s[4:5]
	s_cselect_b64 s[4:5], -1, 0
	s_and_b64 s[4:5], vcc, s[4:5]
	s_cmp_lt_i32 s22, s76
	s_waitcnt vmcnt(19)
	v_cndmask_b32_e64 v57, 0, v57, s[4:5]
	s_cselect_b64 s[4:5], -1, 0
	s_and_b64 s[4:5], vcc, s[4:5]
	s_cmp_lt_i32 s23, s76
	s_waitcnt vmcnt(18)
	v_cndmask_b32_e64 v56, 0, v56, s[4:5]
	s_cselect_b64 s[4:5], -1, 0
	s_and_b64 s[4:5], vcc, s[4:5]
	s_cmp_lt_i32 s30, s76
	s_waitcnt vmcnt(17)
	v_cndmask_b32_e64 v55, 0, v55, s[4:5]
	s_cselect_b64 s[4:5], -1, 0
	s_and_b64 s[4:5], vcc, s[4:5]
	s_cmp_lt_i32 s31, s76
	s_waitcnt vmcnt(16)
	v_cndmask_b32_e64 v54, 0, v54, s[4:5]
	s_cselect_b64 s[4:5], -1, 0
	s_and_b64 s[4:5], vcc, s[4:5]
	s_cmp_lt_i32 s36, s76
	s_waitcnt vmcnt(15)
	v_cndmask_b32_e64 v70, 0, v70, s[4:5]
	s_cselect_b64 s[4:5], -1, 0
	s_and_b64 s[4:5], vcc, s[4:5]
	s_cmp_lt_i32 s37, s76
	s_waitcnt vmcnt(14)
	v_cndmask_b32_e64 v69, 0, v69, s[4:5]
	s_cselect_b64 s[4:5], -1, 0
	s_and_b64 s[4:5], vcc, s[4:5]
	s_cmp_lt_i32 s38, s76
	s_waitcnt vmcnt(13)
	v_cndmask_b32_e64 v68, 0, v68, s[4:5]
	s_cselect_b64 s[4:5], -1, 0
	s_and_b64 s[4:5], vcc, s[4:5]
	s_cmp_lt_i32 s39, s76
	s_waitcnt vmcnt(12)
	v_cndmask_b32_e64 v67, 0, v67, s[4:5]
	s_cselect_b64 s[4:5], -1, 0
	s_and_b64 s[4:5], vcc, s[4:5]
	s_cmp_lt_i32 s34, s76
	s_waitcnt vmcnt(11)
	v_cndmask_b32_e64 v66, 0, v66, s[4:5]
	s_cselect_b64 s[4:5], -1, 0
	s_and_b64 s[4:5], vcc, s[4:5]
	s_cmp_lt_i32 s35, s76
	s_waitcnt vmcnt(10)
	v_cndmask_b32_e64 v64, 0, v64, s[4:5]
	s_cselect_b64 s[4:5], -1, 0
	s_and_b64 s[4:5], vcc, s[4:5]
	s_cmp_lt_i32 s42, s76
	s_waitcnt vmcnt(9)
	v_cndmask_b32_e64 v63, 0, v63, s[4:5]
	s_cselect_b64 s[4:5], -1, 0
	s_and_b64 s[4:5], vcc, s[4:5]
	s_cmp_lt_i32 s43, s76
	s_waitcnt vmcnt(8)
	v_cndmask_b32_e64 v62, 0, v62, s[4:5]
	s_cselect_b64 s[4:5], -1, 0
	s_and_b64 s[4:5], vcc, s[4:5]
	s_cmp_lt_i32 s54, s76
	s_waitcnt vmcnt(7)
	v_cndmask_b32_e64 v65, 0, v65, s[4:5]
	s_cselect_b64 s[4:5], -1, 0
	s_and_b64 s[4:5], vcc, s[4:5]
	s_cmp_lt_i32 s55, s76
	s_waitcnt vmcnt(6)
	v_cndmask_b32_e64 v74, 0, v74, s[4:5]
	s_cselect_b64 s[4:5], -1, 0
	s_and_b64 s[4:5], vcc, s[4:5]
	s_cmp_lt_i32 s46, s76
	ds_write2_b32 v12, v21, v20 offset1:65
	ds_write2_b32 v12, v19, v18 offset0:130 offset1:195
	v_add_u32_e32 v18, 0x400, v12
	s_waitcnt vmcnt(5)
	v_cndmask_b32_e64 v73, 0, v73, s[4:5]
	s_cselect_b64 s[4:5], -1, 0
	ds_write2_b32 v18, v17, v16 offset0:4 offset1:69
	ds_write2_b32 v18, v15, v8 offset0:134 offset1:199
	v_add_u32_e32 v8, 0x800, v12
	s_and_b64 s[4:5], vcc, s[4:5]
	ds_write2_b32 v8, v29, v28 offset0:8 offset1:73
	ds_write2_b32 v8, v27, v26 offset0:138 offset1:203
	v_add_u32_e32 v8, 0xc00, v12
	s_cmp_lt_i32 s47, s76
	ds_write2_b32 v8, v25, v24 offset0:12 offset1:77
	ds_write2_b32 v8, v23, v22 offset0:142 offset1:207
	v_add_u32_e32 v8, 0x1000, v12
	s_waitcnt vmcnt(4)
	v_cndmask_b32_e64 v72, 0, v72, s[4:5]
	s_cselect_b64 s[4:5], -1, 0
	ds_write2_b32 v8, v37, v36 offset0:16 offset1:81
	ds_write2_b32 v8, v35, v34 offset0:146 offset1:211
	v_add_u32_e32 v8, 0x1400, v12
	s_and_b64 s[4:5], vcc, s[4:5]
	ds_write2_b32 v8, v33, v32 offset0:20 offset1:85
	ds_write2_b32 v8, v31, v30 offset0:150 offset1:215
	v_add_u32_e32 v8, 0x1800, v12
	s_cmp_lt_i32 s48, s76
	ds_write2_b32 v8, v45, v44 offset0:24 offset1:89
	ds_write2_b32 v8, v43, v42 offset0:154 offset1:219
	v_add_u32_e32 v8, 0x1c00, v12
	s_waitcnt vmcnt(3)
	v_cndmask_b32_e64 v71, 0, v71, s[4:5]
	s_cselect_b64 s[4:5], -1, 0
	ds_write2_b32 v8, v41, v40 offset0:28 offset1:93
	ds_write2_b32 v8, v39, v38 offset0:158 offset1:223
	v_add_u32_e32 v8, 0x2000, v12
	s_and_b64 s[4:5], vcc, s[4:5]
	ds_write2_b32 v8, v53, v52 offset0:32 offset1:97
	ds_write2_b32 v8, v51, v50 offset0:162 offset1:227
	v_add_u32_e32 v8, 0x2400, v12
	s_cmp_lt_i32 s49, s76
	ds_write2_b32 v8, v49, v48 offset0:36 offset1:101
	ds_write2_b32 v8, v47, v46 offset0:166 offset1:231
	v_add_u32_e32 v8, 0x2800, v12
	s_waitcnt vmcnt(2)
	v_cndmask_b32_e64 v77, 0, v77, s[4:5]
	s_cselect_b64 s[4:5], -1, 0
	ds_write2_b32 v8, v61, v60 offset0:40 offset1:105
	ds_write2_b32 v8, v59, v58 offset0:170 offset1:235
	v_add_u32_e32 v8, 0x2c00, v12
	s_and_b64 s[4:5], vcc, s[4:5]
	ds_write2_b32 v8, v57, v56 offset0:44 offset1:109
	ds_write2_b32 v8, v55, v54 offset0:174 offset1:239
	v_add_u32_e32 v8, 0x3000, v12
	s_cmp_lt_i32 s44, s76
	ds_write2_b32 v8, v70, v69 offset0:48 offset1:113
	ds_write2_b32 v8, v68, v67 offset0:178 offset1:243
	v_add_u32_e32 v8, 0x3400, v12
	s_waitcnt vmcnt(1)
	v_cndmask_b32_e64 v76, 0, v76, s[4:5]
	s_cselect_b64 s[4:5], -1, 0
	ds_write2_b32 v8, v66, v64 offset0:52 offset1:117
	ds_write2_b32 v8, v63, v62 offset0:182 offset1:247
	v_add_u32_e32 v8, 0x3800, v12
	s_and_b64 vcc, vcc, s[4:5]
	ds_write2_b32 v8, v65, v74 offset0:56 offset1:121
	ds_write2_b32 v8, v73, v72 offset0:186 offset1:251
	v_add_u32_e32 v8, 0x3c00, v12
	s_waitcnt vmcnt(0)
	v_cndmask_b32_e32 v75, 0, v75, vcc
	ds_write2_b32 v8, v71, v77 offset0:60 offset1:125
	ds_write2_b32 v8, v76, v75 offset0:190 offset1:255
	s_waitcnt lgkmcnt(0)
	ds_read2_b32 v[16:17], v14 offset1:65
	v_add_u32_e32 v24, s59, v13
	v_mul_lo_u32 v22, s57, v24
	s_ashr_i32 s59, s58, 31
	v_readlane_b32 s76, v254, 31
	s_waitcnt lgkmcnt(0)
; __device__ __forceinline__ unsigned cvt_pk_bf16(float lo, float hi) { unsigned r; asm volatile("v_cvt_pk_bf16_f32 %0, %1, %2" : "=v"(r) : "v"(lo), "v"(hi)); return r; }
; #define LAS __attribute__((address_space(3)))
; #define LDS_WAIT() asm volatile("s_waitcnt lgkmcnt(0)" ::: "memory")
; __device__ __forceinline__ void conv_store(const ConvItem& ci, LAS float* scr, int lane, const float (&v)[64]) {
;     ...
;     LDS_WAIT(); asm volatile("" ::: "memory");
; #pragma unroll
;     for (int j = 0; j < 8; ++j) { const int n = (lane >> 3) + 8 * j; const LAS float* s = scr + (8 * c) * 65 + n;
;         v4u o; o.x = cvt_pk_bf16(s[0 * 65] * s0[0], s[1 * 65] * s0[1]); o.y = cvt_pk_bf16(s[2 * 65] * s0[2], s[3 * 65] * s0[3]); o.z = cvt_pk_bf16(s[4 * 65] * s1[0], s[5 * 65] * s1[1]); o.w = cvt_pk_bf16(s[6 * 65] * s1[2], s[7 * 65] * s1[3]);
;         *(v4u*)(ci.dst + (size_t)(ci.drow0 + n) * ci.ldd + ci.k0 + 8 * c) = o; }
; __global__ void __launch_bounds__(NWAVES * 64, 2) mk_fwd(Args args) {
;     ...
;             for (int it = gw; it < NITEMS; it += NGW) {
	v_mul_f32_e32 v8, v4, v16
	v_mul_f32_e32 v15, v5, v17
	v_cvt_pk_bf16_f32 v16, v8, v15
	ds_read2_b32 v[18:19], v14 offset0:130 offset1:195
	s_add_i32 s3, s3, s33
	s_add_i32 s66, s66, s67
	s_add_i32 s68, s68, s69
	s_add_i32 s70, s70, s71
	s_waitcnt lgkmcnt(0)
	v_mul_f32_e32 v15, v7, v19
	v_mul_f32_e32 v8, v6, v18
	v_cvt_pk_bf16_f32 v17, v8, v15
	v_add_u32_e32 v15, 0x400, v14
	ds_read2_b32 v[18:19], v15 offset0:4 offset1:69
	s_add_i32 s72, s72, s73
	s_add_i32 s74, s74, s75
	v_readlane_b32 s78, v254, 33
	v_readlane_b32 s79, v254, 34
	s_waitcnt lgkmcnt(0)
	v_mul_f32_e32 v8, v0, v18
	v_mul_f32_e32 v18, v1, v19
	v_cvt_pk_bf16_f32 v18, v8, v18
	ds_read2_b32 v[20:21], v15 offset0:134 offset1:199
	v_readlane_b32 s80, v255, 21
	v_readlane_b32 s77, v254, 32
	s_movk_i32 s78, 0x1580
	v_readlane_b32 s82, v255, 23
	s_waitcnt lgkmcnt(0)
	v_mul_f32_e32 v8, v2, v20
	v_mul_f32_e32 v19, v3, v21
	v_cvt_pk_bf16_f32 v19, v8, v19
	v_ashrrev_i32_e32 v8, 31, v24
	v_mul_lo_u32 v8, s56, v8
	v_mad_u64_u32 v[20:21], s[4:5], s56, v24, 0
	v_add3_u32 v21, v21, v8, v22
	ds_read2_b32 v[22:23], v14 offset0:8 offset1:73
	v_lshl_add_u64 v[20:21], v[20:21], 1, s[60:61]
	s_lshl_b64 s[4:5], s[58:59], 1
	v_lshl_add_u64 v[20:21], v[20:21], 0, s[4:5]
	v_lshlrev_b32_e32 v8, 1, v10
	v_lshl_add_u64 v[20:21], v[20:21], 0, v[8:9]
	global_store_dwordx4 v[20:21], v[16:19], off
	s_cmp_lt_i32 s3, s99
	v_readlane_b32 s83, v255, 24
	s_waitcnt lgkmcnt(0)
	v_mul_f32_e32 v16, v4, v22
	v_mul_f32_e32 v17, v5, v23
	v_cvt_pk_bf16_f32 v16, v16, v17
	ds_read2_b32 v[18:19], v14 offset0:138 offset1:203
	s_mov_b32 s79, 0x3f22f983
	s_mov_b32 s85, 0xbfc90fda
	s_brev_b32 s86, 1
	s_movk_i32 s87, 0x1f8
	s_waitcnt lgkmcnt(0)
	v_mul_f32_e32 v17, v6, v18
	v_mul_f32_e32 v18, v7, v19
	v_cvt_pk_bf16_f32 v17, v17, v18
	ds_read2_b32 v[18:19], v15 offset0:12 offset1:77
	s_mov_b64 s[88:89], 0x80
	s_mov_b64 s[92:93], 0x4000
	s_mov_b64 s[94:95], 0x4800
	v_readlane_b32 s81, v255, 22
	s_waitcnt lgkmcnt(0)
	v_mul_f32_e32 v18, v0, v18
	v_mul_f32_e32 v19, v1, v19
	v_cvt_pk_bf16_f32 v18, v18, v19
	ds_read2_b32 v[20:21], v15 offset0:142 offset1:207
	s_waitcnt lgkmcnt(0)
	v_mul_f32_e32 v19, v2, v20
	v_mul_f32_e32 v20, v3, v21
	v_cvt_pk_bf16_f32 v19, v19, v20
	v_add_u32_e32 v20, 8, v24
	v_ashrrev_i32_e32 v21, 31, v20
	v_mul_lo_u32 v22, s56, v21
	v_mul_lo_u32 v23, s57, v20
	v_mad_u64_u32 v[20:21], s[6:7], s56, v20, 0
	v_add3_u32 v21, v21, v22, v23
	ds_read2_b32 v[22:23], v14 offset0:16 offset1:81
	v_lshl_add_u64 v[20:21], v[20:21], 1, s[60:61]
	v_lshl_add_u64 v[20:21], v[20:21], 0, s[4:5]
	v_lshl_add_u64 v[20:21], v[20:21], 0, v[8:9]
	global_store_dwordx4 v[20:21], v[16:19], off
	s_waitcnt lgkmcnt(0)
	s_nop 0
	v_mul_f32_e32 v16, v4, v22
	v_mul_f32_e32 v17, v5, v23
	v_cvt_pk_bf16_f32 v16, v16, v17
	ds_read2_b32 v[18:19], v14 offset0:146 offset1:211
	s_waitcnt lgkmcnt(0)
	v_mul_f32_e32 v17, v6, v18
	v_mul_f32_e32 v18, v7, v19
	v_cvt_pk_bf16_f32 v17, v17, v18
	ds_read2_b32 v[18:19], v15 offset0:20 offset1:85
	s_waitcnt lgkmcnt(0)
	v_mul_f32_e32 v18, v0, v18
	v_mul_f32_e32 v19, v1, v19
	v_cvt_pk_bf16_f32 v18, v18, v19
	ds_read2_b32 v[20:21], v15 offset0:150 offset1:215
	s_waitcnt lgkmcnt(0)
	v_mul_f32_e32 v19, v2, v20
	v_mul_f32_e32 v20, v3, v21
	v_cvt_pk_bf16_f32 v19, v19, v20
	v_add_u32_e32 v20, 16, v24
	v_ashrrev_i32_e32 v21, 31, v20
	v_mul_lo_u32 v22, s56, v21
	v_mul_lo_u32 v23, s57, v20
	v_mad_u64_u32 v[20:21], s[6:7], s56, v20, 0
	v_add3_u32 v21, v21, v22, v23
	ds_read2_b32 v[22:23], v14 offset0:24 offset1:89
	v_lshl_add_u64 v[20:21], v[20:21], 1, s[60:61]
	v_lshl_add_u64 v[20:21], v[20:21], 0, s[4:5]
	v_lshl_add_u64 v[20:21], v[20:21], 0, v[8:9]
	global_store_dwordx4 v[20:21], v[16:19], off
	s_waitcnt lgkmcnt(0)
	s_nop 0
	v_mul_f32_e32 v16, v4, v22
	v_mul_f32_e32 v17, v5, v23
	v_cvt_pk_bf16_f32 v16, v16, v17
	ds_read2_b32 v[18:19], v14 offset0:154 offset1:219
	s_waitcnt lgkmcnt(0)
	v_mul_f32_e32 v17, v6, v18
	v_mul_f32_e32 v18, v7, v19
	v_cvt_pk_bf16_f32 v17, v17, v18
	ds_read2_b32 v[18:19], v15 offset0:28 offset1:93
	s_waitcnt lgkmcnt(0)
	v_mul_f32_e32 v18, v0, v18
	v_mul_f32_e32 v19, v1, v19
	v_cvt_pk_bf16_f32 v18, v18, v19
	ds_read2_b32 v[20:21], v15 offset0:158 offset1:223
	s_waitcnt lgkmcnt(0)
; __device__ __forceinline__ unsigned cvt_pk_bf16(float lo, float hi) { unsigned r; asm volatile("v_cvt_pk_bf16_f32 %0, %1, %2" : "=v"(r) : "v"(lo), "v"(hi)); return r; }
; #define LAS __attribute__((address_space(3)))
; #define LDS_WAIT() asm volatile("s_waitcnt lgkmcnt(0)" ::: "memory")
; __device__ __forceinline__ void conv_store(const ConvItem& ci, LAS float* scr, int lane, const float (&v)[64]) {
;     ...
;     for (int j = 0; j < 8; ++j) { const int n = (lane >> 3) + 8 * j; const LAS float* s = scr + (8 * c) * 65 + n;
;         v4u o; o.x = cvt_pk_bf16(s[0 * 65] * s0[0], s[1 * 65] * s0[1]); o.y = cvt_pk_bf16(s[2 * 65] * s0[2], s[3 * 65] * s0[3]); o.z = cvt_pk_bf16(s[4 * 65] * s1[0], s[5 * 65] * s1[1]); o.w = cvt_pk_bf16(s[6 * 65] * s1[2], s[7 * 65] * s1[3]);
;         *(v4u*)(ci.dst + (size_t)(ci.drow0 + n) * ci.ldd + ci.k0 + 8 * c) = o; }
;     LDS_WAIT(); asm volatile("" ::: "memory");
; }
	v_mul_f32_e32 v19, v2, v20
	v_mul_f32_e32 v20, v3, v21
	v_cvt_pk_bf16_f32 v19, v19, v20
	v_add_u32_e32 v20, 24, v24
	v_ashrrev_i32_e32 v21, 31, v20
	v_mul_lo_u32 v22, s56, v21
	v_mul_lo_u32 v23, s57, v20
	v_mad_u64_u32 v[20:21], s[6:7], s56, v20, 0
	v_add3_u32 v21, v21, v22, v23
	ds_read2_b32 v[22:23], v14 offset0:32 offset1:97
	v_lshl_add_u64 v[20:21], v[20:21], 1, s[60:61]
	v_lshl_add_u64 v[20:21], v[20:21], 0, s[4:5]
	v_lshl_add_u64 v[20:21], v[20:21], 0, v[8:9]
	global_store_dwordx4 v[20:21], v[16:19], off
	s_waitcnt lgkmcnt(0)
	s_nop 0
	v_mul_f32_e32 v16, v4, v22
	v_mul_f32_e32 v17, v5, v23
	v_cvt_pk_bf16_f32 v16, v16, v17
	ds_read2_b32 v[18:19], v14 offset0:162 offset1:227
	s_waitcnt lgkmcnt(0)
	v_mul_f32_e32 v17, v6, v18
	v_mul_f32_e32 v18, v7, v19
	v_cvt_pk_bf16_f32 v17, v17, v18
	ds_read2_b32 v[18:19], v15 offset0:36 offset1:101
	s_waitcnt lgkmcnt(0)
	v_mul_f32_e32 v18, v0, v18
	v_mul_f32_e32 v19, v1, v19
	v_cvt_pk_bf16_f32 v18, v18, v19
	ds_read2_b32 v[20:21], v15 offset0:166 offset1:231
	s_waitcnt lgkmcnt(0)
	v_mul_f32_e32 v19, v2, v20
	v_mul_f32_e32 v20, v3, v21
	v_cvt_pk_bf16_f32 v19, v19, v20
	v_add_u32_e32 v20, 32, v24
	v_ashrrev_i32_e32 v21, 31, v20
	v_mul_lo_u32 v22, s56, v21
	v_mul_lo_u32 v23, s57, v20
	v_mad_u64_u32 v[20:21], s[6:7], s56, v20, 0
	v_add3_u32 v21, v21, v22, v23
	ds_read2_b32 v[22:23], v14 offset0:40 offset1:105
	v_lshl_add_u64 v[20:21], v[20:21], 1, s[60:61]
	v_lshl_add_u64 v[20:21], v[20:21], 0, s[4:5]
	v_lshl_add_u64 v[20:21], v[20:21], 0, v[8:9]
	global_store_dwordx4 v[20:21], v[16:19], off
	s_waitcnt lgkmcnt(0)
	s_nop 0
	v_mul_f32_e32 v16, v4, v22
	v_mul_f32_e32 v17, v5, v23
	v_cvt_pk_bf16_f32 v16, v16, v17
	ds_read2_b32 v[18:19], v14 offset0:170 offset1:235
	s_waitcnt lgkmcnt(0)
	v_mul_f32_e32 v17, v6, v18
	v_mul_f32_e32 v18, v7, v19
	v_cvt_pk_bf16_f32 v17, v17, v18
	ds_read2_b32 v[18:19], v15 offset0:44 offset1:109
	s_waitcnt lgkmcnt(0)
	v_mul_f32_e32 v18, v0, v18
	v_mul_f32_e32 v19, v1, v19
	v_cvt_pk_bf16_f32 v18, v18, v19
	ds_read2_b32 v[20:21], v15 offset0:174 offset1:239
	s_waitcnt lgkmcnt(0)
	v_mul_f32_e32 v19, v2, v20
	v_mul_f32_e32 v20, v3, v21
	v_cvt_pk_bf16_f32 v19, v19, v20
	v_add_u32_e32 v20, 40, v24
	v_ashrrev_i32_e32 v21, 31, v20
	v_mul_lo_u32 v22, s56, v21
	v_mul_lo_u32 v23, s57, v20
	v_mad_u64_u32 v[20:21], s[6:7], s56, v20, 0
	v_add3_u32 v21, v21, v22, v23
	ds_read2_b32 v[22:23], v14 offset0:48 offset1:113
	v_lshl_add_u64 v[20:21], v[20:21], 1, s[60:61]
	v_lshl_add_u64 v[20:21], v[20:21], 0, s[4:5]
	v_lshl_add_u64 v[20:21], v[20:21], 0, v[8:9]
	global_store_dwordx4 v[20:21], v[16:19], off
	s_waitcnt lgkmcnt(0)
	s_nop 0
	v_mul_f32_e32 v16, v4, v22
	v_mul_f32_e32 v17, v5, v23
	v_cvt_pk_bf16_f32 v16, v16, v17
	ds_read2_b32 v[18:19], v14 offset0:178 offset1:243
	s_waitcnt lgkmcnt(0)
	v_mul_f32_e32 v17, v6, v18
	v_mul_f32_e32 v18, v7, v19
	v_cvt_pk_bf16_f32 v17, v17, v18
	ds_read2_b32 v[18:19], v15 offset0:52 offset1:117
	s_waitcnt lgkmcnt(0)
	v_mul_f32_e32 v18, v0, v18
	v_mul_f32_e32 v19, v1, v19
	v_cvt_pk_bf16_f32 v18, v18, v19
	ds_read2_b32 v[20:21], v15 offset0:182 offset1:247
	s_waitcnt lgkmcnt(0)
	v_mul_f32_e32 v19, v2, v20
	v_mul_f32_e32 v20, v3, v21
	v_cvt_pk_bf16_f32 v19, v19, v20
	v_add_u32_e32 v20, 48, v24
	v_ashrrev_i32_e32 v21, 31, v20
	v_mul_lo_u32 v22, s56, v21
	v_mul_lo_u32 v23, s57, v20
	v_mad_u64_u32 v[20:21], s[6:7], s56, v20, 0
	v_add3_u32 v21, v21, v22, v23
	ds_read2_b32 v[22:23], v14 offset0:56 offset1:121
	v_lshl_add_u64 v[20:21], v[20:21], 1, s[60:61]
	v_lshl_add_u64 v[20:21], v[20:21], 0, s[4:5]
	v_lshl_add_u64 v[20:21], v[20:21], 0, v[8:9]
	global_store_dwordx4 v[20:21], v[16:19], off
	s_waitcnt lgkmcnt(0)
	v_mul_f32_e32 v4, v4, v22
	v_mul_f32_e32 v5, v5, v23
	v_cvt_pk_bf16_f32 v4, v4, v5
	ds_read2_b32 v[16:17], v14 offset0:186 offset1:251
	s_waitcnt lgkmcnt(0)
	v_mul_f32_e32 v5, v6, v16
	v_mul_f32_e32 v6, v7, v17
	v_cvt_pk_bf16_f32 v5, v5, v6
	ds_read2_b32 v[6:7], v15 offset0:60 offset1:125
	s_waitcnt lgkmcnt(0)
	v_mul_f32_e32 v0, v0, v6
	v_mul_f32_e32 v1, v1, v7
	v_cvt_pk_bf16_f32 v6, v0, v1
	ds_read2_b32 v[0:1], v15 offset0:190 offset1:255
	s_waitcnt lgkmcnt(0)
	v_mul_f32_e32 v0, v2, v0
	v_mul_f32_e32 v1, v3, v1
	v_cvt_pk_bf16_f32 v7, v0, v1
	v_add_u32_e32 v0, 56, v24
	v_ashrrev_i32_e32 v1, 31, v0
	v_mul_lo_u32 v2, s56, v1
	v_mul_lo_u32 v3, s57, v0
	v_mad_u64_u32 v[0:1], s[6:7], s56, v0, 0
	v_add3_u32 v1, v1, v2, v3
	v_lshl_add_u64 v[0:1], v[0:1], 1, s[60:61]
	v_lshl_add_u64 v[0:1], v[0:1], 0, s[4:5]
	v_lshl_add_u64 v[0:1], v[0:1], 0, v[8:9]
	global_store_dwordx4 v[0:1], v[4:7], off
	s_waitcnt lgkmcnt(0)
	s_cbranch_scc0 .Lmy_p0_second

; #define LAS __attribute__((address_space(3)))
; #define IN(k) in_range(lo, hi, (k))
; __global__ void __launch_bounds__(NWAVES * 64, 2) mk_fwd(Args args) {
;     ...
;         if (EN(0) && IN(pb + 0)) {
;             PH_LOCALS
;             LAS float* scr = (LAS float*)(lds + RING_OFF + wave * 16640);   static_assert(8 * 16640 <= LDSCTL_OFF, "converter scratch below the LDS control words");
;             constexpr int I_UP = (D / 64) * (NUP / 64), I_DN = (DFF / 64) * (D / 64), I_IN = (D / 64) * (DINP / 64), I_GLU = 16 * 16, I_L = 4 * 16, I_V1 = 16 * 4, I_V2 = 4 * 16,
;                           I_BS5 = 16 * 32, I_BAT = 8 * 32, I_BRW = 16 * 32, I_OUT = 32 * 32;
;             constexpr int NITEMS = 2 * I_UP + 2 * I_DN + I_IN + I_GLU + 3 * I_L + I_V1 + I_V2 + I_BS5 + I_BAT + I_BRW + I_OUT;
;             const int lv = l > 0 ? l - 1 : 0;
;     ...
;             for (int it = gw; it < NITEMS; it += NGW) {
;                 ConvItem ca; CONV_DESC(ca, it);
;                 float va[64];
;                 conv_load(ca, lane, va);
;                 conv_store(ca, scr, lane, va);
;             }
.Lmy_p0_second:
	v_readlane_b32 s98, v254, 38
	s_nop 3
	s_cmp_lt_u32 s98, 1
	s_cbranch_scc1 .LBB0_92
	v_readlane_b32 s0, v254, 8
	v_readlane_b32 s4, v254, 10
	v_readlane_b32 s1, v254, 9
	v_mbcnt_lo_u32_b32 v11, -1, 0
	v_mbcnt_hi_u32_b32 v11, -1, v11
	s_load_dword s6, s[0:1], 0x0
	s_mov_b32 s3, s84
	s_waitcnt lgkmcnt(0)
	s_movk_i32 s6, 256
	s_lshl_b32 s3, s3, 3
	v_readlane_b32 s0, v254, 0
	s_add_i32 s3, s3, s4
	s_add_i32 s3, s3, 0x53c0
	v_readlane_b32 s1, v254, 1
	s_cmpk_gt_i32 s3, 27071
	s_cbranch_scc1 .Lcvp0b_ret
	s_load_dwordx2 s[8:9], s[0:1], 0x138
	v_readlane_b32 s14, v254, 38
	s_mulk_i32 s4, 0x4100
	s_add_i32 s7, s4, 0
	v_sub_u32_e64 v0, s14, 1 clamp
	s_lshl_b32 s33, s6, 3
	v_readfirstlane_b32 s4, v0
	s_lshl_b32 s96, s4, 16
	s_waitcnt lgkmcnt(0)
	s_add_u32 s4, s8, 0x22800000
	s_addc_u32 s5, s9, 0
	v_writelane_b32 v254, s4, 39
	s_mov_b32 s15, s97
	v_and_b32_e32 v0, 7, v11
	v_writelane_b32 v254, s5, 40
	s_add_u32 s4, s8, 0x22780000
	s_addc_u32 s5, s9, 0
	v_writelane_b32 v254, s4, 41
	v_ashrrev_i32_e32 v13, 3, v11
	v_lshlrev_b32_e32 v10, 3, v0
	v_writelane_b32 v254, s5, 42
	s_lshl_b32 s4, s14, 18
	s_add_u32 s10, s8, 0x22700000
	s_addc_u32 s11, s9, 0
	v_writelane_b32 v254, s10, 43
	s_mov_b32 s5, s97
	v_mul_u32_u24_e32 v0, 0x820, v0
	v_writelane_b32 v254, s11, 44
	s_mul_i32 s10, s14, 0x18000
	s_mov_b32 s11, s97
	v_writelane_b32 v254, s10, 45
	v_lshlrev_b32_e32 v1, 2, v13
	v_lshl_add_u32 v12, v11, 2, s7
	v_writelane_b32 v254, s11, 46
	s_add_u32 s10, s8, 0x22680000
	s_addc_u32 s11, s9, 0
	v_writelane_b32 v254, s10, 47
	v_add3_u32 v14, s7, v0, v1
	s_mov_b32 s41, s97
	v_writelane_b32 v254, s11, 48
	s_add_u32 s10, s8, 0x22600000
	s_addc_u32 s11, s9, 0
	v_writelane_b32 v254, s10, 49
	s_nop 1
	v_writelane_b32 v254, s11, 50
	s_lshl_b32 s10, s14, 20
	s_mov_b32 s11, s97
	v_writelane_b32 v254, s10, 51
	s_nop 1
	v_writelane_b32 v254, s11, 52
	s_add_u32 s10, s8, 0x22400000
	s_addc_u32 s11, s9, 0
	v_writelane_b32 v254, s10, 53
	s_nop 1
	v_writelane_b32 v254, s11, 54
	s_lshl_b32 s10, s14, 21
	s_mov_b32 s11, s97
	v_writelane_b32 v254, s10, 55
	s_nop 1
	v_writelane_b32 v254, s11, 56
	s_add_u32 s10, s8, 0x22e80000
	s_addc_u32 s11, s9, 0
	v_writelane_b32 v254, s10, 57
	s_nop 1
	v_writelane_b32 v254, s11, 58
	s_add_u32 s10, s8, 0x27b80000
	s_addc_u32 s11, s9, 0
	v_writelane_b32 v254, s10, 59
	s_nop 1
	v_writelane_b32 v254, s11, 60
	s_add_u32 s10, s8, 0x22880000
	s_addc_u32 s11, s9, 0
	v_writelane_b32 v254, s10, 61
	s_nop 1
	v_writelane_b32 v254, s11, 62
	s_lshl_b32 s10, s14, 22
	s_add_u32 s12, s8, 0x23280000
	s_addc_u32 s13, s9, 0
	v_writelane_b32 v254, s12, 63
	s_mov_b32 s11, s97
	s_nop 0
	v_writelane_b32 v255, s13, 0
	s_mul_i32 s12, s14, 0xac0000
	s_mov_b32 s13, s97
	v_writelane_b32 v255, s12, 1
	s_nop 1
	v_writelane_b32 v255, s13, 2
	s_add_u32 s12, s8, 0x26580000
	s_addc_u32 s13, s9, 0
	v_writelane_b32 v255, s12, 3
	s_nop 1
	v_writelane_b32 v255, s13, 4
	s_add_u32 s12, s8, 0x1d200000
	s_addc_u32 s13, s9, 0
	s_lshl_b32 s40, s14, 11
	v_writelane_b32 v255, s12, 5
	s_add_u32 s16, s8, 0x1e800000
	s_addc_u32 s17, s9, 0
	v_writelane_b32 v255, s13, 6
	v_writelane_b32 v255, s16, 7
	s_mul_i32 s12, s14, 0x1de0000
	s_mul_i32 s14, s14, 0x1580000
	v_writelane_b32 v255, s17, 8
	v_writelane_b32 v255, s14, 9
	s_mov_b32 s13, s97
	s_nop 0
	v_writelane_b32 v255, s15, 10
	s_add_u32 s14, s8, 0x23a80000
	s_addc_u32 s15, s9, 0
	v_writelane_b32 v255, s14, 11
	s_add_u32 s8, s8, 0x1a700000
	s_addc_u32 s9, s9, 0
	v_writelane_b32 v255, s15, 12
	v_writelane_b32 v255, s8, 13
	s_lshl_b64 s[4:5], s[4:5], 2
	s_lshl_b32 s7, s3, 4
	v_writelane_b32 v255, s9, 14
	v_writelane_b32 v255, s4, 15
	s_add_i32 s72, s7, 0xc00
	s_lshl_b32 s7, s3, 1
	v_writelane_b32 v255, s5, 16
	s_lshl_b64 s[4:5], s[10:11], 2
	v_writelane_b32 v255, s4, 17
	s_lshl_b32 s66, s3, 6
	s_lshl_b32 s67, s6, 9
	v_writelane_b32 v255, s5, 18
	s_lshl_b64 s[4:5], s[12:13], 2
	v_writelane_b32 v255, s4, 19
	s_lshl_b32 s68, s3, 5
	s_lshl_b32 s69, s6, 8
	v_writelane_b32 v255, s5, 20
	v_writelane_b32 v255, s80, 21
	s_lshl_b32 s70, s3, 2
	s_lshl_b32 s71, s6, 5
	v_writelane_b32 v255, s81, 22
	v_writelane_b32 v255, s82, 23
	s_lshl_b32 s73, s6, 7
	s_add_i32 s74, s7, 0x13500
	s_lshl_b32 s75, s6, 4
	v_writelane_b32 v255, s83, 24
	s_branch .Lcvp0b_31

; __device__ __forceinline__ void conv_load(const ConvItem& ci, int lane, float (&v)[64]) {
;     ...
;     for (int i = 0; i < 64; ++i) { const int k = ci.k0 + i, kk = k < kmax ? k : kmax; v[i] = __builtin_nontemporal_load(base + (size_t)kk * ci.ldw); }
; #pragma unroll
;     for (int i = 0; i < 64; ++i) v[i] = (okc && (ci.k0 + i) < ci.Ksrc) ? v[i] : 0.f;
.Lcvp0b_30:
	s_cmp_lt_i32 s58, s76
	s_cselect_b64 s[4:5], -1, 0
	s_and_b64 s[4:5], vcc, s[4:5]
	s_cmp_lt_i32 s64, s76
	s_waitcnt vmcnt(62)
	v_cndmask_b32_e64 v21, 0, v21, s[4:5]
	s_cselect_b64 s[4:5], -1, 0
	s_and_b64 s[4:5], vcc, s[4:5]
	s_cmp_lt_i32 s65, s76
	v_cndmask_b32_e64 v20, 0, v20, s[4:5]
	s_cselect_b64 s[4:5], -1, 0
	s_and_b64 s[4:5], vcc, s[4:5]
	s_cmp_lt_i32 s78, s76
	s_waitcnt vmcnt(61)
	v_cndmask_b32_e64 v19, 0, v19, s[4:5]
	s_cselect_b64 s[4:5], -1, 0
	s_and_b64 s[4:5], vcc, s[4:5]
	s_cmp_lt_i32 s79, s76
	s_waitcnt vmcnt(60)
	v_cndmask_b32_e64 v18, 0, v18, s[4:5]
	s_cselect_b64 s[4:5], -1, 0
	s_and_b64 s[4:5], vcc, s[4:5]
	s_cmp_lt_i32 s80, s76
	s_waitcnt vmcnt(59)
	v_cndmask_b32_e64 v17, 0, v17, s[4:5]
	s_cselect_b64 s[4:5], -1, 0
	s_and_b64 s[4:5], vcc, s[4:5]
	s_cmp_lt_i32 s81, s76
	s_waitcnt vmcnt(58)
	v_cndmask_b32_e64 v16, 0, v16, s[4:5]
	s_cselect_b64 s[4:5], -1, 0
	s_and_b64 s[4:5], vcc, s[4:5]
	s_cmp_lt_i32 s82, s76
	s_waitcnt vmcnt(57)
	v_cndmask_b32_e64 v15, 0, v15, s[4:5]
	s_cselect_b64 s[4:5], -1, 0
	s_and_b64 s[4:5], vcc, s[4:5]
	s_cmp_lt_i32 s83, s76
	s_waitcnt vmcnt(56)
	v_cndmask_b32_e64 v8, 0, v8, s[4:5]
	s_cselect_b64 s[4:5], -1, 0
	s_and_b64 s[4:5], vcc, s[4:5]
	s_cmp_lt_i32 s85, s76
	s_waitcnt vmcnt(55)
	v_cndmask_b32_e64 v29, 0, v29, s[4:5]
	s_cselect_b64 s[4:5], -1, 0
	s_and_b64 s[4:5], vcc, s[4:5]
	s_cmp_lt_i32 s86, s76
	s_waitcnt vmcnt(54)
	v_cndmask_b32_e64 v28, 0, v28, s[4:5]
	s_cselect_b64 s[4:5], -1, 0
	s_and_b64 s[4:5], vcc, s[4:5]
	s_cmp_lt_i32 s87, s76
	s_waitcnt vmcnt(53)
	v_cndmask_b32_e64 v27, 0, v27, s[4:5]
	s_cselect_b64 s[4:5], -1, 0
	s_and_b64 s[4:5], vcc, s[4:5]
	s_cmp_lt_i32 s88, s76
	s_waitcnt vmcnt(52)
	v_cndmask_b32_e64 v26, 0, v26, s[4:5]
	s_cselect_b64 s[4:5], -1, 0
	s_and_b64 s[4:5], vcc, s[4:5]
	s_cmp_lt_i32 s89, s76
	s_waitcnt vmcnt(51)
	v_cndmask_b32_e64 v25, 0, v25, s[4:5]
	s_cselect_b64 s[4:5], -1, 0
	s_and_b64 s[4:5], vcc, s[4:5]
	s_cmp_lt_i32 s90, s76
	s_waitcnt vmcnt(50)
	v_cndmask_b32_e64 v24, 0, v24, s[4:5]
	s_cselect_b64 s[4:5], -1, 0
	s_and_b64 s[4:5], vcc, s[4:5]
	s_cmp_lt_i32 s92, s76
	s_waitcnt vmcnt(49)
	v_cndmask_b32_e64 v23, 0, v23, s[4:5]
	s_cselect_b64 s[4:5], -1, 0
	s_and_b64 s[4:5], vcc, s[4:5]
	s_cmp_lt_i32 s93, s76
	s_waitcnt vmcnt(48)
	v_cndmask_b32_e64 v22, 0, v22, s[4:5]
	s_cselect_b64 s[4:5], -1, 0
	s_and_b64 s[4:5], vcc, s[4:5]
	s_cmp_lt_i32 s94, s76
	s_waitcnt vmcnt(47)
	v_cndmask_b32_e64 v37, 0, v37, s[4:5]
	s_cselect_b64 s[4:5], -1, 0
	s_and_b64 s[4:5], vcc, s[4:5]
	s_cmp_lt_i32 s95, s76
	s_waitcnt vmcnt(46)
	v_cndmask_b32_e64 v36, 0, v36, s[4:5]
	s_cselect_b64 s[4:5], -1, 0
	s_and_b64 s[4:5], vcc, s[4:5]
	s_cmp_lt_i32 s50, s76
	s_waitcnt vmcnt(45)
	v_cndmask_b32_e64 v35, 0, v35, s[4:5]
	s_cselect_b64 s[4:5], -1, 0
	s_and_b64 s[4:5], vcc, s[4:5]
	s_cmp_lt_i32 s51, s76
	s_waitcnt vmcnt(44)
	v_cndmask_b32_e64 v34, 0, v34, s[4:5]
	s_cselect_b64 s[4:5], -1, 0
	s_and_b64 s[4:5], vcc, s[4:5]
	s_cmp_lt_i32 s52, s76
	s_waitcnt vmcnt(43)
	v_cndmask_b32_e64 v33, 0, v33, s[4:5]
	s_cselect_b64 s[4:5], -1, 0
	s_and_b64 s[4:5], vcc, s[4:5]
	s_cmp_lt_i32 s53, s76
	s_waitcnt vmcnt(42)
	v_cndmask_b32_e64 v32, 0, v32, s[4:5]
	s_cselect_b64 s[4:5], -1, 0
	s_and_b64 s[4:5], vcc, s[4:5]
	s_cmp_lt_i32 s6, s76
	s_waitcnt vmcnt(41)
	v_cndmask_b32_e64 v31, 0, v31, s[4:5]
	s_cselect_b64 s[4:5], -1, 0
	s_and_b64 s[4:5], vcc, s[4:5]
	s_cmp_lt_i32 s7, s76
	s_waitcnt vmcnt(40)
	v_cndmask_b32_e64 v30, 0, v30, s[4:5]
	s_cselect_b64 s[4:5], -1, 0
	s_and_b64 s[4:5], vcc, s[4:5]
	s_cmp_lt_i32 s8, s76
	s_waitcnt vmcnt(39)
	v_cndmask_b32_e64 v45, 0, v45, s[4:5]
	s_cselect_b64 s[4:5], -1, 0
	s_and_b64 s[4:5], vcc, s[4:5]
	s_cmp_lt_i32 s9, s76
	s_waitcnt vmcnt(38)
	v_cndmask_b32_e64 v44, 0, v44, s[4:5]
	s_cselect_b64 s[4:5], -1, 0
	s_and_b64 s[4:5], vcc, s[4:5]
	s_cmp_lt_i32 s10, s76
	s_waitcnt vmcnt(37)
	v_cndmask_b32_e64 v43, 0, v43, s[4:5]
	s_cselect_b64 s[4:5], -1, 0
	s_and_b64 s[4:5], vcc, s[4:5]
	s_cmp_lt_i32 s11, s76
	s_waitcnt vmcnt(36)
	v_cndmask_b32_e64 v42, 0, v42, s[4:5]
	s_cselect_b64 s[4:5], -1, 0
	s_and_b64 s[4:5], vcc, s[4:5]
	s_cmp_lt_i32 s14, s76
	s_waitcnt vmcnt(35)
	v_cndmask_b32_e64 v41, 0, v41, s[4:5]
	s_cselect_b64 s[4:5], -1, 0
	s_and_b64 s[4:5], vcc, s[4:5]
	s_cmp_lt_i32 s15, s76
	s_waitcnt vmcnt(34)
	v_cndmask_b32_e64 v40, 0, v40, s[4:5]
	s_cselect_b64 s[4:5], -1, 0
	s_and_b64 s[4:5], vcc, s[4:5]
	s_cmp_lt_i32 s16, s76
	s_waitcnt vmcnt(33)
	v_cndmask_b32_e64 v39, 0, v39, s[4:5]
	s_cselect_b64 s[4:5], -1, 0
	s_and_b64 s[4:5], vcc, s[4:5]
	s_cmp_lt_i32 s17, s76
	s_waitcnt vmcnt(32)
	v_cndmask_b32_e64 v38, 0, v38, s[4:5]
	s_cselect_b64 s[4:5], -1, 0
	s_and_b64 s[4:5], vcc, s[4:5]
	s_cmp_lt_i32 s12, s76
	s_waitcnt vmcnt(31)
	v_cndmask_b32_e64 v53, 0, v53, s[4:5]
	s_cselect_b64 s[4:5], -1, 0
	s_and_b64 s[4:5], vcc, s[4:5]
	s_cmp_lt_i32 s13, s76
	s_waitcnt vmcnt(30)
	v_cndmask_b32_e64 v52, 0, v52, s[4:5]
	s_cselect_b64 s[4:5], -1, 0
	s_and_b64 s[4:5], vcc, s[4:5]
	s_cmp_lt_i32 s20, s76
	s_waitcnt vmcnt(29)
	v_cndmask_b32_e64 v51, 0, v51, s[4:5]
	s_cselect_b64 s[4:5], -1, 0
	s_and_b64 s[4:5], vcc, s[4:5]
	s_cmp_lt_i32 s21, s76
	s_waitcnt vmcnt(28)
	v_cndmask_b32_e64 v50, 0, v50, s[4:5]
	s_cselect_b64 s[4:5], -1, 0
	s_and_b64 s[4:5], vcc, s[4:5]
	s_cmp_lt_i32 s24, s76
	s_waitcnt vmcnt(27)
	v_cndmask_b32_e64 v49, 0, v49, s[4:5]
	s_cselect_b64 s[4:5], -1, 0
	s_and_b64 s[4:5], vcc, s[4:5]
	s_cmp_lt_i32 s25, s76
	s_waitcnt vmcnt(26)
	v_cndmask_b32_e64 v48, 0, v48, s[4:5]
	s_cselect_b64 s[4:5], -1, 0
	s_and_b64 s[4:5], vcc, s[4:5]
	s_cmp_lt_i32 s26, s76
	s_waitcnt vmcnt(25)
	v_cndmask_b32_e64 v47, 0, v47, s[4:5]
	s_cselect_b64 s[4:5], -1, 0
	s_and_b64 s[4:5], vcc, s[4:5]
	s_cmp_lt_i32 s27, s76
	s_waitcnt vmcnt(24)
; #define LAS __attribute__((address_space(3)))
; #define LDS_WAIT() asm volatile("s_waitcnt lgkmcnt(0)" ::: "memory")
; __device__ __forceinline__ void conv_load(const ConvItem& ci, int lane, float (&v)[64]) {
;     ...
;     for (int i = 0; i < 64; ++i) v[i] = (okc && (ci.k0 + i) < ci.Ksrc) ? v[i] : 0.f;
; }
; __device__ __forceinline__ void conv_store(const ConvItem& ci, LAS float* scr, int lane, const float (&v)[64]) {
;     const int c = lane & 7;
;     f32x4 s0 = {1.f, 1.f, 1.f, 1.f}, s1 = s0;
;     if (ci.ks) { const int kb = ci.k0 + 8 * c < ci.Ksrc - 8 ? ci.k0 + 8 * c : ci.Ksrc - 8; s0 = *(const f32x4*)(ci.ks + kb); s1 = *(const f32x4*)(ci.ks + kb + 4); }
; #pragma unroll
;     for (int i = 0; i < 64; ++i) scr[i * 65 + lane] = v[i];
;     LDS_WAIT(); asm volatile("" ::: "memory");
	v_cndmask_b32_e64 v46, 0, v46, s[4:5]
	s_cselect_b64 s[4:5], -1, 0
	s_and_b64 s[4:5], vcc, s[4:5]
	s_cmp_lt_i32 s18, s76
	s_waitcnt vmcnt(23)
	v_cndmask_b32_e64 v61, 0, v61, s[4:5]
	s_cselect_b64 s[4:5], -1, 0
	s_and_b64 s[4:5], vcc, s[4:5]
	s_cmp_lt_i32 s19, s76
	s_waitcnt vmcnt(22)
	v_cndmask_b32_e64 v60, 0, v60, s[4:5]
	s_cselect_b64 s[4:5], -1, 0
	s_and_b64 s[4:5], vcc, s[4:5]
	s_cmp_lt_i32 s28, s76
	s_waitcnt vmcnt(21)
	v_cndmask_b32_e64 v59, 0, v59, s[4:5]
	s_cselect_b64 s[4:5], -1, 0
	s_and_b64 s[4:5], vcc, s[4:5]
	s_cmp_lt_i32 s29, s76
	s_waitcnt vmcnt(20)
	v_cndmask_b32_e64 v58, 0, v58, s[4:5]
	s_cselect_b64 s[4:5], -1, 0
	s_and_b64 s[4:5], vcc, s[4:5]
	s_cmp_lt_i32 s22, s76
	s_waitcnt vmcnt(19)
	v_cndmask_b32_e64 v57, 0, v57, s[4:5]
	s_cselect_b64 s[4:5], -1, 0
	s_and_b64 s[4:5], vcc, s[4:5]
	s_cmp_lt_i32 s23, s76
	s_waitcnt vmcnt(18)
	v_cndmask_b32_e64 v56, 0, v56, s[4:5]
	s_cselect_b64 s[4:5], -1, 0
	s_and_b64 s[4:5], vcc, s[4:5]
	s_cmp_lt_i32 s30, s76
	s_waitcnt vmcnt(17)
	v_cndmask_b32_e64 v55, 0, v55, s[4:5]
	s_cselect_b64 s[4:5], -1, 0
	s_and_b64 s[4:5], vcc, s[4:5]
	s_cmp_lt_i32 s31, s76
	s_waitcnt vmcnt(16)
	v_cndmask_b32_e64 v54, 0, v54, s[4:5]
	s_cselect_b64 s[4:5], -1, 0
	s_and_b64 s[4:5], vcc, s[4:5]
	s_cmp_lt_i32 s36, s76
	s_waitcnt vmcnt(15)
	v_cndmask_b32_e64 v70, 0, v70, s[4:5]
	s_cselect_b64 s[4:5], -1, 0
	s_and_b64 s[4:5], vcc, s[4:5]
	s_cmp_lt_i32 s37, s76
	s_waitcnt vmcnt(14)
	v_cndmask_b32_e64 v69, 0, v69, s[4:5]
	s_cselect_b64 s[4:5], -1, 0
	s_and_b64 s[4:5], vcc, s[4:5]
	s_cmp_lt_i32 s38, s76
	s_waitcnt vmcnt(13)
	v_cndmask_b32_e64 v68, 0, v68, s[4:5]
	s_cselect_b64 s[4:5], -1, 0
	s_and_b64 s[4:5], vcc, s[4:5]
	s_cmp_lt_i32 s39, s76
	s_waitcnt vmcnt(12)
	v_cndmask_b32_e64 v67, 0, v67, s[4:5]
	s_cselect_b64 s[4:5], -1, 0
	s_and_b64 s[4:5], vcc, s[4:5]
	s_cmp_lt_i32 s34, s76
	s_waitcnt vmcnt(11)
	v_cndmask_b32_e64 v66, 0, v66, s[4:5]
	s_cselect_b64 s[4:5], -1, 0
	s_and_b64 s[4:5], vcc, s[4:5]
	s_cmp_lt_i32 s35, s76
	s_waitcnt vmcnt(10)
	v_cndmask_b32_e64 v64, 0, v64, s[4:5]
	s_cselect_b64 s[4:5], -1, 0
	s_and_b64 s[4:5], vcc, s[4:5]
	s_cmp_lt_i32 s42, s76
	s_waitcnt vmcnt(9)
	v_cndmask_b32_e64 v63, 0, v63, s[4:5]
	s_cselect_b64 s[4:5], -1, 0
	s_and_b64 s[4:5], vcc, s[4:5]
	s_cmp_lt_i32 s43, s76
	s_waitcnt vmcnt(8)
	v_cndmask_b32_e64 v62, 0, v62, s[4:5]
	s_cselect_b64 s[4:5], -1, 0
	s_and_b64 s[4:5], vcc, s[4:5]
	s_cmp_lt_i32 s54, s76
	s_waitcnt vmcnt(7)
	v_cndmask_b32_e64 v65, 0, v65, s[4:5]
	s_cselect_b64 s[4:5], -1, 0
	s_and_b64 s[4:5], vcc, s[4:5]
	s_cmp_lt_i32 s55, s76
	s_waitcnt vmcnt(6)
	v_cndmask_b32_e64 v74, 0, v74, s[4:5]
	s_cselect_b64 s[4:5], -1, 0
	s_and_b64 s[4:5], vcc, s[4:5]
	s_cmp_lt_i32 s46, s76
	ds_write2_b32 v12, v21, v20 offset1:65
	ds_write2_b32 v12, v19, v18 offset0:130 offset1:195
	v_add_u32_e32 v18, 0x400, v12
	s_waitcnt vmcnt(5)
	v_cndmask_b32_e64 v73, 0, v73, s[4:5]
	s_cselect_b64 s[4:5], -1, 0
	ds_write2_b32 v18, v17, v16 offset0:4 offset1:69
	ds_write2_b32 v18, v15, v8 offset0:134 offset1:199
	v_add_u32_e32 v8, 0x800, v12
	s_and_b64 s[4:5], vcc, s[4:5]
	ds_write2_b32 v8, v29, v28 offset0:8 offset1:73
	ds_write2_b32 v8, v27, v26 offset0:138 offset1:203
	v_add_u32_e32 v8, 0xc00, v12
	s_cmp_lt_i32 s47, s76
	ds_write2_b32 v8, v25, v24 offset0:12 offset1:77
	ds_write2_b32 v8, v23, v22 offset0:142 offset1:207
	v_add_u32_e32 v8, 0x1000, v12
	s_waitcnt vmcnt(4)
	v_cndmask_b32_e64 v72, 0, v72, s[4:5]
	s_cselect_b64 s[4:5], -1, 0
	ds_write2_b32 v8, v37, v36 offset0:16 offset1:81
	ds_write2_b32 v8, v35, v34 offset0:146 offset1:211
	v_add_u32_e32 v8, 0x1400, v12
	s_and_b64 s[4:5], vcc, s[4:5]
	ds_write2_b32 v8, v33, v32 offset0:20 offset1:85
	ds_write2_b32 v8, v31, v30 offset0:150 offset1:215
	v_add_u32_e32 v8, 0x1800, v12
	s_cmp_lt_i32 s48, s76
	ds_write2_b32 v8, v45, v44 offset0:24 offset1:89
	ds_write2_b32 v8, v43, v42 offset0:154 offset1:219
	v_add_u32_e32 v8, 0x1c00, v12
	s_waitcnt vmcnt(3)
	v_cndmask_b32_e64 v71, 0, v71, s[4:5]
	s_cselect_b64 s[4:5], -1, 0
	ds_write2_b32 v8, v41, v40 offset0:28 offset1:93
	ds_write2_b32 v8, v39, v38 offset0:158 offset1:223
	v_add_u32_e32 v8, 0x2000, v12
	s_and_b64 s[4:5], vcc, s[4:5]
	ds_write2_b32 v8, v53, v52 offset0:32 offset1:97
	ds_write2_b32 v8, v51, v50 offset0:162 offset1:227
	v_add_u32_e32 v8, 0x2400, v12
	s_cmp_lt_i32 s49, s76
	ds_write2_b32 v8, v49, v48 offset0:36 offset1:101
	ds_write2_b32 v8, v47, v46 offset0:166 offset1:231
	v_add_u32_e32 v8, 0x2800, v12
	s_waitcnt vmcnt(2)
	v_cndmask_b32_e64 v77, 0, v77, s[4:5]
	s_cselect_b64 s[4:5], -1, 0
	ds_write2_b32 v8, v61, v60 offset0:40 offset1:105
	ds_write2_b32 v8, v59, v58 offset0:170 offset1:235
	v_add_u32_e32 v8, 0x2c00, v12
	s_and_b64 s[4:5], vcc, s[4:5]
	ds_write2_b32 v8, v57, v56 offset0:44 offset1:109
	ds_write2_b32 v8, v55, v54 offset0:174 offset1:239
	v_add_u32_e32 v8, 0x3000, v12
	s_cmp_lt_i32 s44, s76
	ds_write2_b32 v8, v70, v69 offset0:48 offset1:113
	ds_write2_b32 v8, v68, v67 offset0:178 offset1:243
	v_add_u32_e32 v8, 0x3400, v12
	s_waitcnt vmcnt(1)
	v_cndmask_b32_e64 v76, 0, v76, s[4:5]
	s_cselect_b64 s[4:5], -1, 0
	ds_write2_b32 v8, v66, v64 offset0:52 offset1:117
	ds_write2_b32 v8, v63, v62 offset0:182 offset1:247
	v_add_u32_e32 v8, 0x3800, v12
	s_and_b64 vcc, vcc, s[4:5]
	ds_write2_b32 v8, v65, v74 offset0:56 offset1:121
	ds_write2_b32 v8, v73, v72 offset0:186 offset1:251
	v_add_u32_e32 v8, 0x3c00, v12
	s_waitcnt vmcnt(0)
	v_cndmask_b32_e32 v75, 0, v75, vcc
	ds_write2_b32 v8, v71, v77 offset0:60 offset1:125
	ds_write2_b32 v8, v76, v75 offset0:190 offset1:255
	s_waitcnt lgkmcnt(0)
	ds_read2_b32 v[16:17], v14 offset1:65
	v_add_u32_e32 v24, s59, v13
	v_mul_lo_u32 v22, s57, v24
	s_ashr_i32 s59, s58, 31
	v_readlane_b32 s76, v254, 31
	s_waitcnt lgkmcnt(0)
; __device__ __forceinline__ unsigned cvt_pk_bf16(float lo, float hi) { unsigned r; asm volatile("v_cvt_pk_bf16_f32 %0, %1, %2" : "=v"(r) : "v"(lo), "v"(hi)); return r; }
; #define LAS __attribute__((address_space(3)))
; #define LDS_WAIT() asm volatile("s_waitcnt lgkmcnt(0)" ::: "memory")
; __device__ __forceinline__ void conv_store(const ConvItem& ci, LAS float* scr, int lane, const float (&v)[64]) {
;     ...
;     LDS_WAIT(); asm volatile("" ::: "memory");
; #pragma unroll
;     for (int j = 0; j < 8; ++j) { const int n = (lane >> 3) + 8 * j; const LAS float* s = scr + (8 * c) * 65 + n;
;         v4u o; o.x = cvt_pk_bf16(s[0 * 65] * s0[0], s[1 * 65] * s0[1]); o.y = cvt_pk_bf16(s[2 * 65] * s0[2], s[3 * 65] * s0[3]); o.z = cvt_pk_bf16(s[4 * 65] * s1[0], s[5 * 65] * s1[1]); o.w = cvt_pk_bf16(s[6 * 65] * s1[2], s[7 * 65] * s1[3]);
;         *(v4u*)(ci.dst + (size_t)(ci.drow0 + n) * ci.ldd + ci.k0 + 8 * c) = o; }
	v_mul_f32_e32 v8, v4, v16
	v_mul_f32_e32 v15, v5, v17
	v_cvt_pk_bf16_f32 v16, v8, v15
	ds_read2_b32 v[18:19], v14 offset0:130 offset1:195
	s_add_i32 s3, s3, s33
	s_add_i32 s66, s66, s67
	s_add_i32 s68, s68, s69
	s_add_i32 s70, s70, s71
	s_waitcnt lgkmcnt(0)
	v_mul_f32_e32 v15, v7, v19
	v_mul_f32_e32 v8, v6, v18
	v_cvt_pk_bf16_f32 v17, v8, v15
	v_add_u32_e32 v15, 0x400, v14
	ds_read2_b32 v[18:19], v15 offset0:4 offset1:69
	s_add_i32 s72, s72, s73
	s_add_i32 s74, s74, s75
	v_readlane_b32 s78, v254, 33
	v_readlane_b32 s79, v254, 34
	s_waitcnt lgkmcnt(0)
	v_mul_f32_e32 v8, v0, v18
	v_mul_f32_e32 v18, v1, v19
	v_cvt_pk_bf16_f32 v18, v8, v18
	ds_read2_b32 v[20:21], v15 offset0:134 offset1:199
	v_readlane_b32 s80, v255, 21
	v_readlane_b32 s77, v254, 32
	s_movk_i32 s78, 0x1580
	v_readlane_b32 s82, v255, 23
	s_waitcnt lgkmcnt(0)
	v_mul_f32_e32 v8, v2, v20
	v_mul_f32_e32 v19, v3, v21
	v_cvt_pk_bf16_f32 v19, v8, v19
	v_ashrrev_i32_e32 v8, 31, v24
	v_mul_lo_u32 v8, s56, v8
	v_mad_u64_u32 v[20:21], s[4:5], s56, v24, 0
	v_add3_u32 v21, v21, v8, v22
	ds_read2_b32 v[22:23], v14 offset0:8 offset1:73
	v_lshl_add_u64 v[20:21], v[20:21], 1, s[60:61]
	s_lshl_b64 s[4:5], s[58:59], 1
	v_lshl_add_u64 v[20:21], v[20:21], 0, s[4:5]
	v_lshlrev_b32_e32 v8, 1, v10
	v_lshl_add_u64 v[20:21], v[20:21], 0, v[8:9]
	global_store_dwordx4 v[20:21], v[16:19], off
	s_cmpk_lt_i32 s3, 27072
	v_readlane_b32 s83, v255, 24
	s_waitcnt lgkmcnt(0)
	v_mul_f32_e32 v16, v4, v22
	v_mul_f32_e32 v17, v5, v23
	v_cvt_pk_bf16_f32 v16, v16, v17
	ds_read2_b32 v[18:19], v14 offset0:138 offset1:203
	s_mov_b32 s79, 0x3f22f983
	s_mov_b32 s85, 0xbfc90fda
	s_brev_b32 s86, 1
	s_movk_i32 s87, 0x1f8
	s_waitcnt lgkmcnt(0)
	v_mul_f32_e32 v17, v6, v18
	v_mul_f32_e32 v18, v7, v19
	v_cvt_pk_bf16_f32 v17, v17, v18
	ds_read2_b32 v[18:19], v15 offset0:12 offset1:77
	s_mov_b64 s[88:89], 0x80
	s_mov_b64 s[92:93], 0x4000
	s_mov_b64 s[94:95], 0x4800
	v_readlane_b32 s81, v255, 22
	s_waitcnt lgkmcnt(0)
	v_mul_f32_e32 v18, v0, v18
	v_mul_f32_e32 v19, v1, v19
	v_cvt_pk_bf16_f32 v18, v18, v19
	ds_read2_b32 v[20:21], v15 offset0:142 offset1:207
	s_waitcnt lgkmcnt(0)
	v_mul_f32_e32 v19, v2, v20
	v_mul_f32_e32 v20, v3, v21
	v_cvt_pk_bf16_f32 v19, v19, v20
	v_add_u32_e32 v20, 8, v24
	v_ashrrev_i32_e32 v21, 31, v20
	v_mul_lo_u32 v22, s56, v21
	v_mul_lo_u32 v23, s57, v20
	v_mad_u64_u32 v[20:21], s[6:7], s56, v20, 0
	v_add3_u32 v21, v21, v22, v23
	ds_read2_b32 v[22:23], v14 offset0:16 offset1:81
	v_lshl_add_u64 v[20:21], v[20:21], 1, s[60:61]
	v_lshl_add_u64 v[20:21], v[20:21], 0, s[4:5]
	v_lshl_add_u64 v[20:21], v[20:21], 0, v[8:9]
	global_store_dwordx4 v[20:21], v[16:19], off
	s_waitcnt lgkmcnt(0)
	s_nop 0
	v_mul_f32_e32 v16, v4, v22
	v_mul_f32_e32 v17, v5, v23
	v_cvt_pk_bf16_f32 v16, v16, v17
	ds_read2_b32 v[18:19], v14 offset0:146 offset1:211
	s_waitcnt lgkmcnt(0)
	v_mul_f32_e32 v17, v6, v18
	v_mul_f32_e32 v18, v7, v19
	v_cvt_pk_bf16_f32 v17, v17, v18
	ds_read2_b32 v[18:19], v15 offset0:20 offset1:85
	s_waitcnt lgkmcnt(0)
	v_mul_f32_e32 v18, v0, v18
	v_mul_f32_e32 v19, v1, v19
	v_cvt_pk_bf16_f32 v18, v18, v19
	ds_read2_b32 v[20:21], v15 offset0:150 offset1:215
	s_waitcnt lgkmcnt(0)
	v_mul_f32_e32 v19, v2, v20
	v_mul_f32_e32 v20, v3, v21
	v_cvt_pk_bf16_f32 v19, v19, v20
	v_add_u32_e32 v20, 16, v24
	v_ashrrev_i32_e32 v21, 31, v20
	v_mul_lo_u32 v22, s56, v21
	v_mul_lo_u32 v23, s57, v20
	v_mad_u64_u32 v[20:21], s[6:7], s56, v20, 0
	v_add3_u32 v21, v21, v22, v23
	ds_read2_b32 v[22:23], v14 offset0:24 offset1:89
	v_lshl_add_u64 v[20:21], v[20:21], 1, s[60:61]
	v_lshl_add_u64 v[20:21], v[20:21], 0, s[4:5]
	v_lshl_add_u64 v[20:21], v[20:21], 0, v[8:9]
	global_store_dwordx4 v[20:21], v[16:19], off
	s_waitcnt lgkmcnt(0)
	s_nop 0
	v_mul_f32_e32 v16, v4, v22
	v_mul_f32_e32 v17, v5, v23
	v_cvt_pk_bf16_f32 v16, v16, v17
	ds_read2_b32 v[18:19], v14 offset0:154 offset1:219
	s_waitcnt lgkmcnt(0)
	v_mul_f32_e32 v17, v6, v18
	v_mul_f32_e32 v18, v7, v19
	v_cvt_pk_bf16_f32 v17, v17, v18
	ds_read2_b32 v[18:19], v15 offset0:28 offset1:93
	s_waitcnt lgkmcnt(0)
	v_mul_f32_e32 v18, v0, v18
	v_mul_f32_e32 v19, v1, v19
	v_cvt_pk_bf16_f32 v18, v18, v19
	ds_read2_b32 v[20:21], v15 offset0:158 offset1:223
	s_waitcnt lgkmcnt(0)
; __device__ __forceinline__ unsigned cvt_pk_bf16(float lo, float hi) { unsigned r; asm volatile("v_cvt_pk_bf16_f32 %0, %1, %2" : "=v"(r) : "v"(lo), "v"(hi)); return r; }
; #define LAS __attribute__((address_space(3)))
; #define LDS_WAIT() asm volatile("s_waitcnt lgkmcnt(0)" ::: "memory")
; __device__ __forceinline__ void conv_store(const ConvItem& ci, LAS float* scr, int lane, const float (&v)[64]) {
;     ...
;     for (int j = 0; j < 8; ++j) { const int n = (lane >> 3) + 8 * j; const LAS float* s = scr + (8 * c) * 65 + n;
;         v4u o; o.x = cvt_pk_bf16(s[0 * 65] * s0[0], s[1 * 65] * s0[1]); o.y = cvt_pk_bf16(s[2 * 65] * s0[2], s[3 * 65] * s0[3]); o.z = cvt_pk_bf16(s[4 * 65] * s1[0], s[5 * 65] * s1[1]); o.w = cvt_pk_bf16(s[6 * 65] * s1[2], s[7 * 65] * s1[3]);
;         *(v4u*)(ci.dst + (size_t)(ci.drow0 + n) * ci.ldd + ci.k0 + 8 * c) = o; }
;     LDS_WAIT(); asm volatile("" ::: "memory");
; }
	v_mul_f32_e32 v19, v2, v20
	v_mul_f32_e32 v20, v3, v21
	v_cvt_pk_bf16_f32 v19, v19, v20
	v_add_u32_e32 v20, 24, v24
	v_ashrrev_i32_e32 v21, 31, v20
	v_mul_lo_u32 v22, s56, v21
	v_mul_lo_u32 v23, s57, v20
	v_mad_u64_u32 v[20:21], s[6:7], s56, v20, 0
	v_add3_u32 v21, v21, v22, v23
	ds_read2_b32 v[22:23], v14 offset0:32 offset1:97
	v_lshl_add_u64 v[20:21], v[20:21], 1, s[60:61]
	v_lshl_add_u64 v[20:21], v[20:21], 0, s[4:5]
	v_lshl_add_u64 v[20:21], v[20:21], 0, v[8:9]
	global_store_dwordx4 v[20:21], v[16:19], off
	s_waitcnt lgkmcnt(0)
	s_nop 0
	v_mul_f32_e32 v16, v4, v22
	v_mul_f32_e32 v17, v5, v23
	v_cvt_pk_bf16_f32 v16, v16, v17
	ds_read2_b32 v[18:19], v14 offset0:162 offset1:227
	s_waitcnt lgkmcnt(0)
	v_mul_f32_e32 v17, v6, v18
	v_mul_f32_e32 v18, v7, v19
	v_cvt_pk_bf16_f32 v17, v17, v18
	ds_read2_b32 v[18:19], v15 offset0:36 offset1:101
	s_waitcnt lgkmcnt(0)
	v_mul_f32_e32 v18, v0, v18
	v_mul_f32_e32 v19, v1, v19
	v_cvt_pk_bf16_f32 v18, v18, v19
	ds_read2_b32 v[20:21], v15 offset0:166 offset1:231
	s_waitcnt lgkmcnt(0)
	v_mul_f32_e32 v19, v2, v20
	v_mul_f32_e32 v20, v3, v21
	v_cvt_pk_bf16_f32 v19, v19, v20
	v_add_u32_e32 v20, 32, v24
	v_ashrrev_i32_e32 v21, 31, v20
	v_mul_lo_u32 v22, s56, v21
	v_mul_lo_u32 v23, s57, v20
	v_mad_u64_u32 v[20:21], s[6:7], s56, v20, 0
	v_add3_u32 v21, v21, v22, v23
	ds_read2_b32 v[22:23], v14 offset0:40 offset1:105
	v_lshl_add_u64 v[20:21], v[20:21], 1, s[60:61]
	v_lshl_add_u64 v[20:21], v[20:21], 0, s[4:5]
	v_lshl_add_u64 v[20:21], v[20:21], 0, v[8:9]
	global_store_dwordx4 v[20:21], v[16:19], off
	s_waitcnt lgkmcnt(0)
	s_nop 0
	v_mul_f32_e32 v16, v4, v22
	v_mul_f32_e32 v17, v5, v23
	v_cvt_pk_bf16_f32 v16, v16, v17
	ds_read2_b32 v[18:19], v14 offset0:170 offset1:235
	s_waitcnt lgkmcnt(0)
	v_mul_f32_e32 v17, v6, v18
	v_mul_f32_e32 v18, v7, v19
	v_cvt_pk_bf16_f32 v17, v17, v18
	ds_read2_b32 v[18:19], v15 offset0:44 offset1:109
	s_waitcnt lgkmcnt(0)
	v_mul_f32_e32 v18, v0, v18
	v_mul_f32_e32 v19, v1, v19
	v_cvt_pk_bf16_f32 v18, v18, v19
	ds_read2_b32 v[20:21], v15 offset0:174 offset1:239
	s_waitcnt lgkmcnt(0)
	v_mul_f32_e32 v19, v2, v20
	v_mul_f32_e32 v20, v3, v21
	v_cvt_pk_bf16_f32 v19, v19, v20
	v_add_u32_e32 v20, 40, v24
	v_ashrrev_i32_e32 v21, 31, v20
	v_mul_lo_u32 v22, s56, v21
	v_mul_lo_u32 v23, s57, v20
	v_mad_u64_u32 v[20:21], s[6:7], s56, v20, 0
	v_add3_u32 v21, v21, v22, v23
	ds_read2_b32 v[22:23], v14 offset0:48 offset1:113
	v_lshl_add_u64 v[20:21], v[20:21], 1, s[60:61]
	v_lshl_add_u64 v[20:21], v[20:21], 0, s[4:5]
	v_lshl_add_u64 v[20:21], v[20:21], 0, v[8:9]
	global_store_dwordx4 v[20:21], v[16:19], off
	s_waitcnt lgkmcnt(0)
	s_nop 0
	v_mul_f32_e32 v16, v4, v22
	v_mul_f32_e32 v17, v5, v23
	v_cvt_pk_bf16_f32 v16, v16, v17
	ds_read2_b32 v[18:19], v14 offset0:178 offset1:243
	s_waitcnt lgkmcnt(0)
	v_mul_f32_e32 v17, v6, v18
	v_mul_f32_e32 v18, v7, v19
	v_cvt_pk_bf16_f32 v17, v17, v18
	ds_read2_b32 v[18:19], v15 offset0:52 offset1:117
	s_waitcnt lgkmcnt(0)
	v_mul_f32_e32 v18, v0, v18
	v_mul_f32_e32 v19, v1, v19
	v_cvt_pk_bf16_f32 v18, v18, v19
	ds_read2_b32 v[20:21], v15 offset0:182 offset1:247
	s_waitcnt lgkmcnt(0)
	v_mul_f32_e32 v19, v2, v20
	v_mul_f32_e32 v20, v3, v21
	v_cvt_pk_bf16_f32 v19, v19, v20
	v_add_u32_e32 v20, 48, v24
	v_ashrrev_i32_e32 v21, 31, v20
	v_mul_lo_u32 v22, s56, v21
	v_mul_lo_u32 v23, s57, v20
	v_mad_u64_u32 v[20:21], s[6:7], s56, v20, 0
	v_add3_u32 v21, v21, v22, v23
	ds_read2_b32 v[22:23], v14 offset0:56 offset1:121
	v_lshl_add_u64 v[20:21], v[20:21], 1, s[60:61]
	v_lshl_add_u64 v[20:21], v[20:21], 0, s[4:5]
	v_lshl_add_u64 v[20:21], v[20:21], 0, v[8:9]
	global_store_dwordx4 v[20:21], v[16:19], off
	s_waitcnt lgkmcnt(0)
	v_mul_f32_e32 v4, v4, v22
	v_mul_f32_e32 v5, v5, v23
	v_cvt_pk_bf16_f32 v4, v4, v5
	ds_read2_b32 v[16:17], v14 offset0:186 offset1:251
	s_waitcnt lgkmcnt(0)
	v_mul_f32_e32 v5, v6, v16
	v_mul_f32_e32 v6, v7, v17
	v_cvt_pk_bf16_f32 v5, v5, v6
	ds_read2_b32 v[6:7], v15 offset0:60 offset1:125
	s_waitcnt lgkmcnt(0)
	v_mul_f32_e32 v0, v0, v6
	v_mul_f32_e32 v1, v1, v7
	v_cvt_pk_bf16_f32 v6, v0, v1
	ds_read2_b32 v[0:1], v15 offset0:190 offset1:255
	s_waitcnt lgkmcnt(0)
	v_mul_f32_e32 v0, v2, v0
	v_mul_f32_e32 v1, v3, v1
	v_cvt_pk_bf16_f32 v7, v0, v1
	v_add_u32_e32 v0, 56, v24
	v_ashrrev_i32_e32 v1, 31, v0
	v_mul_lo_u32 v2, s56, v1
	v_mul_lo_u32 v3, s57, v0
	v_mad_u64_u32 v[0:1], s[6:7], s56, v0, 0
	v_add3_u32 v1, v1, v2, v3
	v_lshl_add_u64 v[0:1], v[0:1], 1, s[60:61]
	v_lshl_add_u64 v[0:1], v[0:1], 0, s[4:5]
	v_lshl_add_u64 v[0:1], v[0:1], 0, v[8:9]
	global_store_dwordx4 v[0:1], v[4:7], off
	s_waitcnt lgkmcnt(0)
	s_cbranch_scc0 .Lcvp0b_ret

; __device__ __forceinline__ void xcd_barrier(const XcdBarrier& b) {
;     asm volatile("s_waitcnt vmcnt(0)" ::: "memory");
;     __syncthreads();
;     if (threadIdx.x == 0) {
;         unsigned* bar = b.bar;
;         __builtin_amdgcn_s_waitcnt(0);
;         unsigned nloc = b.st[0], nx = b.st[1];
;         if (nloc == 0u) { xcd_barrier_complete(bar, b.x, nloc, nx); b.st[0] = nloc; b.st[1] = nx; }
.Lcvp0b_ret:
.LBB0_92:
	s_cmp_gt_i32 s76, s2
	s_cselect_b64 s[0:1], -1, 0
	s_cmp_ge_i32 s2, s77
	s_cselect_b64 s[2:3], -1, 0
	v_readlane_b32 s53, v254, 36
	s_or_b64 s[0:1], s[0:1], s[2:3]
	s_add_i32 s38, s53, 2
	s_and_b64 vcc, exec, s[0:1]
	s_movk_i32 s70, 0xad
	s_cbranch_vccnz .LBB0_125
	s_mov_b32 s2, s38
	s_cmp_le_i32 s76, s2
	s_cselect_b64 s[0:1], -1, 0
	s_cmp_lt_i32 s2, s77
	s_cselect_b64 s[2:3], -1, 0
	s_and_b64 s[0:1], s[0:1], s[2:3]
	v_readlane_b32 s2, v254, 4
	v_readlane_b32 s3, v254, 5
	s_and_b64 s[0:1], s[2:3], s[0:1]
	s_andn2_b64 vcc, exec, s[0:1]
	s_cbranch_vccnz .LBB0_125
	v_readlane_b32 s36, v254, 2
	v_readlane_b32 s37, v254, 3
	v_readlane_b32 s33, v254, 6
	s_waitcnt vmcnt(0)
	s_waitcnt lgkmcnt(0)
	s_barrier
	s_mov_b64 s[0:1], exec
	v_readlane_b32 s2, v254, 13
	v_readlane_b32 s3, v254, 14
	s_and_b64 s[2:3], s[0:1], s[2:3]
	s_mov_b64 exec, s[2:3]
	s_cbranch_execz .LBB0_124
	v_readlane_b32 s2, v254, 7
	s_waitcnt vmcnt(0) expcnt(0) lgkmcnt(0)
	s_nop 0
	v_mov_b32_e32 v0, s2
	ds_read_b32 v2, v0
	ds_read_b32 v0, v0 offset:4
	s_waitcnt lgkmcnt(1)
	v_cmp_ne_u32_e32 vcc, 0, v2
	s_cbranch_vccnz .LBB0_109
	v_readlane_b32 s4, v254, 8
	v_readlane_b32 s5, v254, 9
	s_load_dwordx2 s[2:3], s[4:5], 0x0
	s_load_dword s7, s[4:5], 0x8
	s_add_u32 s4, s36, 0x1000
	s_addc_u32 s5, s37, 0
	s_add_u32 s6, s36, 0x1100
	s_waitcnt lgkmcnt(0)
	s_mul_i32 s30, s3, s2
	s_mul_i32 s30, s30, s7
	s_addc_u32 s7, s37, 0
	s_add_u32 s8, s36, 0x1200
	s_addc_u32 s9, s37, 0
	s_add_u32 s10, s36, 0x1300
	s_addc_u32 s11, s37, 0
	s_mov_b32 s31, 1
	s_mov_b64 s[12:13], 0
	s_branch .LBB0_99

; #define LAS __attribute__((address_space(3)))
; #define IN(k) in_range(lo, hi, (k))
; __global__ void __launch_bounds__(NWAVES * 64, 2) mk_fwd(Args args) {
;     ...
;         if (EN(0) && IN(pb + 0)) {
;             PH_LOCALS
;             LAS float* scr = (LAS float*)(lds + RING_OFF + wave * 16640);   static_assert(8 * 16640 <= LDSCTL_OFF, "converter scratch below the LDS control words");
;             constexpr int I_UP = (D / 64) * (NUP / 64), I_DN = (DFF / 64) * (D / 64), I_IN = (D / 64) * (DINP / 64), I_GLU = 16 * 16, I_L = 4 * 16, I_V1 = 16 * 4, I_V2 = 4 * 16,
;                           I_BS5 = 16 * 32, I_BAT = 8 * 32, I_BRW = 16 * 32, I_OUT = 32 * 32;
;             constexpr int NITEMS = 2 * I_UP + 2 * I_DN + I_IN + I_GLU + 3 * I_L + I_V1 + I_V2 + I_BS5 + I_BAT + I_BRW + I_OUT;
;             const int lv = l > 0 ? l - 1 : 0;
;     ...
;             for (int it = gw; it < NITEMS; it += NGW) {
;                 ConvItem ca; CONV_DESC(ca, it);
.LBB0_346:
	v_readlane_b32 s99, v254, 35
	v_readlane_b32 s98, v254, 38
	s_nop 3
	s_cmp_lt_u32 s99, 128
	s_cbranch_scc1 .Lcvskip_p3
	s_cmp_gt_u32 s98, 2
	s_cbranch_scc1 .Lcvskip_p3
	v_mov_b32_e32 v250, v254
	v_mov_b32_e32 v251, v255
	v_writelane_b32 v252, s0, 0
	s_nop 0
	v_writelane_b32 v252, s1, 1
	s_nop 0
	v_writelane_b32 v252, s2, 2
	s_nop 0
	v_writelane_b32 v252, s3, 3
	s_nop 0
	v_writelane_b32 v252, s4, 4
	s_nop 0
	v_writelane_b32 v252, s5, 5
	s_nop 0
	v_writelane_b32 v252, s6, 6
	s_nop 0
	v_writelane_b32 v252, s7, 7
	s_nop 0
	v_writelane_b32 v252, s8, 8
	s_nop 0
	v_writelane_b32 v252, s9, 9
	s_nop 0
	v_writelane_b32 v252, s10, 10
	s_nop 0
	v_writelane_b32 v252, s11, 11
	s_nop 0
	v_writelane_b32 v252, s12, 12
	s_nop 0
	v_writelane_b32 v252, s13, 13
	s_nop 0
	v_writelane_b32 v252, s14, 14
	s_nop 0
	v_writelane_b32 v252, s15, 15
	s_nop 0
	v_writelane_b32 v252, s16, 16
	s_nop 0
	v_writelane_b32 v252, s17, 17
	s_nop 0
	v_writelane_b32 v252, s18, 18
	s_nop 0
	v_writelane_b32 v252, s19, 19
	s_nop 0
	v_writelane_b32 v252, s20, 20
	s_nop 0
	v_writelane_b32 v252, s21, 21
	s_nop 0
	v_writelane_b32 v252, s22, 22
	s_nop 0
	v_writelane_b32 v252, s23, 23
	s_nop 0
	v_writelane_b32 v252, s24, 24
	s_nop 0
	v_writelane_b32 v252, s25, 25
	s_nop 0
	v_writelane_b32 v252, s26, 26
	s_nop 0
	v_writelane_b32 v252, s27, 27
	s_nop 0
	v_writelane_b32 v252, s28, 28
	s_nop 0
	v_writelane_b32 v252, s29, 29
	s_nop 0
	v_writelane_b32 v252, s30, 30
	s_nop 0
	v_writelane_b32 v252, s31, 31
	s_nop 0
	v_writelane_b32 v252, s32, 32
	s_nop 0
	v_writelane_b32 v252, s33, 33
	s_nop 0
	v_writelane_b32 v252, s34, 34
	s_nop 0
	v_writelane_b32 v252, s35, 35
	s_nop 0
	v_writelane_b32 v252, s36, 36
	s_nop 0
	v_writelane_b32 v252, s37, 37
	s_nop 0
	v_writelane_b32 v252, s38, 38
	s_nop 0
	v_writelane_b32 v252, s39, 39
	s_nop 0
	v_writelane_b32 v252, s40, 40
	s_nop 0
	v_writelane_b32 v252, s41, 41
	s_nop 0
	v_writelane_b32 v252, s42, 42
	s_nop 0
	v_writelane_b32 v252, s43, 43
	s_nop 0
	v_writelane_b32 v252, s44, 44
	s_nop 0
	v_writelane_b32 v252, s45, 45
	s_nop 0
	v_writelane_b32 v252, s46, 46
	s_nop 0
	v_writelane_b32 v252, s47, 47
	s_nop 0
	v_writelane_b32 v252, s48, 48
	s_nop 0
	v_writelane_b32 v252, s49, 49
	s_nop 0
	v_writelane_b32 v252, s50, 50
	s_nop 0
	v_writelane_b32 v252, s51, 51
	s_nop 0
	v_writelane_b32 v252, s52, 52
	s_nop 0
	v_writelane_b32 v252, s53, 53
	s_nop 0
	v_writelane_b32 v252, s54, 54
	s_nop 0
	v_writelane_b32 v252, s55, 55
	s_nop 0
	v_writelane_b32 v252, s56, 56
	s_nop 0
	v_writelane_b32 v252, s57, 57
	s_nop 0
	v_writelane_b32 v252, s58, 58
	s_nop 0
	v_writelane_b32 v252, s59, 59
	s_nop 0
	v_writelane_b32 v252, s60, 60
	s_nop 0
	v_writelane_b32 v252, s61, 61
	s_nop 0
	v_writelane_b32 v252, s62, 62
	s_nop 0
	v_writelane_b32 v252, s63, 63
	s_nop 0
	v_writelane_b32 v253, s64, 0
	s_nop 0
	v_writelane_b32 v253, s65, 1
	s_nop 0
	v_writelane_b32 v253, s66, 2
	s_nop 0
	v_writelane_b32 v253, s67, 3
	s_nop 0
	v_writelane_b32 v253, s68, 4
	s_nop 0
	v_writelane_b32 v253, s69, 5
	s_nop 0
	v_writelane_b32 v253, s70, 6
	s_nop 0
	v_writelane_b32 v253, s71, 7
	s_nop 0
	v_writelane_b32 v253, s72, 8
	s_nop 0
	v_writelane_b32 v253, s73, 9
	s_nop 0
	v_writelane_b32 v253, s74, 10
	s_nop 0
	v_writelane_b32 v253, s75, 11
	s_nop 0
	v_writelane_b32 v253, s76, 12
	s_nop 0
	v_writelane_b32 v253, s77, 13
	s_nop 0
	v_writelane_b32 v253, s78, 14
	s_nop 0
	v_writelane_b32 v253, s79, 15
	s_nop 0
	v_writelane_b32 v253, s80, 16
	s_nop 0
	v_writelane_b32 v253, s81, 17
	s_nop 0
	v_writelane_b32 v253, s82, 18
	s_nop 0
	v_writelane_b32 v253, s83, 19
	s_nop 0
	v_writelane_b32 v253, s84, 20
	s_nop 0
	v_writelane_b32 v253, s85, 21
	s_nop 0
	v_writelane_b32 v253, s86, 22
	s_nop 0
	v_writelane_b32 v253, s87, 23
	s_nop 0
	v_writelane_b32 v253, s88, 24
	s_nop 0
	v_writelane_b32 v253, s89, 25
	s_nop 0
	v_writelane_b32 v253, s90, 26
	s_nop 0
	v_writelane_b32 v253, s91, 27
	s_nop 0
	v_writelane_b32 v253, s92, 28
	s_nop 0
	v_writelane_b32 v253, s93, 29
	s_nop 0
	v_writelane_b32 v253, s94, 30
	s_nop 0
	v_writelane_b32 v253, s95, 31
	s_nop 0
	v_writelane_b32 v253, s96, 32
	s_nop 0
	v_writelane_b32 v253, s97, 33
	s_nop 0
	v_writelane_b32 v253, vcc_lo, 34
	s_nop 0
	v_writelane_b32 v253, vcc_hi, 35
	s_nop 1
	v_readlane_b32 s84, v254, 35
	s_nop 3
	v_readlane_b32 s0, v254, 8
	v_readlane_b32 s4, v254, 10
	v_readlane_b32 s1, v254, 9
	v_mbcnt_lo_u32_b32 v11, -1, 0
	v_mbcnt_hi_u32_b32 v11, -1, v11
	s_load_dword s6, s[0:1], 0x0
	s_mov_b32 s3, s84
	s_waitcnt lgkmcnt(0)
	s_movk_i32 s6, 128
	s_lshl_b32 s3, s3, 3
	v_readlane_b32 s0, v254, 0
	s_add_i32 s3, s3, s4
	s_add_i32 s3, s3, 0x4500
	v_readlane_b32 s1, v254, 1
	s_cmpk_gt_i32 s3, 21439
	s_cbranch_scc1 .Lcvp30_ret
; __global__ void __launch_bounds__(NWAVES * 64, 2) mk_fwd(Args args) {
;     ...
;             for (int it = gw; it < NITEMS; it += NGW) {
;                 ConvItem ca; CONV_DESC(ca, it);
	s_load_dwordx2 s[8:9], s[0:1], 0x138
	v_readlane_b32 s14, v254, 38
	s_nop 0
	s_add_i32 s14, s14, 1
	s_mulk_i32 s4, 0x4100
	s_add_i32 s7, s4, 0
	v_sub_u32_e64 v0, s14, 1 clamp
	s_lshl_b32 s33, s6, 3
	v_readfirstlane_b32 s4, v0
	s_lshl_b32 s96, s4, 16
	s_waitcnt lgkmcnt(0)
	s_add_u32 s4, s8, 0x22800000
	s_addc_u32 s5, s9, 0
	v_writelane_b32 v254, s4, 39
	s_mov_b32 s15, s97
	v_and_b32_e32 v0, 7, v11
	v_writelane_b32 v254, s5, 40
	s_add_u32 s4, s8, 0x22780000
	s_addc_u32 s5, s9, 0
	v_writelane_b32 v254, s4, 41
	v_ashrrev_i32_e32 v13, 3, v11
	v_lshlrev_b32_e32 v10, 3, v0
	v_writelane_b32 v254, s5, 42
	s_lshl_b32 s4, s14, 18
	s_add_u32 s10, s8, 0x22700000
	s_addc_u32 s11, s9, 0
	v_writelane_b32 v254, s10, 43
	s_mov_b32 s5, s97
	v_mul_u32_u24_e32 v0, 0x820, v0
	v_writelane_b32 v254, s11, 44
	s_mul_i32 s10, s14, 0x18000
	s_mov_b32 s11, s97
	v_writelane_b32 v254, s10, 45
	v_lshlrev_b32_e32 v1, 2, v13
	v_lshl_add_u32 v12, v11, 2, s7
	v_writelane_b32 v254, s11, 46
	s_add_u32 s10, s8, 0x22680000
	s_addc_u32 s11, s9, 0
	v_writelane_b32 v254, s10, 47
	v_add3_u32 v14, s7, v0, v1
	s_mov_b32 s41, s97
	v_writelane_b32 v254, s11, 48
	s_add_u32 s10, s8, 0x22600000
	s_addc_u32 s11, s9, 0
	v_writelane_b32 v254, s10, 49
	s_nop 1
	v_writelane_b32 v254, s11, 50
	s_lshl_b32 s10, s14, 20
	s_mov_b32 s11, s97
	v_writelane_b32 v254, s10, 51
	s_nop 1
	v_writelane_b32 v254, s11, 52
	s_add_u32 s10, s8, 0x22400000
	s_addc_u32 s11, s9, 0
	v_writelane_b32 v254, s10, 53
	s_nop 1
	v_writelane_b32 v254, s11, 54
	s_lshl_b32 s10, s14, 21
	s_mov_b32 s11, s97
	v_writelane_b32 v254, s10, 55
	s_nop 1
	v_writelane_b32 v254, s11, 56
	s_add_u32 s10, s8, 0x22e80000
	s_addc_u32 s11, s9, 0
	v_writelane_b32 v254, s10, 57
	s_nop 1
	v_writelane_b32 v254, s11, 58
	s_add_u32 s10, s8, 0x27b80000
	s_addc_u32 s11, s9, 0
	v_writelane_b32 v254, s10, 59
	s_nop 1
	v_writelane_b32 v254, s11, 60
	s_add_u32 s10, s8, 0x22880000
	s_addc_u32 s11, s9, 0
	v_writelane_b32 v254, s10, 61
	s_nop 1
	v_writelane_b32 v254, s11, 62
	s_lshl_b32 s10, s14, 22
	s_add_u32 s12, s8, 0x23280000
	s_addc_u32 s13, s9, 0
	v_writelane_b32 v254, s12, 63
	s_mov_b32 s11, s97
	s_nop 0
	v_writelane_b32 v255, s13, 0
	s_mul_i32 s12, s14, 0xac0000
	s_mov_b32 s13, s97
	v_writelane_b32 v255, s12, 1
	s_nop 1
	v_writelane_b32 v255, s13, 2
	s_add_u32 s12, s8, 0x26580000
	s_addc_u32 s13, s9, 0
	v_writelane_b32 v255, s12, 3
	s_nop 1
	v_writelane_b32 v255, s13, 4
	s_add_u32 s12, s8, 0x1d200000
	s_addc_u32 s13, s9, 0
	s_lshl_b32 s40, s14, 11
	v_writelane_b32 v255, s12, 5
	s_add_u32 s16, s8, 0x1e800000
	s_addc_u32 s17, s9, 0
	v_writelane_b32 v255, s13, 6
	v_writelane_b32 v255, s16, 7
	s_mul_i32 s12, s14, 0x1de0000
	s_mul_i32 s14, s14, 0x1580000
	v_writelane_b32 v255, s17, 8
	v_writelane_b32 v255, s14, 9
	s_mov_b32 s13, s97
	s_nop 0
	v_writelane_b32 v255, s15, 10
	s_add_u32 s14, s8, 0x23a80000
	s_addc_u32 s15, s9, 0
	v_writelane_b32 v255, s14, 11
	s_add_u32 s8, s8, 0x1a700000
	s_addc_u32 s9, s9, 0
	v_writelane_b32 v255, s15, 12
	v_writelane_b32 v255, s8, 13
	s_lshl_b64 s[4:5], s[4:5], 2
	s_lshl_b32 s7, s3, 4
	v_writelane_b32 v255, s9, 14
	v_writelane_b32 v255, s4, 15
	s_add_i32 s72, s7, 0xc00
	s_lshl_b32 s7, s3, 1
	v_writelane_b32 v255, s5, 16
	s_lshl_b64 s[4:5], s[10:11], 2
	v_writelane_b32 v255, s4, 17
	s_lshl_b32 s66, s3, 6
	s_lshl_b32 s67, s6, 9
	v_writelane_b32 v255, s5, 18
	s_lshl_b64 s[4:5], s[12:13], 2
	v_writelane_b32 v255, s4, 19
	s_lshl_b32 s68, s3, 5
	s_lshl_b32 s69, s6, 8
	v_writelane_b32 v255, s5, 20
	v_writelane_b32 v255, s80, 21
	s_lshl_b32 s70, s3, 2
	s_lshl_b32 s71, s6, 5
	v_writelane_b32 v255, s81, 22
	v_writelane_b32 v255, s82, 23
	s_lshl_b32 s73, s6, 7
	s_add_i32 s74, s7, 0x13500
	s_lshl_b32 s75, s6, 4
	v_writelane_b32 v255, s83, 24
	s_branch .Lcvp30_31

; __device__ __forceinline__ void conv_load(const ConvItem& ci, int lane, float (&v)[64]) {
;     ...
;     for (int i = 0; i < 64; ++i) { const int k = ci.k0 + i, kk = k < kmax ? k : kmax; v[i] = __builtin_nontemporal_load(base + (size_t)kk * ci.ldw); }
; #pragma unroll
;     for (int i = 0; i < 64; ++i) v[i] = (okc && (ci.k0 + i) < ci.Ksrc) ? v[i] : 0.f;
.Lcvp30_30:
	s_cmp_lt_i32 s58, s76
	s_cselect_b64 s[4:5], -1, 0
	s_and_b64 s[4:5], vcc, s[4:5]
	s_cmp_lt_i32 s64, s76
	s_waitcnt vmcnt(62)
	v_cndmask_b32_e64 v21, 0, v21, s[4:5]
	s_cselect_b64 s[4:5], -1, 0
	s_and_b64 s[4:5], vcc, s[4:5]
	s_cmp_lt_i32 s65, s76
	v_cndmask_b32_e64 v20, 0, v20, s[4:5]
	s_cselect_b64 s[4:5], -1, 0
	s_and_b64 s[4:5], vcc, s[4:5]
	s_cmp_lt_i32 s78, s76
	s_waitcnt vmcnt(61)
	v_cndmask_b32_e64 v19, 0, v19, s[4:5]
	s_cselect_b64 s[4:5], -1, 0
	s_and_b64 s[4:5], vcc, s[4:5]
	s_cmp_lt_i32 s79, s76
	s_waitcnt vmcnt(60)
	v_cndmask_b32_e64 v18, 0, v18, s[4:5]
	s_cselect_b64 s[4:5], -1, 0
	s_and_b64 s[4:5], vcc, s[4:5]
	s_cmp_lt_i32 s80, s76
	s_waitcnt vmcnt(59)
	v_cndmask_b32_e64 v17, 0, v17, s[4:5]
	s_cselect_b64 s[4:5], -1, 0
	s_and_b64 s[4:5], vcc, s[4:5]
	s_cmp_lt_i32 s81, s76
	s_waitcnt vmcnt(58)
	v_cndmask_b32_e64 v16, 0, v16, s[4:5]
	s_cselect_b64 s[4:5], -1, 0
	s_and_b64 s[4:5], vcc, s[4:5]
	s_cmp_lt_i32 s82, s76
	s_waitcnt vmcnt(57)
	v_cndmask_b32_e64 v15, 0, v15, s[4:5]
	s_cselect_b64 s[4:5], -1, 0
	s_and_b64 s[4:5], vcc, s[4:5]
	s_cmp_lt_i32 s83, s76
	s_waitcnt vmcnt(56)
	v_cndmask_b32_e64 v8, 0, v8, s[4:5]
	s_cselect_b64 s[4:5], -1, 0
	s_and_b64 s[4:5], vcc, s[4:5]
	s_cmp_lt_i32 s85, s76
	s_waitcnt vmcnt(55)
	v_cndmask_b32_e64 v29, 0, v29, s[4:5]
	s_cselect_b64 s[4:5], -1, 0
	s_and_b64 s[4:5], vcc, s[4:5]
	s_cmp_lt_i32 s86, s76
	s_waitcnt vmcnt(54)
	v_cndmask_b32_e64 v28, 0, v28, s[4:5]
	s_cselect_b64 s[4:5], -1, 0
	s_and_b64 s[4:5], vcc, s[4:5]
	s_cmp_lt_i32 s87, s76
	s_waitcnt vmcnt(53)
	v_cndmask_b32_e64 v27, 0, v27, s[4:5]
	s_cselect_b64 s[4:5], -1, 0
	s_and_b64 s[4:5], vcc, s[4:5]
	s_cmp_lt_i32 s88, s76
	s_waitcnt vmcnt(52)
	v_cndmask_b32_e64 v26, 0, v26, s[4:5]
	s_cselect_b64 s[4:5], -1, 0
	s_and_b64 s[4:5], vcc, s[4:5]
	s_cmp_lt_i32 s89, s76
	s_waitcnt vmcnt(51)
	v_cndmask_b32_e64 v25, 0, v25, s[4:5]
	s_cselect_b64 s[4:5], -1, 0
	s_and_b64 s[4:5], vcc, s[4:5]
	s_cmp_lt_i32 s90, s76
	s_waitcnt vmcnt(50)
	v_cndmask_b32_e64 v24, 0, v24, s[4:5]
	s_cselect_b64 s[4:5], -1, 0
	s_and_b64 s[4:5], vcc, s[4:5]
	s_cmp_lt_i32 s92, s76
	s_waitcnt vmcnt(49)
	v_cndmask_b32_e64 v23, 0, v23, s[4:5]
	s_cselect_b64 s[4:5], -1, 0
	s_and_b64 s[4:5], vcc, s[4:5]
	s_cmp_lt_i32 s93, s76
	s_waitcnt vmcnt(48)
	v_cndmask_b32_e64 v22, 0, v22, s[4:5]
	s_cselect_b64 s[4:5], -1, 0
	s_and_b64 s[4:5], vcc, s[4:5]
	s_cmp_lt_i32 s94, s76
	s_waitcnt vmcnt(47)
	v_cndmask_b32_e64 v37, 0, v37, s[4:5]
	s_cselect_b64 s[4:5], -1, 0
	s_and_b64 s[4:5], vcc, s[4:5]
	s_cmp_lt_i32 s95, s76
	s_waitcnt vmcnt(46)
	v_cndmask_b32_e64 v36, 0, v36, s[4:5]
	s_cselect_b64 s[4:5], -1, 0
	s_and_b64 s[4:5], vcc, s[4:5]
	s_cmp_lt_i32 s50, s76
	s_waitcnt vmcnt(45)
	v_cndmask_b32_e64 v35, 0, v35, s[4:5]
	s_cselect_b64 s[4:5], -1, 0
	s_and_b64 s[4:5], vcc, s[4:5]
	s_cmp_lt_i32 s51, s76
	s_waitcnt vmcnt(44)
	v_cndmask_b32_e64 v34, 0, v34, s[4:5]
	s_cselect_b64 s[4:5], -1, 0
	s_and_b64 s[4:5], vcc, s[4:5]
	s_cmp_lt_i32 s52, s76
	s_waitcnt vmcnt(43)
	v_cndmask_b32_e64 v33, 0, v33, s[4:5]
	s_cselect_b64 s[4:5], -1, 0
	s_and_b64 s[4:5], vcc, s[4:5]
	s_cmp_lt_i32 s53, s76
	s_waitcnt vmcnt(42)
	v_cndmask_b32_e64 v32, 0, v32, s[4:5]
	s_cselect_b64 s[4:5], -1, 0
	s_and_b64 s[4:5], vcc, s[4:5]
	s_cmp_lt_i32 s6, s76
	s_waitcnt vmcnt(41)
	v_cndmask_b32_e64 v31, 0, v31, s[4:5]
	s_cselect_b64 s[4:5], -1, 0
	s_and_b64 s[4:5], vcc, s[4:5]
	s_cmp_lt_i32 s7, s76
	s_waitcnt vmcnt(40)
	v_cndmask_b32_e64 v30, 0, v30, s[4:5]
	s_cselect_b64 s[4:5], -1, 0
	s_and_b64 s[4:5], vcc, s[4:5]
	s_cmp_lt_i32 s8, s76
	s_waitcnt vmcnt(39)
	v_cndmask_b32_e64 v45, 0, v45, s[4:5]
	s_cselect_b64 s[4:5], -1, 0
	s_and_b64 s[4:5], vcc, s[4:5]
	s_cmp_lt_i32 s9, s76
	s_waitcnt vmcnt(38)
	v_cndmask_b32_e64 v44, 0, v44, s[4:5]
	s_cselect_b64 s[4:5], -1, 0
	s_and_b64 s[4:5], vcc, s[4:5]
	s_cmp_lt_i32 s10, s76
	s_waitcnt vmcnt(37)
	v_cndmask_b32_e64 v43, 0, v43, s[4:5]
	s_cselect_b64 s[4:5], -1, 0
	s_and_b64 s[4:5], vcc, s[4:5]
	s_cmp_lt_i32 s11, s76
	s_waitcnt vmcnt(36)
	v_cndmask_b32_e64 v42, 0, v42, s[4:5]
	s_cselect_b64 s[4:5], -1, 0
	s_and_b64 s[4:5], vcc, s[4:5]
	s_cmp_lt_i32 s14, s76
	s_waitcnt vmcnt(35)
	v_cndmask_b32_e64 v41, 0, v41, s[4:5]
	s_cselect_b64 s[4:5], -1, 0
	s_and_b64 s[4:5], vcc, s[4:5]
	s_cmp_lt_i32 s15, s76
	s_waitcnt vmcnt(34)
	v_cndmask_b32_e64 v40, 0, v40, s[4:5]
	s_cselect_b64 s[4:5], -1, 0
	s_and_b64 s[4:5], vcc, s[4:5]
	s_cmp_lt_i32 s16, s76
	s_waitcnt vmcnt(33)
	v_cndmask_b32_e64 v39, 0, v39, s[4:5]
	s_cselect_b64 s[4:5], -1, 0
	s_and_b64 s[4:5], vcc, s[4:5]
	s_cmp_lt_i32 s17, s76
	s_waitcnt vmcnt(32)
	v_cndmask_b32_e64 v38, 0, v38, s[4:5]
	s_cselect_b64 s[4:5], -1, 0
	s_and_b64 s[4:5], vcc, s[4:5]
	s_cmp_lt_i32 s12, s76
	s_waitcnt vmcnt(31)
	v_cndmask_b32_e64 v53, 0, v53, s[4:5]
	s_cselect_b64 s[4:5], -1, 0
	s_and_b64 s[4:5], vcc, s[4:5]
	s_cmp_lt_i32 s13, s76
	s_waitcnt vmcnt(30)
	v_cndmask_b32_e64 v52, 0, v52, s[4:5]
	s_cselect_b64 s[4:5], -1, 0
	s_and_b64 s[4:5], vcc, s[4:5]
	s_cmp_lt_i32 s20, s76
	s_waitcnt vmcnt(29)
	v_cndmask_b32_e64 v51, 0, v51, s[4:5]
	s_cselect_b64 s[4:5], -1, 0
	s_and_b64 s[4:5], vcc, s[4:5]
	s_cmp_lt_i32 s21, s76
	s_waitcnt vmcnt(28)
	v_cndmask_b32_e64 v50, 0, v50, s[4:5]
	s_cselect_b64 s[4:5], -1, 0
	s_and_b64 s[4:5], vcc, s[4:5]
	s_cmp_lt_i32 s24, s76
	s_waitcnt vmcnt(27)
	v_cndmask_b32_e64 v49, 0, v49, s[4:5]
	s_cselect_b64 s[4:5], -1, 0
	s_and_b64 s[4:5], vcc, s[4:5]
	s_cmp_lt_i32 s25, s76
	s_waitcnt vmcnt(26)
	v_cndmask_b32_e64 v48, 0, v48, s[4:5]
	s_cselect_b64 s[4:5], -1, 0
	s_and_b64 s[4:5], vcc, s[4:5]
	s_cmp_lt_i32 s26, s76
	s_waitcnt vmcnt(25)
	v_cndmask_b32_e64 v47, 0, v47, s[4:5]
	s_cselect_b64 s[4:5], -1, 0
	s_and_b64 s[4:5], vcc, s[4:5]
	s_cmp_lt_i32 s27, s76
	s_waitcnt vmcnt(24)
; #define LAS __attribute__((address_space(3)))
; #define LDS_WAIT() asm volatile("s_waitcnt lgkmcnt(0)" ::: "memory")
; __device__ __forceinline__ void conv_load(const ConvItem& ci, int lane, float (&v)[64]) {
;     ...
;     for (int i = 0; i < 64; ++i) v[i] = (okc && (ci.k0 + i) < ci.Ksrc) ? v[i] : 0.f;
; }
; __device__ __forceinline__ void conv_store(const ConvItem& ci, LAS float* scr, int lane, const float (&v)[64]) {
;     const int c = lane & 7;
;     f32x4 s0 = {1.f, 1.f, 1.f, 1.f}, s1 = s0;
;     if (ci.ks) { const int kb = ci.k0 + 8 * c < ci.Ksrc - 8 ? ci.k0 + 8 * c : ci.Ksrc - 8; s0 = *(const f32x4*)(ci.ks + kb); s1 = *(const f32x4*)(ci.ks + kb + 4); }
; #pragma unroll
;     for (int i = 0; i < 64; ++i) scr[i * 65 + lane] = v[i];
;     LDS_WAIT(); asm volatile("" ::: "memory");
	v_cndmask_b32_e64 v46, 0, v46, s[4:5]
	s_cselect_b64 s[4:5], -1, 0
	s_and_b64 s[4:5], vcc, s[4:5]
	s_cmp_lt_i32 s18, s76
	s_waitcnt vmcnt(23)
	v_cndmask_b32_e64 v61, 0, v61, s[4:5]
	s_cselect_b64 s[4:5], -1, 0
	s_and_b64 s[4:5], vcc, s[4:5]
	s_cmp_lt_i32 s19, s76
	s_waitcnt vmcnt(22)
	v_cndmask_b32_e64 v60, 0, v60, s[4:5]
	s_cselect_b64 s[4:5], -1, 0
	s_and_b64 s[4:5], vcc, s[4:5]
	s_cmp_lt_i32 s28, s76
	s_waitcnt vmcnt(21)
	v_cndmask_b32_e64 v59, 0, v59, s[4:5]
	s_cselect_b64 s[4:5], -1, 0
	s_and_b64 s[4:5], vcc, s[4:5]
	s_cmp_lt_i32 s29, s76
	s_waitcnt vmcnt(20)
	v_cndmask_b32_e64 v58, 0, v58, s[4:5]
	s_cselect_b64 s[4:5], -1, 0
	s_and_b64 s[4:5], vcc, s[4:5]
	s_cmp_lt_i32 s22, s76
	s_waitcnt vmcnt(19)
	v_cndmask_b32_e64 v57, 0, v57, s[4:5]
	s_cselect_b64 s[4:5], -1, 0
	s_and_b64 s[4:5], vcc, s[4:5]
	s_cmp_lt_i32 s23, s76
	s_waitcnt vmcnt(18)
	v_cndmask_b32_e64 v56, 0, v56, s[4:5]
	s_cselect_b64 s[4:5], -1, 0
	s_and_b64 s[4:5], vcc, s[4:5]
	s_cmp_lt_i32 s30, s76
	s_waitcnt vmcnt(17)
	v_cndmask_b32_e64 v55, 0, v55, s[4:5]
	s_cselect_b64 s[4:5], -1, 0
	s_and_b64 s[4:5], vcc, s[4:5]
	s_cmp_lt_i32 s31, s76
	s_waitcnt vmcnt(16)
	v_cndmask_b32_e64 v54, 0, v54, s[4:5]
	s_cselect_b64 s[4:5], -1, 0
	s_and_b64 s[4:5], vcc, s[4:5]
	s_cmp_lt_i32 s36, s76
	s_waitcnt vmcnt(15)
	v_cndmask_b32_e64 v70, 0, v70, s[4:5]
	s_cselect_b64 s[4:5], -1, 0
	s_and_b64 s[4:5], vcc, s[4:5]
	s_cmp_lt_i32 s37, s76
	s_waitcnt vmcnt(14)
	v_cndmask_b32_e64 v69, 0, v69, s[4:5]
	s_cselect_b64 s[4:5], -1, 0
	s_and_b64 s[4:5], vcc, s[4:5]
	s_cmp_lt_i32 s38, s76
	s_waitcnt vmcnt(13)
	v_cndmask_b32_e64 v68, 0, v68, s[4:5]
	s_cselect_b64 s[4:5], -1, 0
	s_and_b64 s[4:5], vcc, s[4:5]
	s_cmp_lt_i32 s39, s76
	s_waitcnt vmcnt(12)
	v_cndmask_b32_e64 v67, 0, v67, s[4:5]
	s_cselect_b64 s[4:5], -1, 0
	s_and_b64 s[4:5], vcc, s[4:5]
	s_cmp_lt_i32 s34, s76
	s_waitcnt vmcnt(11)
	v_cndmask_b32_e64 v66, 0, v66, s[4:5]
	s_cselect_b64 s[4:5], -1, 0
	s_and_b64 s[4:5], vcc, s[4:5]
	s_cmp_lt_i32 s35, s76
	s_waitcnt vmcnt(10)
	v_cndmask_b32_e64 v64, 0, v64, s[4:5]
	s_cselect_b64 s[4:5], -1, 0
	s_and_b64 s[4:5], vcc, s[4:5]
	s_cmp_lt_i32 s42, s76
	s_waitcnt vmcnt(9)
	v_cndmask_b32_e64 v63, 0, v63, s[4:5]
	s_cselect_b64 s[4:5], -1, 0
	s_and_b64 s[4:5], vcc, s[4:5]
	s_cmp_lt_i32 s43, s76
	s_waitcnt vmcnt(8)
	v_cndmask_b32_e64 v62, 0, v62, s[4:5]
	s_cselect_b64 s[4:5], -1, 0
	s_and_b64 s[4:5], vcc, s[4:5]
	s_cmp_lt_i32 s54, s76
	s_waitcnt vmcnt(7)
	v_cndmask_b32_e64 v65, 0, v65, s[4:5]
	s_cselect_b64 s[4:5], -1, 0
	s_and_b64 s[4:5], vcc, s[4:5]
	s_cmp_lt_i32 s55, s76
	s_waitcnt vmcnt(6)
	v_cndmask_b32_e64 v74, 0, v74, s[4:5]
	s_cselect_b64 s[4:5], -1, 0
	s_and_b64 s[4:5], vcc, s[4:5]
	s_cmp_lt_i32 s46, s76
	ds_write2_b32 v12, v21, v20 offset1:65
	ds_write2_b32 v12, v19, v18 offset0:130 offset1:195
	v_add_u32_e32 v18, 0x400, v12
	s_waitcnt vmcnt(5)
	v_cndmask_b32_e64 v73, 0, v73, s[4:5]
	s_cselect_b64 s[4:5], -1, 0
	ds_write2_b32 v18, v17, v16 offset0:4 offset1:69
	ds_write2_b32 v18, v15, v8 offset0:134 offset1:199
	v_add_u32_e32 v8, 0x800, v12
	s_and_b64 s[4:5], vcc, s[4:5]
	ds_write2_b32 v8, v29, v28 offset0:8 offset1:73
	ds_write2_b32 v8, v27, v26 offset0:138 offset1:203
	v_add_u32_e32 v8, 0xc00, v12
	s_cmp_lt_i32 s47, s76
	ds_write2_b32 v8, v25, v24 offset0:12 offset1:77
	ds_write2_b32 v8, v23, v22 offset0:142 offset1:207
	v_add_u32_e32 v8, 0x1000, v12
	s_waitcnt vmcnt(4)
	v_cndmask_b32_e64 v72, 0, v72, s[4:5]
	s_cselect_b64 s[4:5], -1, 0
	ds_write2_b32 v8, v37, v36 offset0:16 offset1:81
	ds_write2_b32 v8, v35, v34 offset0:146 offset1:211
	v_add_u32_e32 v8, 0x1400, v12
	s_and_b64 s[4:5], vcc, s[4:5]
	ds_write2_b32 v8, v33, v32 offset0:20 offset1:85
	ds_write2_b32 v8, v31, v30 offset0:150 offset1:215
	v_add_u32_e32 v8, 0x1800, v12
	s_cmp_lt_i32 s48, s76
	ds_write2_b32 v8, v45, v44 offset0:24 offset1:89
	ds_write2_b32 v8, v43, v42 offset0:154 offset1:219
	v_add_u32_e32 v8, 0x1c00, v12
	s_waitcnt vmcnt(3)
	v_cndmask_b32_e64 v71, 0, v71, s[4:5]
	s_cselect_b64 s[4:5], -1, 0
	ds_write2_b32 v8, v41, v40 offset0:28 offset1:93
	ds_write2_b32 v8, v39, v38 offset0:158 offset1:223
	v_add_u32_e32 v8, 0x2000, v12
	s_and_b64 s[4:5], vcc, s[4:5]
	ds_write2_b32 v8, v53, v52 offset0:32 offset1:97
	ds_write2_b32 v8, v51, v50 offset0:162 offset1:227
	v_add_u32_e32 v8, 0x2400, v12
	s_cmp_lt_i32 s49, s76
	ds_write2_b32 v8, v49, v48 offset0:36 offset1:101
	ds_write2_b32 v8, v47, v46 offset0:166 offset1:231
	v_add_u32_e32 v8, 0x2800, v12
	s_waitcnt vmcnt(2)
	v_cndmask_b32_e64 v77, 0, v77, s[4:5]
	s_cselect_b64 s[4:5], -1, 0
	ds_write2_b32 v8, v61, v60 offset0:40 offset1:105
	ds_write2_b32 v8, v59, v58 offset0:170 offset1:235
	v_add_u32_e32 v8, 0x2c00, v12
	s_and_b64 s[4:5], vcc, s[4:5]
	ds_write2_b32 v8, v57, v56 offset0:44 offset1:109
	ds_write2_b32 v8, v55, v54 offset0:174 offset1:239
	v_add_u32_e32 v8, 0x3000, v12
	s_cmp_lt_i32 s44, s76
	ds_write2_b32 v8, v70, v69 offset0:48 offset1:113
	ds_write2_b32 v8, v68, v67 offset0:178 offset1:243
	v_add_u32_e32 v8, 0x3400, v12
	s_waitcnt vmcnt(1)
	v_cndmask_b32_e64 v76, 0, v76, s[4:5]
	s_cselect_b64 s[4:5], -1, 0
	ds_write2_b32 v8, v66, v64 offset0:52 offset1:117
	ds_write2_b32 v8, v63, v62 offset0:182 offset1:247
	v_add_u32_e32 v8, 0x3800, v12
	s_and_b64 vcc, vcc, s[4:5]
	ds_write2_b32 v8, v65, v74 offset0:56 offset1:121
	ds_write2_b32 v8, v73, v72 offset0:186 offset1:251
	v_add_u32_e32 v8, 0x3c00, v12
	s_waitcnt vmcnt(0)
	v_cndmask_b32_e32 v75, 0, v75, vcc
	ds_write2_b32 v8, v71, v77 offset0:60 offset1:125
	ds_write2_b32 v8, v76, v75 offset0:190 offset1:255
	s_waitcnt lgkmcnt(0)
	ds_read2_b32 v[16:17], v14 offset1:65
	v_add_u32_e32 v24, s59, v13
	v_mul_lo_u32 v22, s57, v24
	s_ashr_i32 s59, s58, 31
	v_readlane_b32 s76, v254, 31
	s_waitcnt lgkmcnt(0)
; __device__ __forceinline__ unsigned cvt_pk_bf16(float lo, float hi) { unsigned r; asm volatile("v_cvt_pk_bf16_f32 %0, %1, %2" : "=v"(r) : "v"(lo), "v"(hi)); return r; }
; #define LAS __attribute__((address_space(3)))
; #define LDS_WAIT() asm volatile("s_waitcnt lgkmcnt(0)" ::: "memory")
; __device__ __forceinline__ void conv_store(const ConvItem& ci, LAS float* scr, int lane, const float (&v)[64]) {
;     ...
;     LDS_WAIT(); asm volatile("" ::: "memory");
; #pragma unroll
;     for (int j = 0; j < 8; ++j) { const int n = (lane >> 3) + 8 * j; const LAS float* s = scr + (8 * c) * 65 + n;
;         v4u o; o.x = cvt_pk_bf16(s[0 * 65] * s0[0], s[1 * 65] * s0[1]); o.y = cvt_pk_bf16(s[2 * 65] * s0[2], s[3 * 65] * s0[3]); o.z = cvt_pk_bf16(s[4 * 65] * s1[0], s[5 * 65] * s1[1]); o.w = cvt_pk_bf16(s[6 * 65] * s1[2], s[7 * 65] * s1[3]);
;         *(v4u*)(ci.dst + (size_t)(ci.drow0 + n) * ci.ldd + ci.k0 + 8 * c) = o; }
	v_mul_f32_e32 v8, v4, v16
	v_mul_f32_e32 v15, v5, v17
	v_cvt_pk_bf16_f32 v16, v8, v15
	ds_read2_b32 v[18:19], v14 offset0:130 offset1:195
	s_add_i32 s3, s3, s33
	s_add_i32 s66, s66, s67
	s_add_i32 s68, s68, s69
	s_add_i32 s70, s70, s71
	s_waitcnt lgkmcnt(0)
	v_mul_f32_e32 v15, v7, v19
	v_mul_f32_e32 v8, v6, v18
	v_cvt_pk_bf16_f32 v17, v8, v15
	v_add_u32_e32 v15, 0x400, v14
	ds_read2_b32 v[18:19], v15 offset0:4 offset1:69
	s_add_i32 s72, s72, s73
	s_add_i32 s74, s74, s75
	v_readlane_b32 s78, v254, 33
	v_readlane_b32 s79, v254, 34
	s_waitcnt lgkmcnt(0)
	v_mul_f32_e32 v8, v0, v18
	v_mul_f32_e32 v18, v1, v19
	v_cvt_pk_bf16_f32 v18, v8, v18
	ds_read2_b32 v[20:21], v15 offset0:134 offset1:199
	v_readlane_b32 s80, v255, 21
	v_readlane_b32 s77, v254, 32
	s_movk_i32 s78, 0x1580
	v_readlane_b32 s82, v255, 23
	s_waitcnt lgkmcnt(0)
	v_mul_f32_e32 v8, v2, v20
	v_mul_f32_e32 v19, v3, v21
	v_cvt_pk_bf16_f32 v19, v8, v19
	v_ashrrev_i32_e32 v8, 31, v24
	v_mul_lo_u32 v8, s56, v8
	v_mad_u64_u32 v[20:21], s[4:5], s56, v24, 0
	v_add3_u32 v21, v21, v8, v22
	ds_read2_b32 v[22:23], v14 offset0:8 offset1:73
	v_lshl_add_u64 v[20:21], v[20:21], 1, s[60:61]
	s_lshl_b64 s[4:5], s[58:59], 1
	v_lshl_add_u64 v[20:21], v[20:21], 0, s[4:5]
	v_lshlrev_b32_e32 v8, 1, v10
	v_lshl_add_u64 v[20:21], v[20:21], 0, v[8:9]
	global_store_dwordx4 v[20:21], v[16:19], off
	s_cmpk_lt_i32 s3, 21440
	v_readlane_b32 s83, v255, 24
	s_waitcnt lgkmcnt(0)
	v_mul_f32_e32 v16, v4, v22
	v_mul_f32_e32 v17, v5, v23
	v_cvt_pk_bf16_f32 v16, v16, v17
	ds_read2_b32 v[18:19], v14 offset0:138 offset1:203
	s_mov_b32 s79, 0x3f22f983
	s_mov_b32 s85, 0xbfc90fda
	s_brev_b32 s86, 1
	s_movk_i32 s87, 0x1f8
	s_waitcnt lgkmcnt(0)
	v_mul_f32_e32 v17, v6, v18
	v_mul_f32_e32 v18, v7, v19
	v_cvt_pk_bf16_f32 v17, v17, v18
	ds_read2_b32 v[18:19], v15 offset0:12 offset1:77
	s_mov_b64 s[88:89], 0x80
	s_mov_b64 s[92:93], 0x4000
	s_mov_b64 s[94:95], 0x4800
	v_readlane_b32 s81, v255, 22
	s_waitcnt lgkmcnt(0)
	v_mul_f32_e32 v18, v0, v18
	v_mul_f32_e32 v19, v1, v19
	v_cvt_pk_bf16_f32 v18, v18, v19
	ds_read2_b32 v[20:21], v15 offset0:142 offset1:207
	s_waitcnt lgkmcnt(0)
	v_mul_f32_e32 v19, v2, v20
	v_mul_f32_e32 v20, v3, v21
	v_cvt_pk_bf16_f32 v19, v19, v20
	v_add_u32_e32 v20, 8, v24
	v_ashrrev_i32_e32 v21, 31, v20
	v_mul_lo_u32 v22, s56, v21
	v_mul_lo_u32 v23, s57, v20
	v_mad_u64_u32 v[20:21], s[6:7], s56, v20, 0
	v_add3_u32 v21, v21, v22, v23
	ds_read2_b32 v[22:23], v14 offset0:16 offset1:81
	v_lshl_add_u64 v[20:21], v[20:21], 1, s[60:61]
	v_lshl_add_u64 v[20:21], v[20:21], 0, s[4:5]
	v_lshl_add_u64 v[20:21], v[20:21], 0, v[8:9]
	global_store_dwordx4 v[20:21], v[16:19], off
	s_waitcnt lgkmcnt(0)
	s_nop 0
	v_mul_f32_e32 v16, v4, v22
	v_mul_f32_e32 v17, v5, v23
	v_cvt_pk_bf16_f32 v16, v16, v17
	ds_read2_b32 v[18:19], v14 offset0:146 offset1:211
	s_waitcnt lgkmcnt(0)
	v_mul_f32_e32 v17, v6, v18
	v_mul_f32_e32 v18, v7, v19
	v_cvt_pk_bf16_f32 v17, v17, v18
	ds_read2_b32 v[18:19], v15 offset0:20 offset1:85
	s_waitcnt lgkmcnt(0)
	v_mul_f32_e32 v18, v0, v18
	v_mul_f32_e32 v19, v1, v19
	v_cvt_pk_bf16_f32 v18, v18, v19
	ds_read2_b32 v[20:21], v15 offset0:150 offset1:215
	s_waitcnt lgkmcnt(0)
	v_mul_f32_e32 v19, v2, v20
	v_mul_f32_e32 v20, v3, v21
	v_cvt_pk_bf16_f32 v19, v19, v20
	v_add_u32_e32 v20, 16, v24
	v_ashrrev_i32_e32 v21, 31, v20
	v_mul_lo_u32 v22, s56, v21
	v_mul_lo_u32 v23, s57, v20
	v_mad_u64_u32 v[20:21], s[6:7], s56, v20, 0
	v_add3_u32 v21, v21, v22, v23
	ds_read2_b32 v[22:23], v14 offset0:24 offset1:89
	v_lshl_add_u64 v[20:21], v[20:21], 1, s[60:61]
	v_lshl_add_u64 v[20:21], v[20:21], 0, s[4:5]
	v_lshl_add_u64 v[20:21], v[20:21], 0, v[8:9]
	global_store_dwordx4 v[20:21], v[16:19], off
	s_waitcnt lgkmcnt(0)
	s_nop 0
	v_mul_f32_e32 v16, v4, v22
	v_mul_f32_e32 v17, v5, v23
	v_cvt_pk_bf16_f32 v16, v16, v17
	ds_read2_b32 v[18:19], v14 offset0:154 offset1:219
	s_waitcnt lgkmcnt(0)
	v_mul_f32_e32 v17, v6, v18
	v_mul_f32_e32 v18, v7, v19
	v_cvt_pk_bf16_f32 v17, v17, v18
	ds_read2_b32 v[18:19], v15 offset0:28 offset1:93
	s_waitcnt lgkmcnt(0)
	v_mul_f32_e32 v18, v0, v18
	v_mul_f32_e32 v19, v1, v19
	v_cvt_pk_bf16_f32 v18, v18, v19
	ds_read2_b32 v[20:21], v15 offset0:158 offset1:223
	s_waitcnt lgkmcnt(0)
; __device__ __forceinline__ unsigned cvt_pk_bf16(float lo, float hi) { unsigned r; asm volatile("v_cvt_pk_bf16_f32 %0, %1, %2" : "=v"(r) : "v"(lo), "v"(hi)); return r; }
; #define LAS __attribute__((address_space(3)))
; #define LDS_WAIT() asm volatile("s_waitcnt lgkmcnt(0)" ::: "memory")
; __device__ __forceinline__ void conv_store(const ConvItem& ci, LAS float* scr, int lane, const float (&v)[64]) {
;     ...
;     for (int j = 0; j < 8; ++j) { const int n = (lane >> 3) + 8 * j; const LAS float* s = scr + (8 * c) * 65 + n;
;         v4u o; o.x = cvt_pk_bf16(s[0 * 65] * s0[0], s[1 * 65] * s0[1]); o.y = cvt_pk_bf16(s[2 * 65] * s0[2], s[3 * 65] * s0[3]); o.z = cvt_pk_bf16(s[4 * 65] * s1[0], s[5 * 65] * s1[1]); o.w = cvt_pk_bf16(s[6 * 65] * s1[2], s[7 * 65] * s1[3]);
;         *(v4u*)(ci.dst + (size_t)(ci.drow0 + n) * ci.ldd + ci.k0 + 8 * c) = o; }
;     LDS_WAIT(); asm volatile("" ::: "memory");
; }
	v_mul_f32_e32 v19, v2, v20
	v_mul_f32_e32 v20, v3, v21
	v_cvt_pk_bf16_f32 v19, v19, v20
	v_add_u32_e32 v20, 24, v24
	v_ashrrev_i32_e32 v21, 31, v20
	v_mul_lo_u32 v22, s56, v21
	v_mul_lo_u32 v23, s57, v20
	v_mad_u64_u32 v[20:21], s[6:7], s56, v20, 0
	v_add3_u32 v21, v21, v22, v23
	ds_read2_b32 v[22:23], v14 offset0:32 offset1:97
	v_lshl_add_u64 v[20:21], v[20:21], 1, s[60:61]
	v_lshl_add_u64 v[20:21], v[20:21], 0, s[4:5]
	v_lshl_add_u64 v[20:21], v[20:21], 0, v[8:9]
	global_store_dwordx4 v[20:21], v[16:19], off
	s_waitcnt lgkmcnt(0)
	s_nop 0
	v_mul_f32_e32 v16, v4, v22
	v_mul_f32_e32 v17, v5, v23
	v_cvt_pk_bf16_f32 v16, v16, v17
	ds_read2_b32 v[18:19], v14 offset0:162 offset1:227
	s_waitcnt lgkmcnt(0)
	v_mul_f32_e32 v17, v6, v18
	v_mul_f32_e32 v18, v7, v19
	v_cvt_pk_bf16_f32 v17, v17, v18
	ds_read2_b32 v[18:19], v15 offset0:36 offset1:101
	s_waitcnt lgkmcnt(0)
	v_mul_f32_e32 v18, v0, v18
	v_mul_f32_e32 v19, v1, v19
	v_cvt_pk_bf16_f32 v18, v18, v19
	ds_read2_b32 v[20:21], v15 offset0:166 offset1:231
	s_waitcnt lgkmcnt(0)
	v_mul_f32_e32 v19, v2, v20
	v_mul_f32_e32 v20, v3, v21
	v_cvt_pk_bf16_f32 v19, v19, v20
	v_add_u32_e32 v20, 32, v24
	v_ashrrev_i32_e32 v21, 31, v20
	v_mul_lo_u32 v22, s56, v21
	v_mul_lo_u32 v23, s57, v20
	v_mad_u64_u32 v[20:21], s[6:7], s56, v20, 0
	v_add3_u32 v21, v21, v22, v23
	ds_read2_b32 v[22:23], v14 offset0:40 offset1:105
	v_lshl_add_u64 v[20:21], v[20:21], 1, s[60:61]
	v_lshl_add_u64 v[20:21], v[20:21], 0, s[4:5]
	v_lshl_add_u64 v[20:21], v[20:21], 0, v[8:9]
	global_store_dwordx4 v[20:21], v[16:19], off
	s_waitcnt lgkmcnt(0)
	s_nop 0
	v_mul_f32_e32 v16, v4, v22
	v_mul_f32_e32 v17, v5, v23
	v_cvt_pk_bf16_f32 v16, v16, v17
	ds_read2_b32 v[18:19], v14 offset0:170 offset1:235
	s_waitcnt lgkmcnt(0)
	v_mul_f32_e32 v17, v6, v18
	v_mul_f32_e32 v18, v7, v19
	v_cvt_pk_bf16_f32 v17, v17, v18
	ds_read2_b32 v[18:19], v15 offset0:44 offset1:109
	s_waitcnt lgkmcnt(0)
	v_mul_f32_e32 v18, v0, v18
	v_mul_f32_e32 v19, v1, v19
	v_cvt_pk_bf16_f32 v18, v18, v19
	ds_read2_b32 v[20:21], v15 offset0:174 offset1:239
	s_waitcnt lgkmcnt(0)
	v_mul_f32_e32 v19, v2, v20
	v_mul_f32_e32 v20, v3, v21
	v_cvt_pk_bf16_f32 v19, v19, v20
	v_add_u32_e32 v20, 40, v24
	v_ashrrev_i32_e32 v21, 31, v20
	v_mul_lo_u32 v22, s56, v21
	v_mul_lo_u32 v23, s57, v20
	v_mad_u64_u32 v[20:21], s[6:7], s56, v20, 0
	v_add3_u32 v21, v21, v22, v23
	ds_read2_b32 v[22:23], v14 offset0:48 offset1:113
	v_lshl_add_u64 v[20:21], v[20:21], 1, s[60:61]
	v_lshl_add_u64 v[20:21], v[20:21], 0, s[4:5]
	v_lshl_add_u64 v[20:21], v[20:21], 0, v[8:9]
	global_store_dwordx4 v[20:21], v[16:19], off
	s_waitcnt lgkmcnt(0)
	s_nop 0
	v_mul_f32_e32 v16, v4, v22
	v_mul_f32_e32 v17, v5, v23
	v_cvt_pk_bf16_f32 v16, v16, v17
	ds_read2_b32 v[18:19], v14 offset0:178 offset1:243
	s_waitcnt lgkmcnt(0)
	v_mul_f32_e32 v17, v6, v18
	v_mul_f32_e32 v18, v7, v19
	v_cvt_pk_bf16_f32 v17, v17, v18
	ds_read2_b32 v[18:19], v15 offset0:52 offset1:117
	s_waitcnt lgkmcnt(0)
	v_mul_f32_e32 v18, v0, v18
	v_mul_f32_e32 v19, v1, v19
	v_cvt_pk_bf16_f32 v18, v18, v19
	ds_read2_b32 v[20:21], v15 offset0:182 offset1:247
	s_waitcnt lgkmcnt(0)
	v_mul_f32_e32 v19, v2, v20
	v_mul_f32_e32 v20, v3, v21
	v_cvt_pk_bf16_f32 v19, v19, v20
	v_add_u32_e32 v20, 48, v24
	v_ashrrev_i32_e32 v21, 31, v20
	v_mul_lo_u32 v22, s56, v21
	v_mul_lo_u32 v23, s57, v20
	v_mad_u64_u32 v[20:21], s[6:7], s56, v20, 0
	v_add3_u32 v21, v21, v22, v23
	ds_read2_b32 v[22:23], v14 offset0:56 offset1:121
	v_lshl_add_u64 v[20:21], v[20:21], 1, s[60:61]
	v_lshl_add_u64 v[20:21], v[20:21], 0, s[4:5]
	v_lshl_add_u64 v[20:21], v[20:21], 0, v[8:9]
	global_store_dwordx4 v[20:21], v[16:19], off
	s_waitcnt lgkmcnt(0)
	v_mul_f32_e32 v4, v4, v22
	v_mul_f32_e32 v5, v5, v23
	v_cvt_pk_bf16_f32 v4, v4, v5
	ds_read2_b32 v[16:17], v14 offset0:186 offset1:251
	s_waitcnt lgkmcnt(0)
	v_mul_f32_e32 v5, v6, v16
	v_mul_f32_e32 v6, v7, v17
	v_cvt_pk_bf16_f32 v5, v5, v6
	ds_read2_b32 v[6:7], v15 offset0:60 offset1:125
	s_waitcnt lgkmcnt(0)
	v_mul_f32_e32 v0, v0, v6
	v_mul_f32_e32 v1, v1, v7
	v_cvt_pk_bf16_f32 v6, v0, v1
	ds_read2_b32 v[0:1], v15 offset0:190 offset1:255
	s_waitcnt lgkmcnt(0)
	v_mul_f32_e32 v0, v2, v0
	v_mul_f32_e32 v1, v3, v1
	v_cvt_pk_bf16_f32 v7, v0, v1
	v_add_u32_e32 v0, 56, v24
	v_ashrrev_i32_e32 v1, 31, v0
	v_mul_lo_u32 v2, s56, v1
	v_mul_lo_u32 v3, s57, v0
	v_mad_u64_u32 v[0:1], s[6:7], s56, v0, 0
	v_add3_u32 v1, v1, v2, v3
	v_lshl_add_u64 v[0:1], v[0:1], 1, s[60:61]
	v_lshl_add_u64 v[0:1], v[0:1], 0, s[4:5]
	v_lshl_add_u64 v[0:1], v[0:1], 0, v[8:9]
	global_store_dwordx4 v[0:1], v[4:7], off
	s_waitcnt lgkmcnt(0)
	s_cbranch_scc0 .Lcvp30_ret

; #define LAS __attribute__((address_space(3)))
; #define IN(k) in_range(lo, hi, (k))
; __global__ void __launch_bounds__(NWAVES * 64, 2) mk_fwd(Args args) {
;     ...
;         if (EN(0) && IN(pb + 0)) {
;             PH_LOCALS
;             LAS float* scr = (LAS float*)(lds + RING_OFF + wave * 16640);   static_assert(8 * 16640 <= LDSCTL_OFF, "converter scratch below the LDS control words");
;             constexpr int I_UP = (D / 64) * (NUP / 64), I_DN = (DFF / 64) * (D / 64), I_IN = (D / 64) * (DINP / 64), I_GLU = 16 * 16, I_L = 4 * 16, I_V1 = 16 * 4, I_V2 = 4 * 16,
;                           I_BS5 = 16 * 32, I_BAT = 8 * 32, I_BRW = 16 * 32, I_OUT = 32 * 32;
;             constexpr int NITEMS = 2 * I_UP + 2 * I_DN + I_IN + I_GLU + 3 * I_L + I_V1 + I_V2 + I_BS5 + I_BAT + I_BRW + I_OUT;
;             const int lv = l > 0 ? l - 1 : 0;
;     ...
;             for (int it = gw; it < NITEMS; it += NGW) {
;                 ConvItem ca; CONV_DESC(ca, it);
.LBB0_1151:
	v_readlane_b32 s99, v254, 35
	v_readlane_b32 s98, v254, 38
	s_nop 3
	s_cmp_lt_u32 s99, 96
	s_cbranch_scc1 .Lcvskip_p13
	s_cmp_gt_u32 s98, 2
	s_cbranch_scc1 .Lcvskip_p13
	v_mov_b32_e32 v250, v254
	v_mov_b32_e32 v251, v255
	v_writelane_b32 v252, s0, 0
	s_nop 0
	v_writelane_b32 v252, s1, 1
	s_nop 0
	v_writelane_b32 v252, s2, 2
	s_nop 0
	v_writelane_b32 v252, s3, 3
	s_nop 0
	v_writelane_b32 v252, s4, 4
	s_nop 0
	v_writelane_b32 v252, s5, 5
	s_nop 0
	v_writelane_b32 v252, s6, 6
	s_nop 0
	v_writelane_b32 v252, s7, 7
	s_nop 0
	v_writelane_b32 v252, s8, 8
	s_nop 0
	v_writelane_b32 v252, s9, 9
	s_nop 0
	v_writelane_b32 v252, s10, 10
	s_nop 0
	v_writelane_b32 v252, s11, 11
	s_nop 0
	v_writelane_b32 v252, s12, 12
	s_nop 0
	v_writelane_b32 v252, s13, 13
	s_nop 0
	v_writelane_b32 v252, s14, 14
	s_nop 0
	v_writelane_b32 v252, s15, 15
	s_nop 0
	v_writelane_b32 v252, s16, 16
	s_nop 0
	v_writelane_b32 v252, s17, 17
	s_nop 0
	v_writelane_b32 v252, s18, 18
	s_nop 0
	v_writelane_b32 v252, s19, 19
	s_nop 0
	v_writelane_b32 v252, s20, 20
	s_nop 0
	v_writelane_b32 v252, s21, 21
	s_nop 0
	v_writelane_b32 v252, s22, 22
	s_nop 0
	v_writelane_b32 v252, s23, 23
	s_nop 0
	v_writelane_b32 v252, s24, 24
	s_nop 0
	v_writelane_b32 v252, s25, 25
	s_nop 0
	v_writelane_b32 v252, s26, 26
	s_nop 0
	v_writelane_b32 v252, s27, 27
	s_nop 0
	v_writelane_b32 v252, s28, 28
	s_nop 0
	v_writelane_b32 v252, s29, 29
	s_nop 0
	v_writelane_b32 v252, s30, 30
	s_nop 0
	v_writelane_b32 v252, s31, 31
	s_nop 0
	v_writelane_b32 v252, s32, 32
	s_nop 0
	v_writelane_b32 v252, s33, 33
	s_nop 0
	v_writelane_b32 v252, s34, 34
	s_nop 0
	v_writelane_b32 v252, s35, 35
	s_nop 0
	v_writelane_b32 v252, s36, 36
	s_nop 0
	v_writelane_b32 v252, s37, 37
	s_nop 0
	v_writelane_b32 v252, s38, 38
	s_nop 0
	v_writelane_b32 v252, s39, 39
	s_nop 0
	v_writelane_b32 v252, s40, 40
	s_nop 0
	v_writelane_b32 v252, s41, 41
	s_nop 0
	v_writelane_b32 v252, s42, 42
	s_nop 0
	v_writelane_b32 v252, s43, 43
	s_nop 0
	v_writelane_b32 v252, s44, 44
	s_nop 0
	v_writelane_b32 v252, s45, 45
	s_nop 0
	v_writelane_b32 v252, s46, 46
	s_nop 0
	v_writelane_b32 v252, s47, 47
	s_nop 0
	v_writelane_b32 v252, s48, 48
	s_nop 0
	v_writelane_b32 v252, s49, 49
	s_nop 0
	v_writelane_b32 v252, s50, 50
	s_nop 0
	v_writelane_b32 v252, s51, 51
	s_nop 0
	v_writelane_b32 v252, s52, 52
	s_nop 0
	v_writelane_b32 v252, s53, 53
	s_nop 0
	v_writelane_b32 v252, s54, 54
	s_nop 0
	v_writelane_b32 v252, s55, 55
	s_nop 0
	v_writelane_b32 v252, s56, 56
	s_nop 0
	v_writelane_b32 v252, s57, 57
	s_nop 0
	v_writelane_b32 v252, s58, 58
	s_nop 0
	v_writelane_b32 v252, s59, 59
	s_nop 0
	v_writelane_b32 v252, s60, 60
	s_nop 0
	v_writelane_b32 v252, s61, 61
	s_nop 0
	v_writelane_b32 v252, s62, 62
	s_nop 0
	v_writelane_b32 v252, s63, 63
	s_nop 0
	v_writelane_b32 v253, s64, 0
	s_nop 0
	v_writelane_b32 v253, s65, 1
	s_nop 0
	v_writelane_b32 v253, s66, 2
	s_nop 0
	v_writelane_b32 v253, s67, 3
	s_nop 0
	v_writelane_b32 v253, s68, 4
	s_nop 0
	v_writelane_b32 v253, s69, 5
	s_nop 0
	v_writelane_b32 v253, s70, 6
	s_nop 0
	v_writelane_b32 v253, s71, 7
	s_nop 0
	v_writelane_b32 v253, s72, 8
	s_nop 0
	v_writelane_b32 v253, s73, 9
	s_nop 0
	v_writelane_b32 v253, s74, 10
	s_nop 0
	v_writelane_b32 v253, s75, 11
	s_nop 0
	v_writelane_b32 v253, s76, 12
	s_nop 0
	v_writelane_b32 v253, s77, 13
	s_nop 0
	v_writelane_b32 v253, s78, 14
	s_nop 0
	v_writelane_b32 v253, s79, 15
	s_nop 0
	v_writelane_b32 v253, s80, 16
	s_nop 0
	v_writelane_b32 v253, s81, 17
	s_nop 0
	v_writelane_b32 v253, s82, 18
	s_nop 0
	v_writelane_b32 v253, s83, 19
	s_nop 0
	v_writelane_b32 v253, s84, 20
	s_nop 0
	v_writelane_b32 v253, s85, 21
	s_nop 0
	v_writelane_b32 v253, s86, 22
	s_nop 0
	v_writelane_b32 v253, s87, 23
	s_nop 0
	v_writelane_b32 v253, s88, 24
	s_nop 0
	v_writelane_b32 v253, s89, 25
	s_nop 0
	v_writelane_b32 v253, s90, 26
	s_nop 0
	v_writelane_b32 v253, s91, 27
	s_nop 0
	v_writelane_b32 v253, s92, 28
	s_nop 0
	v_writelane_b32 v253, s93, 29
	s_nop 0
	v_writelane_b32 v253, s94, 30
	s_nop 0
	v_writelane_b32 v253, s95, 31
	s_nop 0
	v_writelane_b32 v253, s96, 32
	s_nop 0
	v_writelane_b32 v253, s97, 33
	s_nop 0
	v_writelane_b32 v253, vcc_lo, 34
	s_nop 0
	v_writelane_b32 v253, vcc_hi, 35
	s_nop 1
	v_readlane_b32 s84, v254, 35
	s_nop 3
	v_readlane_b32 s0, v254, 8
	v_readlane_b32 s4, v254, 10
	v_readlane_b32 s1, v254, 9
	v_mbcnt_lo_u32_b32 v11, -1, 0
	v_mbcnt_hi_u32_b32 v11, -1, v11
	s_load_dword s6, s[0:1], 0x0
	s_mov_b32 s3, s84
	s_waitcnt lgkmcnt(0)
	s_movk_i32 s6, 160
	s_lshl_b32 s3, s3, 3
	v_readlane_b32 s0, v254, 0
	s_add_i32 s3, s3, s4
	s_add_i32 s3, s3, 0x2800
	v_readlane_b32 s1, v254, 1
	s_cmpk_gt_i32 s3, 18687
	s_cbranch_scc1 .Lcvp130_ret
; __global__ void __launch_bounds__(NWAVES * 64, 2) mk_fwd(Args args) {
;     ...
;             for (int it = gw; it < NITEMS; it += NGW) {
;                 ConvItem ca; CONV_DESC(ca, it);
	s_load_dwordx2 s[8:9], s[0:1], 0x138
	v_readlane_b32 s14, v254, 38
	s_nop 0
	s_add_i32 s14, s14, 1
	s_mulk_i32 s4, 0x4100
	s_add_i32 s7, s4, 0
	v_sub_u32_e64 v0, s14, 1 clamp
	s_lshl_b32 s33, s6, 3
	v_readfirstlane_b32 s4, v0
	s_lshl_b32 s96, s4, 16
	s_waitcnt lgkmcnt(0)
	s_add_u32 s4, s8, 0x22800000
	s_addc_u32 s5, s9, 0
	v_writelane_b32 v254, s4, 39
	s_mov_b32 s15, s97
	v_and_b32_e32 v0, 7, v11
	v_writelane_b32 v254, s5, 40
	s_add_u32 s4, s8, 0x22780000
	s_addc_u32 s5, s9, 0
	v_writelane_b32 v254, s4, 41
	v_ashrrev_i32_e32 v13, 3, v11
	v_lshlrev_b32_e32 v10, 3, v0
	v_writelane_b32 v254, s5, 42
	s_lshl_b32 s4, s14, 18
	s_add_u32 s10, s8, 0x22700000
	s_addc_u32 s11, s9, 0
	v_writelane_b32 v254, s10, 43
	s_mov_b32 s5, s97
	v_mul_u32_u24_e32 v0, 0x820, v0
	v_writelane_b32 v254, s11, 44
	s_mul_i32 s10, s14, 0x18000
	s_mov_b32 s11, s97
	v_writelane_b32 v254, s10, 45
	v_lshlrev_b32_e32 v1, 2, v13
	v_lshl_add_u32 v12, v11, 2, s7
	v_writelane_b32 v254, s11, 46
	s_add_u32 s10, s8, 0x22680000
	s_addc_u32 s11, s9, 0
	v_writelane_b32 v254, s10, 47
	v_add3_u32 v14, s7, v0, v1
	s_mov_b32 s41, s97
	v_writelane_b32 v254, s11, 48
	s_add_u32 s10, s8, 0x22600000
	s_addc_u32 s11, s9, 0
	v_writelane_b32 v254, s10, 49
	s_nop 1
	v_writelane_b32 v254, s11, 50
	s_lshl_b32 s10, s14, 20
	s_mov_b32 s11, s97
	v_writelane_b32 v254, s10, 51
	s_nop 1
	v_writelane_b32 v254, s11, 52
	s_add_u32 s10, s8, 0x22400000
	s_addc_u32 s11, s9, 0
	v_writelane_b32 v254, s10, 53
	s_nop 1
	v_writelane_b32 v254, s11, 54
	s_lshl_b32 s10, s14, 21
	s_mov_b32 s11, s97
	v_writelane_b32 v254, s10, 55
	s_nop 1
	v_writelane_b32 v254, s11, 56
	s_add_u32 s10, s8, 0x22e80000
	s_addc_u32 s11, s9, 0
	v_writelane_b32 v254, s10, 57
	s_nop 1
	v_writelane_b32 v254, s11, 58
	s_add_u32 s10, s8, 0x27b80000
	s_addc_u32 s11, s9, 0
	v_writelane_b32 v254, s10, 59
	s_nop 1
	v_writelane_b32 v254, s11, 60
	s_add_u32 s10, s8, 0x22880000
	s_addc_u32 s11, s9, 0
	v_writelane_b32 v254, s10, 61
	s_nop 1
	v_writelane_b32 v254, s11, 62
	s_lshl_b32 s10, s14, 22
	s_add_u32 s12, s8, 0x23280000
	s_addc_u32 s13, s9, 0
	v_writelane_b32 v254, s12, 63
	s_mov_b32 s11, s97
	s_nop 0
	v_writelane_b32 v255, s13, 0
	s_mul_i32 s12, s14, 0xac0000
	s_mov_b32 s13, s97
	v_writelane_b32 v255, s12, 1
	s_nop 1
	v_writelane_b32 v255, s13, 2
	s_add_u32 s12, s8, 0x26580000
	s_addc_u32 s13, s9, 0
	v_writelane_b32 v255, s12, 3
	s_nop 1
	v_writelane_b32 v255, s13, 4
	s_add_u32 s12, s8, 0x1d200000
	s_addc_u32 s13, s9, 0
	s_lshl_b32 s40, s14, 11
	v_writelane_b32 v255, s12, 5
	s_add_u32 s16, s8, 0x1e800000
	s_addc_u32 s17, s9, 0
	v_writelane_b32 v255, s13, 6
	v_writelane_b32 v255, s16, 7
	s_mul_i32 s12, s14, 0x1de0000
	s_mul_i32 s14, s14, 0x1580000
	v_writelane_b32 v255, s17, 8
	v_writelane_b32 v255, s14, 9
	s_mov_b32 s13, s97
	s_nop 0
	v_writelane_b32 v255, s15, 10
	s_add_u32 s14, s8, 0x23a80000
	s_addc_u32 s15, s9, 0
	v_writelane_b32 v255, s14, 11
	s_add_u32 s8, s8, 0x1a700000
	s_addc_u32 s9, s9, 0
	v_writelane_b32 v255, s15, 12
	v_writelane_b32 v255, s8, 13
	s_lshl_b64 s[4:5], s[4:5], 2
	s_lshl_b32 s7, s3, 4
	v_writelane_b32 v255, s9, 14
	v_writelane_b32 v255, s4, 15
	s_add_i32 s72, s7, 0xc00
	s_lshl_b32 s7, s3, 1
	v_writelane_b32 v255, s5, 16
	s_lshl_b64 s[4:5], s[10:11], 2
	v_writelane_b32 v255, s4, 17
	s_lshl_b32 s66, s3, 6
	s_lshl_b32 s67, s6, 9
	v_writelane_b32 v255, s5, 18
	s_lshl_b64 s[4:5], s[12:13], 2
	v_writelane_b32 v255, s4, 19
	s_lshl_b32 s68, s3, 5
	s_lshl_b32 s69, s6, 8
	v_writelane_b32 v255, s5, 20
	v_writelane_b32 v255, s80, 21
	s_lshl_b32 s70, s3, 2
	s_lshl_b32 s71, s6, 5
	v_writelane_b32 v255, s81, 22
	v_writelane_b32 v255, s82, 23
	s_lshl_b32 s73, s6, 7
	s_add_i32 s74, s7, 0x13500
	s_lshl_b32 s75, s6, 4
	v_writelane_b32 v255, s83, 24
	s_branch .Lcvp130_31

; __device__ __forceinline__ void conv_load(const ConvItem& ci, int lane, float (&v)[64]) {
;     ...
;     for (int i = 0; i < 64; ++i) { const int k = ci.k0 + i, kk = k < kmax ? k : kmax; v[i] = __builtin_nontemporal_load(base + (size_t)kk * ci.ldw); }
; #pragma unroll
;     for (int i = 0; i < 64; ++i) v[i] = (okc && (ci.k0 + i) < ci.Ksrc) ? v[i] : 0.f;
.Lcvp130_30:
	s_cmp_lt_i32 s58, s76
	s_cselect_b64 s[4:5], -1, 0
	s_and_b64 s[4:5], vcc, s[4:5]
	s_cmp_lt_i32 s64, s76
	s_waitcnt vmcnt(62)
	v_cndmask_b32_e64 v21, 0, v21, s[4:5]
	s_cselect_b64 s[4:5], -1, 0
	s_and_b64 s[4:5], vcc, s[4:5]
	s_cmp_lt_i32 s65, s76
	v_cndmask_b32_e64 v20, 0, v20, s[4:5]
	s_cselect_b64 s[4:5], -1, 0
	s_and_b64 s[4:5], vcc, s[4:5]
	s_cmp_lt_i32 s78, s76
	s_waitcnt vmcnt(61)
	v_cndmask_b32_e64 v19, 0, v19, s[4:5]
	s_cselect_b64 s[4:5], -1, 0
	s_and_b64 s[4:5], vcc, s[4:5]
	s_cmp_lt_i32 s79, s76
	s_waitcnt vmcnt(60)
	v_cndmask_b32_e64 v18, 0, v18, s[4:5]
	s_cselect_b64 s[4:5], -1, 0
	s_and_b64 s[4:5], vcc, s[4:5]
	s_cmp_lt_i32 s80, s76
	s_waitcnt vmcnt(59)
	v_cndmask_b32_e64 v17, 0, v17, s[4:5]
	s_cselect_b64 s[4:5], -1, 0
	s_and_b64 s[4:5], vcc, s[4:5]
	s_cmp_lt_i32 s81, s76
	s_waitcnt vmcnt(58)
	v_cndmask_b32_e64 v16, 0, v16, s[4:5]
	s_cselect_b64 s[4:5], -1, 0
	s_and_b64 s[4:5], vcc, s[4:5]
	s_cmp_lt_i32 s82, s76
	s_waitcnt vmcnt(57)
	v_cndmask_b32_e64 v15, 0, v15, s[4:5]
	s_cselect_b64 s[4:5], -1, 0
	s_and_b64 s[4:5], vcc, s[4:5]
	s_cmp_lt_i32 s83, s76
	s_waitcnt vmcnt(56)
	v_cndmask_b32_e64 v8, 0, v8, s[4:5]
	s_cselect_b64 s[4:5], -1, 0
	s_and_b64 s[4:5], vcc, s[4:5]
	s_cmp_lt_i32 s85, s76
	s_waitcnt vmcnt(55)
	v_cndmask_b32_e64 v29, 0, v29, s[4:5]
	s_cselect_b64 s[4:5], -1, 0
	s_and_b64 s[4:5], vcc, s[4:5]
	s_cmp_lt_i32 s86, s76
	s_waitcnt vmcnt(54)
	v_cndmask_b32_e64 v28, 0, v28, s[4:5]
	s_cselect_b64 s[4:5], -1, 0
	s_and_b64 s[4:5], vcc, s[4:5]
	s_cmp_lt_i32 s87, s76
	s_waitcnt vmcnt(53)
	v_cndmask_b32_e64 v27, 0, v27, s[4:5]
	s_cselect_b64 s[4:5], -1, 0
	s_and_b64 s[4:5], vcc, s[4:5]
	s_cmp_lt_i32 s88, s76
	s_waitcnt vmcnt(52)
	v_cndmask_b32_e64 v26, 0, v26, s[4:5]
	s_cselect_b64 s[4:5], -1, 0
	s_and_b64 s[4:5], vcc, s[4:5]
	s_cmp_lt_i32 s89, s76
	s_waitcnt vmcnt(51)
	v_cndmask_b32_e64 v25, 0, v25, s[4:5]
	s_cselect_b64 s[4:5], -1, 0
	s_and_b64 s[4:5], vcc, s[4:5]
	s_cmp_lt_i32 s90, s76
	s_waitcnt vmcnt(50)
	v_cndmask_b32_e64 v24, 0, v24, s[4:5]
	s_cselect_b64 s[4:5], -1, 0
	s_and_b64 s[4:5], vcc, s[4:5]
	s_cmp_lt_i32 s92, s76
	s_waitcnt vmcnt(49)
	v_cndmask_b32_e64 v23, 0, v23, s[4:5]
	s_cselect_b64 s[4:5], -1, 0
	s_and_b64 s[4:5], vcc, s[4:5]
	s_cmp_lt_i32 s93, s76
	s_waitcnt vmcnt(48)
	v_cndmask_b32_e64 v22, 0, v22, s[4:5]
	s_cselect_b64 s[4:5], -1, 0
	s_and_b64 s[4:5], vcc, s[4:5]
	s_cmp_lt_i32 s94, s76
	s_waitcnt vmcnt(47)
	v_cndmask_b32_e64 v37, 0, v37, s[4:5]
	s_cselect_b64 s[4:5], -1, 0
	s_and_b64 s[4:5], vcc, s[4:5]
	s_cmp_lt_i32 s95, s76
	s_waitcnt vmcnt(46)
	v_cndmask_b32_e64 v36, 0, v36, s[4:5]
	s_cselect_b64 s[4:5], -1, 0
	s_and_b64 s[4:5], vcc, s[4:5]
	s_cmp_lt_i32 s50, s76
	s_waitcnt vmcnt(45)
	v_cndmask_b32_e64 v35, 0, v35, s[4:5]
	s_cselect_b64 s[4:5], -1, 0
	s_and_b64 s[4:5], vcc, s[4:5]
	s_cmp_lt_i32 s51, s76
	s_waitcnt vmcnt(44)
	v_cndmask_b32_e64 v34, 0, v34, s[4:5]
	s_cselect_b64 s[4:5], -1, 0
	s_and_b64 s[4:5], vcc, s[4:5]
	s_cmp_lt_i32 s52, s76
	s_waitcnt vmcnt(43)
	v_cndmask_b32_e64 v33, 0, v33, s[4:5]
	s_cselect_b64 s[4:5], -1, 0
	s_and_b64 s[4:5], vcc, s[4:5]
	s_cmp_lt_i32 s53, s76
	s_waitcnt vmcnt(42)
	v_cndmask_b32_e64 v32, 0, v32, s[4:5]
	s_cselect_b64 s[4:5], -1, 0
	s_and_b64 s[4:5], vcc, s[4:5]
	s_cmp_lt_i32 s6, s76
	s_waitcnt vmcnt(41)
	v_cndmask_b32_e64 v31, 0, v31, s[4:5]
	s_cselect_b64 s[4:5], -1, 0
	s_and_b64 s[4:5], vcc, s[4:5]
	s_cmp_lt_i32 s7, s76
	s_waitcnt vmcnt(40)
	v_cndmask_b32_e64 v30, 0, v30, s[4:5]
	s_cselect_b64 s[4:5], -1, 0
	s_and_b64 s[4:5], vcc, s[4:5]
	s_cmp_lt_i32 s8, s76
	s_waitcnt vmcnt(39)
	v_cndmask_b32_e64 v45, 0, v45, s[4:5]
	s_cselect_b64 s[4:5], -1, 0
	s_and_b64 s[4:5], vcc, s[4:5]
	s_cmp_lt_i32 s9, s76
	s_waitcnt vmcnt(38)
	v_cndmask_b32_e64 v44, 0, v44, s[4:5]
	s_cselect_b64 s[4:5], -1, 0
	s_and_b64 s[4:5], vcc, s[4:5]
	s_cmp_lt_i32 s10, s76
	s_waitcnt vmcnt(37)
	v_cndmask_b32_e64 v43, 0, v43, s[4:5]
	s_cselect_b64 s[4:5], -1, 0
	s_and_b64 s[4:5], vcc, s[4:5]
	s_cmp_lt_i32 s11, s76
	s_waitcnt vmcnt(36)
	v_cndmask_b32_e64 v42, 0, v42, s[4:5]
	s_cselect_b64 s[4:5], -1, 0
	s_and_b64 s[4:5], vcc, s[4:5]
	s_cmp_lt_i32 s14, s76
	s_waitcnt vmcnt(35)
	v_cndmask_b32_e64 v41, 0, v41, s[4:5]
	s_cselect_b64 s[4:5], -1, 0
	s_and_b64 s[4:5], vcc, s[4:5]
	s_cmp_lt_i32 s15, s76
	s_waitcnt vmcnt(34)
	v_cndmask_b32_e64 v40, 0, v40, s[4:5]
	s_cselect_b64 s[4:5], -1, 0
	s_and_b64 s[4:5], vcc, s[4:5]
	s_cmp_lt_i32 s16, s76
	s_waitcnt vmcnt(33)
	v_cndmask_b32_e64 v39, 0, v39, s[4:5]
	s_cselect_b64 s[4:5], -1, 0
	s_and_b64 s[4:5], vcc, s[4:5]
	s_cmp_lt_i32 s17, s76
	s_waitcnt vmcnt(32)
	v_cndmask_b32_e64 v38, 0, v38, s[4:5]
	s_cselect_b64 s[4:5], -1, 0
	s_and_b64 s[4:5], vcc, s[4:5]
	s_cmp_lt_i32 s12, s76
	s_waitcnt vmcnt(31)
	v_cndmask_b32_e64 v53, 0, v53, s[4:5]
	s_cselect_b64 s[4:5], -1, 0
	s_and_b64 s[4:5], vcc, s[4:5]
	s_cmp_lt_i32 s13, s76
	s_waitcnt vmcnt(30)
	v_cndmask_b32_e64 v52, 0, v52, s[4:5]
	s_cselect_b64 s[4:5], -1, 0
	s_and_b64 s[4:5], vcc, s[4:5]
	s_cmp_lt_i32 s20, s76
	s_waitcnt vmcnt(29)
	v_cndmask_b32_e64 v51, 0, v51, s[4:5]
	s_cselect_b64 s[4:5], -1, 0
	s_and_b64 s[4:5], vcc, s[4:5]
	s_cmp_lt_i32 s21, s76
	s_waitcnt vmcnt(28)
	v_cndmask_b32_e64 v50, 0, v50, s[4:5]
	s_cselect_b64 s[4:5], -1, 0
	s_and_b64 s[4:5], vcc, s[4:5]
	s_cmp_lt_i32 s24, s76
	s_waitcnt vmcnt(27)
	v_cndmask_b32_e64 v49, 0, v49, s[4:5]
	s_cselect_b64 s[4:5], -1, 0
	s_and_b64 s[4:5], vcc, s[4:5]
	s_cmp_lt_i32 s25, s76
	s_waitcnt vmcnt(26)
	v_cndmask_b32_e64 v48, 0, v48, s[4:5]
	s_cselect_b64 s[4:5], -1, 0
	s_and_b64 s[4:5], vcc, s[4:5]
	s_cmp_lt_i32 s26, s76
	s_waitcnt vmcnt(25)
	v_cndmask_b32_e64 v47, 0, v47, s[4:5]
	s_cselect_b64 s[4:5], -1, 0
	s_and_b64 s[4:5], vcc, s[4:5]
	s_cmp_lt_i32 s27, s76
	s_waitcnt vmcnt(24)
; #define LAS __attribute__((address_space(3)))
; #define LDS_WAIT() asm volatile("s_waitcnt lgkmcnt(0)" ::: "memory")
; __device__ __forceinline__ void conv_load(const ConvItem& ci, int lane, float (&v)[64]) {
;     ...
;     for (int i = 0; i < 64; ++i) v[i] = (okc && (ci.k0 + i) < ci.Ksrc) ? v[i] : 0.f;
; }
; __device__ __forceinline__ void conv_store(const ConvItem& ci, LAS float* scr, int lane, const float (&v)[64]) {
;     const int c = lane & 7;
;     f32x4 s0 = {1.f, 1.f, 1.f, 1.f}, s1 = s0;
;     if (ci.ks) { const int kb = ci.k0 + 8 * c < ci.Ksrc - 8 ? ci.k0 + 8 * c : ci.Ksrc - 8; s0 = *(const f32x4*)(ci.ks + kb); s1 = *(const f32x4*)(ci.ks + kb + 4); }
; #pragma unroll
;     for (int i = 0; i < 64; ++i) scr[i * 65 + lane] = v[i];
;     LDS_WAIT(); asm volatile("" ::: "memory");
	v_cndmask_b32_e64 v46, 0, v46, s[4:5]
	s_cselect_b64 s[4:5], -1, 0
	s_and_b64 s[4:5], vcc, s[4:5]
	s_cmp_lt_i32 s18, s76
	s_waitcnt vmcnt(23)
	v_cndmask_b32_e64 v61, 0, v61, s[4:5]
	s_cselect_b64 s[4:5], -1, 0
	s_and_b64 s[4:5], vcc, s[4:5]
	s_cmp_lt_i32 s19, s76
	s_waitcnt vmcnt(22)
	v_cndmask_b32_e64 v60, 0, v60, s[4:5]
	s_cselect_b64 s[4:5], -1, 0
	s_and_b64 s[4:5], vcc, s[4:5]
	s_cmp_lt_i32 s28, s76
	s_waitcnt vmcnt(21)
	v_cndmask_b32_e64 v59, 0, v59, s[4:5]
	s_cselect_b64 s[4:5], -1, 0
	s_and_b64 s[4:5], vcc, s[4:5]
	s_cmp_lt_i32 s29, s76
	s_waitcnt vmcnt(20)
	v_cndmask_b32_e64 v58, 0, v58, s[4:5]
	s_cselect_b64 s[4:5], -1, 0
	s_and_b64 s[4:5], vcc, s[4:5]
	s_cmp_lt_i32 s22, s76
	s_waitcnt vmcnt(19)
	v_cndmask_b32_e64 v57, 0, v57, s[4:5]
	s_cselect_b64 s[4:5], -1, 0
	s_and_b64 s[4:5], vcc, s[4:5]
	s_cmp_lt_i32 s23, s76
	s_waitcnt vmcnt(18)
	v_cndmask_b32_e64 v56, 0, v56, s[4:5]
	s_cselect_b64 s[4:5], -1, 0
	s_and_b64 s[4:5], vcc, s[4:5]
	s_cmp_lt_i32 s30, s76
	s_waitcnt vmcnt(17)
	v_cndmask_b32_e64 v55, 0, v55, s[4:5]
	s_cselect_b64 s[4:5], -1, 0
	s_and_b64 s[4:5], vcc, s[4:5]
	s_cmp_lt_i32 s31, s76
	s_waitcnt vmcnt(16)
	v_cndmask_b32_e64 v54, 0, v54, s[4:5]
	s_cselect_b64 s[4:5], -1, 0
	s_and_b64 s[4:5], vcc, s[4:5]
	s_cmp_lt_i32 s36, s76
	s_waitcnt vmcnt(15)
	v_cndmask_b32_e64 v70, 0, v70, s[4:5]
	s_cselect_b64 s[4:5], -1, 0
	s_and_b64 s[4:5], vcc, s[4:5]
	s_cmp_lt_i32 s37, s76
	s_waitcnt vmcnt(14)
	v_cndmask_b32_e64 v69, 0, v69, s[4:5]
	s_cselect_b64 s[4:5], -1, 0
	s_and_b64 s[4:5], vcc, s[4:5]
	s_cmp_lt_i32 s38, s76
	s_waitcnt vmcnt(13)
	v_cndmask_b32_e64 v68, 0, v68, s[4:5]
	s_cselect_b64 s[4:5], -1, 0
	s_and_b64 s[4:5], vcc, s[4:5]
	s_cmp_lt_i32 s39, s76
	s_waitcnt vmcnt(12)
	v_cndmask_b32_e64 v67, 0, v67, s[4:5]
	s_cselect_b64 s[4:5], -1, 0
	s_and_b64 s[4:5], vcc, s[4:5]
	s_cmp_lt_i32 s34, s76
	s_waitcnt vmcnt(11)
	v_cndmask_b32_e64 v66, 0, v66, s[4:5]
	s_cselect_b64 s[4:5], -1, 0
	s_and_b64 s[4:5], vcc, s[4:5]
	s_cmp_lt_i32 s35, s76
	s_waitcnt vmcnt(10)
	v_cndmask_b32_e64 v64, 0, v64, s[4:5]
	s_cselect_b64 s[4:5], -1, 0
	s_and_b64 s[4:5], vcc, s[4:5]
	s_cmp_lt_i32 s42, s76
	s_waitcnt vmcnt(9)
	v_cndmask_b32_e64 v63, 0, v63, s[4:5]
	s_cselect_b64 s[4:5], -1, 0
	s_and_b64 s[4:5], vcc, s[4:5]
	s_cmp_lt_i32 s43, s76
	s_waitcnt vmcnt(8)
	v_cndmask_b32_e64 v62, 0, v62, s[4:5]
	s_cselect_b64 s[4:5], -1, 0
	s_and_b64 s[4:5], vcc, s[4:5]
	s_cmp_lt_i32 s54, s76
	s_waitcnt vmcnt(7)
	v_cndmask_b32_e64 v65, 0, v65, s[4:5]
	s_cselect_b64 s[4:5], -1, 0
	s_and_b64 s[4:5], vcc, s[4:5]
	s_cmp_lt_i32 s55, s76
	s_waitcnt vmcnt(6)
	v_cndmask_b32_e64 v74, 0, v74, s[4:5]
	s_cselect_b64 s[4:5], -1, 0
	s_and_b64 s[4:5], vcc, s[4:5]
	s_cmp_lt_i32 s46, s76
	ds_write2_b32 v12, v21, v20 offset1:65
	ds_write2_b32 v12, v19, v18 offset0:130 offset1:195
	v_add_u32_e32 v18, 0x400, v12
	s_waitcnt vmcnt(5)
	v_cndmask_b32_e64 v73, 0, v73, s[4:5]
	s_cselect_b64 s[4:5], -1, 0
	ds_write2_b32 v18, v17, v16 offset0:4 offset1:69
	ds_write2_b32 v18, v15, v8 offset0:134 offset1:199
	v_add_u32_e32 v8, 0x800, v12
	s_and_b64 s[4:5], vcc, s[4:5]
	ds_write2_b32 v8, v29, v28 offset0:8 offset1:73
	ds_write2_b32 v8, v27, v26 offset0:138 offset1:203
	v_add_u32_e32 v8, 0xc00, v12
	s_cmp_lt_i32 s47, s76
	ds_write2_b32 v8, v25, v24 offset0:12 offset1:77
	ds_write2_b32 v8, v23, v22 offset0:142 offset1:207
	v_add_u32_e32 v8, 0x1000, v12
	s_waitcnt vmcnt(4)
	v_cndmask_b32_e64 v72, 0, v72, s[4:5]
	s_cselect_b64 s[4:5], -1, 0
	ds_write2_b32 v8, v37, v36 offset0:16 offset1:81
	ds_write2_b32 v8, v35, v34 offset0:146 offset1:211
	v_add_u32_e32 v8, 0x1400, v12
	s_and_b64 s[4:5], vcc, s[4:5]
	ds_write2_b32 v8, v33, v32 offset0:20 offset1:85
	ds_write2_b32 v8, v31, v30 offset0:150 offset1:215
	v_add_u32_e32 v8, 0x1800, v12
	s_cmp_lt_i32 s48, s76
	ds_write2_b32 v8, v45, v44 offset0:24 offset1:89
	ds_write2_b32 v8, v43, v42 offset0:154 offset1:219
	v_add_u32_e32 v8, 0x1c00, v12
	s_waitcnt vmcnt(3)
	v_cndmask_b32_e64 v71, 0, v71, s[4:5]
	s_cselect_b64 s[4:5], -1, 0
	ds_write2_b32 v8, v41, v40 offset0:28 offset1:93
	ds_write2_b32 v8, v39, v38 offset0:158 offset1:223
	v_add_u32_e32 v8, 0x2000, v12
	s_and_b64 s[4:5], vcc, s[4:5]
	ds_write2_b32 v8, v53, v52 offset0:32 offset1:97
	ds_write2_b32 v8, v51, v50 offset0:162 offset1:227
	v_add_u32_e32 v8, 0x2400, v12
	s_cmp_lt_i32 s49, s76
	ds_write2_b32 v8, v49, v48 offset0:36 offset1:101
	ds_write2_b32 v8, v47, v46 offset0:166 offset1:231
	v_add_u32_e32 v8, 0x2800, v12
	s_waitcnt vmcnt(2)
	v_cndmask_b32_e64 v77, 0, v77, s[4:5]
	s_cselect_b64 s[4:5], -1, 0
	ds_write2_b32 v8, v61, v60 offset0:40 offset1:105
	ds_write2_b32 v8, v59, v58 offset0:170 offset1:235
	v_add_u32_e32 v8, 0x2c00, v12
	s_and_b64 s[4:5], vcc, s[4:5]
	ds_write2_b32 v8, v57, v56 offset0:44 offset1:109
	ds_write2_b32 v8, v55, v54 offset0:174 offset1:239
	v_add_u32_e32 v8, 0x3000, v12
	s_cmp_lt_i32 s44, s76
	ds_write2_b32 v8, v70, v69 offset0:48 offset1:113
	ds_write2_b32 v8, v68, v67 offset0:178 offset1:243
	v_add_u32_e32 v8, 0x3400, v12
	s_waitcnt vmcnt(1)
	v_cndmask_b32_e64 v76, 0, v76, s[4:5]
	s_cselect_b64 s[4:5], -1, 0
	ds_write2_b32 v8, v66, v64 offset0:52 offset1:117
	ds_write2_b32 v8, v63, v62 offset0:182 offset1:247
	v_add_u32_e32 v8, 0x3800, v12
	s_and_b64 vcc, vcc, s[4:5]
	ds_write2_b32 v8, v65, v74 offset0:56 offset1:121
	ds_write2_b32 v8, v73, v72 offset0:186 offset1:251
	v_add_u32_e32 v8, 0x3c00, v12
	s_waitcnt vmcnt(0)
	v_cndmask_b32_e32 v75, 0, v75, vcc
	ds_write2_b32 v8, v71, v77 offset0:60 offset1:125
	ds_write2_b32 v8, v76, v75 offset0:190 offset1:255
	s_waitcnt lgkmcnt(0)
	ds_read2_b32 v[16:17], v14 offset1:65
	v_add_u32_e32 v24, s59, v13
	v_mul_lo_u32 v22, s57, v24
	s_ashr_i32 s59, s58, 31
	v_readlane_b32 s76, v254, 31
	s_waitcnt lgkmcnt(0)
; __device__ __forceinline__ unsigned cvt_pk_bf16(float lo, float hi) { unsigned r; asm volatile("v_cvt_pk_bf16_f32 %0, %1, %2" : "=v"(r) : "v"(lo), "v"(hi)); return r; }
; #define LAS __attribute__((address_space(3)))
; #define LDS_WAIT() asm volatile("s_waitcnt lgkmcnt(0)" ::: "memory")
; __device__ __forceinline__ void conv_store(const ConvItem& ci, LAS float* scr, int lane, const float (&v)[64]) {
;     ...
;     LDS_WAIT(); asm volatile("" ::: "memory");
; #pragma unroll
;     for (int j = 0; j < 8; ++j) { const int n = (lane >> 3) + 8 * j; const LAS float* s = scr + (8 * c) * 65 + n;
;         v4u o; o.x = cvt_pk_bf16(s[0 * 65] * s0[0], s[1 * 65] * s0[1]); o.y = cvt_pk_bf16(s[2 * 65] * s0[2], s[3 * 65] * s0[3]); o.z = cvt_pk_bf16(s[4 * 65] * s1[0], s[5 * 65] * s1[1]); o.w = cvt_pk_bf16(s[6 * 65] * s1[2], s[7 * 65] * s1[3]);
;         *(v4u*)(ci.dst + (size_t)(ci.drow0 + n) * ci.ldd + ci.k0 + 8 * c) = o; }
	v_mul_f32_e32 v8, v4, v16
	v_mul_f32_e32 v15, v5, v17
	v_cvt_pk_bf16_f32 v16, v8, v15
	ds_read2_b32 v[18:19], v14 offset0:130 offset1:195
	s_add_i32 s3, s3, s33
	s_add_i32 s66, s66, s67
	s_add_i32 s68, s68, s69
	s_add_i32 s70, s70, s71
	s_waitcnt lgkmcnt(0)
	v_mul_f32_e32 v15, v7, v19
	v_mul_f32_e32 v8, v6, v18
	v_cvt_pk_bf16_f32 v17, v8, v15
	v_add_u32_e32 v15, 0x400, v14
	ds_read2_b32 v[18:19], v15 offset0:4 offset1:69
	s_add_i32 s72, s72, s73
	s_add_i32 s74, s74, s75
	v_readlane_b32 s78, v254, 33
	v_readlane_b32 s79, v254, 34
	s_waitcnt lgkmcnt(0)
	v_mul_f32_e32 v8, v0, v18
	v_mul_f32_e32 v18, v1, v19
	v_cvt_pk_bf16_f32 v18, v8, v18
	ds_read2_b32 v[20:21], v15 offset0:134 offset1:199
	v_readlane_b32 s80, v255, 21
	v_readlane_b32 s77, v254, 32
	s_movk_i32 s78, 0x1580
	v_readlane_b32 s82, v255, 23
	s_waitcnt lgkmcnt(0)
	v_mul_f32_e32 v8, v2, v20
	v_mul_f32_e32 v19, v3, v21
	v_cvt_pk_bf16_f32 v19, v8, v19
	v_ashrrev_i32_e32 v8, 31, v24
	v_mul_lo_u32 v8, s56, v8
	v_mad_u64_u32 v[20:21], s[4:5], s56, v24, 0
	v_add3_u32 v21, v21, v8, v22
	ds_read2_b32 v[22:23], v14 offset0:8 offset1:73
	v_lshl_add_u64 v[20:21], v[20:21], 1, s[60:61]
	s_lshl_b64 s[4:5], s[58:59], 1
	v_lshl_add_u64 v[20:21], v[20:21], 0, s[4:5]
	v_lshlrev_b32_e32 v8, 1, v10
	v_lshl_add_u64 v[20:21], v[20:21], 0, v[8:9]
	global_store_dwordx4 v[20:21], v[16:19], off
	s_cmpk_lt_i32 s3, 18688
	v_readlane_b32 s83, v255, 24
	s_waitcnt lgkmcnt(0)
	v_mul_f32_e32 v16, v4, v22
	v_mul_f32_e32 v17, v5, v23
	v_cvt_pk_bf16_f32 v16, v16, v17
	ds_read2_b32 v[18:19], v14 offset0:138 offset1:203
	s_mov_b32 s79, 0x3f22f983
	s_mov_b32 s85, 0xbfc90fda
	s_brev_b32 s86, 1
	s_movk_i32 s87, 0x1f8
	s_waitcnt lgkmcnt(0)
	v_mul_f32_e32 v17, v6, v18
	v_mul_f32_e32 v18, v7, v19
	v_cvt_pk_bf16_f32 v17, v17, v18
	ds_read2_b32 v[18:19], v15 offset0:12 offset1:77
	s_mov_b64 s[88:89], 0x80
	s_mov_b64 s[92:93], 0x4000
	s_mov_b64 s[94:95], 0x4800
	v_readlane_b32 s81, v255, 22
	s_waitcnt lgkmcnt(0)
	v_mul_f32_e32 v18, v0, v18
	v_mul_f32_e32 v19, v1, v19
	v_cvt_pk_bf16_f32 v18, v18, v19
	ds_read2_b32 v[20:21], v15 offset0:142 offset1:207
	s_waitcnt lgkmcnt(0)
	v_mul_f32_e32 v19, v2, v20
	v_mul_f32_e32 v20, v3, v21
	v_cvt_pk_bf16_f32 v19, v19, v20
	v_add_u32_e32 v20, 8, v24
	v_ashrrev_i32_e32 v21, 31, v20
	v_mul_lo_u32 v22, s56, v21
	v_mul_lo_u32 v23, s57, v20
	v_mad_u64_u32 v[20:21], s[6:7], s56, v20, 0
	v_add3_u32 v21, v21, v22, v23
	ds_read2_b32 v[22:23], v14 offset0:16 offset1:81
	v_lshl_add_u64 v[20:21], v[20:21], 1, s[60:61]
	v_lshl_add_u64 v[20:21], v[20:21], 0, s[4:5]
	v_lshl_add_u64 v[20:21], v[20:21], 0, v[8:9]
	global_store_dwordx4 v[20:21], v[16:19], off
	s_waitcnt lgkmcnt(0)
	s_nop 0
	v_mul_f32_e32 v16, v4, v22
	v_mul_f32_e32 v17, v5, v23
	v_cvt_pk_bf16_f32 v16, v16, v17
	ds_read2_b32 v[18:19], v14 offset0:146 offset1:211
	s_waitcnt lgkmcnt(0)
	v_mul_f32_e32 v17, v6, v18
	v_mul_f32_e32 v18, v7, v19
	v_cvt_pk_bf16_f32 v17, v17, v18
	ds_read2_b32 v[18:19], v15 offset0:20 offset1:85
	s_waitcnt lgkmcnt(0)
	v_mul_f32_e32 v18, v0, v18
	v_mul_f32_e32 v19, v1, v19
	v_cvt_pk_bf16_f32 v18, v18, v19
	ds_read2_b32 v[20:21], v15 offset0:150 offset1:215
	s_waitcnt lgkmcnt(0)
	v_mul_f32_e32 v19, v2, v20
	v_mul_f32_e32 v20, v3, v21
	v_cvt_pk_bf16_f32 v19, v19, v20
	v_add_u32_e32 v20, 16, v24
	v_ashrrev_i32_e32 v21, 31, v20
	v_mul_lo_u32 v22, s56, v21
	v_mul_lo_u32 v23, s57, v20
	v_mad_u64_u32 v[20:21], s[6:7], s56, v20, 0
	v_add3_u32 v21, v21, v22, v23
	ds_read2_b32 v[22:23], v14 offset0:24 offset1:89
	v_lshl_add_u64 v[20:21], v[20:21], 1, s[60:61]
	v_lshl_add_u64 v[20:21], v[20:21], 0, s[4:5]
	v_lshl_add_u64 v[20:21], v[20:21], 0, v[8:9]
	global_store_dwordx4 v[20:21], v[16:19], off
	s_waitcnt lgkmcnt(0)
	s_nop 0
	v_mul_f32_e32 v16, v4, v22
	v_mul_f32_e32 v17, v5, v23
	v_cvt_pk_bf16_f32 v16, v16, v17
	ds_read2_b32 v[18:19], v14 offset0:154 offset1:219
	s_waitcnt lgkmcnt(0)
	v_mul_f32_e32 v17, v6, v18
	v_mul_f32_e32 v18, v7, v19
	v_cvt_pk_bf16_f32 v17, v17, v18
	ds_read2_b32 v[18:19], v15 offset0:28 offset1:93
	s_waitcnt lgkmcnt(0)
	v_mul_f32_e32 v18, v0, v18
	v_mul_f32_e32 v19, v1, v19
	v_cvt_pk_bf16_f32 v18, v18, v19
	ds_read2_b32 v[20:21], v15 offset0:158 offset1:223
	s_waitcnt lgkmcnt(0)
; __device__ __forceinline__ unsigned cvt_pk_bf16(float lo, float hi) { unsigned r; asm volatile("v_cvt_pk_bf16_f32 %0, %1, %2" : "=v"(r) : "v"(lo), "v"(hi)); return r; }
; #define LAS __attribute__((address_space(3)))
; #define LDS_WAIT() asm volatile("s_waitcnt lgkmcnt(0)" ::: "memory")
; __device__ __forceinline__ void conv_store(const ConvItem& ci, LAS float* scr, int lane, const float (&v)[64]) {
;     ...
;     for (int j = 0; j < 8; ++j) { const int n = (lane >> 3) + 8 * j; const LAS float* s = scr + (8 * c) * 65 + n;
;         v4u o; o.x = cvt_pk_bf16(s[0 * 65] * s0[0], s[1 * 65] * s0[1]); o.y = cvt_pk_bf16(s[2 * 65] * s0[2], s[3 * 65] * s0[3]); o.z = cvt_pk_bf16(s[4 * 65] * s1[0], s[5 * 65] * s1[1]); o.w = cvt_pk_bf16(s[6 * 65] * s1[2], s[7 * 65] * s1[3]);
;         *(v4u*)(ci.dst + (size_t)(ci.drow0 + n) * ci.ldd + ci.k0 + 8 * c) = o; }
;     LDS_WAIT(); asm volatile("" ::: "memory");
	v_mul_f32_e32 v19, v2, v20
	v_mul_f32_e32 v20, v3, v21
	v_cvt_pk_bf16_f32 v19, v19, v20
	v_add_u32_e32 v20, 24, v24
	v_ashrrev_i32_e32 v21, 31, v20
	v_mul_lo_u32 v22, s56, v21
	v_mul_lo_u32 v23, s57, v20
	v_mad_u64_u32 v[20:21], s[6:7], s56, v20, 0
	v_add3_u32 v21, v21, v22, v23
	ds_read2_b32 v[22:23], v14 offset0:32 offset1:97
	v_lshl_add_u64 v[20:21], v[20:21], 1, s[60:61]
	v_lshl_add_u64 v[20:21], v[20:21], 0, s[4:5]
	v_lshl_add_u64 v[20:21], v[20:21], 0, v[8:9]
	global_store_dwordx4 v[20:21], v[16:19], off
	s_waitcnt lgkmcnt(0)
	s_nop 0
	v_mul_f32_e32 v16, v4, v22
	v_mul_f32_e32 v17, v5, v23
	v_cvt_pk_bf16_f32 v16, v16, v17
	ds_read2_b32 v[18:19], v14 offset0:162 offset1:227
	s_waitcnt lgkmcnt(0)
	v_mul_f32_e32 v17, v6, v18
	v_mul_f32_e32 v18, v7, v19
	v_cvt_pk_bf16_f32 v17, v17, v18
	ds_read2_b32 v[18:19], v15 offset0:36 offset1:101
	s_waitcnt lgkmcnt(0)
	v_mul_f32_e32 v18, v0, v18
	v_mul_f32_e32 v19, v1, v19
	v_cvt_pk_bf16_f32 v18, v18, v19
	ds_read2_b32 v[20:21], v15 offset0:166 offset1:231
	s_waitcnt lgkmcnt(0)
	v_mul_f32_e32 v19, v2, v20
	v_mul_f32_e32 v20, v3, v21
	v_cvt_pk_bf16_f32 v19, v19, v20
	v_add_u32_e32 v20, 32, v24
	v_ashrrev_i32_e32 v21, 31, v20
	v_mul_lo_u32 v22, s56, v21
	v_mul_lo_u32 v23, s57, v20
	v_mad_u64_u32 v[20:21], s[6:7], s56, v20, 0
	v_add3_u32 v21, v21, v22, v23
	ds_read2_b32 v[22:23], v14 offset0:40 offset1:105
	v_lshl_add_u64 v[20:21], v[20:21], 1, s[60:61]
	v_lshl_add_u64 v[20:21], v[20:21], 0, s[4:5]
	v_lshl_add_u64 v[20:21], v[20:21], 0, v[8:9]
	global_store_dwordx4 v[20:21], v[16:19], off
	s_waitcnt lgkmcnt(0)
	s_nop 0
	v_mul_f32_e32 v16, v4, v22
	v_mul_f32_e32 v17, v5, v23
	v_cvt_pk_bf16_f32 v16, v16, v17
	ds_read2_b32 v[18:19], v14 offset0:170 offset1:235
	s_waitcnt lgkmcnt(0)
	v_mul_f32_e32 v17, v6, v18
	v_mul_f32_e32 v18, v7, v19
	v_cvt_pk_bf16_f32 v17, v17, v18
	ds_read2_b32 v[18:19], v15 offset0:44 offset1:109
	s_waitcnt lgkmcnt(0)
	v_mul_f32_e32 v18, v0, v18
	v_mul_f32_e32 v19, v1, v19
	v_cvt_pk_bf16_f32 v18, v18, v19
	ds_read2_b32 v[20:21], v15 offset0:174 offset1:239
	s_waitcnt lgkmcnt(0)
	v_mul_f32_e32 v19, v2, v20
	v_mul_f32_e32 v20, v3, v21
	v_cvt_pk_bf16_f32 v19, v19, v20
	v_add_u32_e32 v20, 40, v24
	v_ashrrev_i32_e32 v21, 31, v20
	v_mul_lo_u32 v22, s56, v21
	v_mul_lo_u32 v23, s57, v20
	v_mad_u64_u32 v[20:21], s[6:7], s56, v20, 0
	v_add3_u32 v21, v21, v22, v23
	ds_read2_b32 v[22:23], v14 offset0:48 offset1:113
	v_lshl_add_u64 v[20:21], v[20:21], 1, s[60:61]
	v_lshl_add_u64 v[20:21], v[20:21], 0, s[4:5]
	v_lshl_add_u64 v[20:21], v[20:21], 0, v[8:9]
	global_store_dwordx4 v[20:21], v[16:19], off
	s_waitcnt lgkmcnt(0)
	s_nop 0
	v_mul_f32_e32 v16, v4, v22
	v_mul_f32_e32 v17, v5, v23
	v_cvt_pk_bf16_f32 v16, v16, v17
	ds_read2_b32 v[18:19], v14 offset0:178 offset1:243
	s_waitcnt lgkmcnt(0)
	v_mul_f32_e32 v17, v6, v18
	v_mul_f32_e32 v18, v7, v19
	v_cvt_pk_bf16_f32 v17, v17, v18
	ds_read2_b32 v[18:19], v15 offset0:52 offset1:117
	s_waitcnt lgkmcnt(0)
	v_mul_f32_e32 v18, v0, v18
	v_mul_f32_e32 v19, v1, v19
	v_cvt_pk_bf16_f32 v18, v18, v19
	ds_read2_b32 v[20:21], v15 offset0:182 offset1:247
	s_waitcnt lgkmcnt(0)
	v_mul_f32_e32 v19, v2, v20
	v_mul_f32_e32 v20, v3, v21
	v_cvt_pk_bf16_f32 v19, v19, v20
	v_add_u32_e32 v20, 48, v24
	v_ashrrev_i32_e32 v21, 31, v20
	v_mul_lo_u32 v22, s56, v21
	v_mul_lo_u32 v23, s57, v20
	v_mad_u64_u32 v[20:21], s[6:7], s56, v20, 0
	v_add3_u32 v21, v21, v22, v23
	ds_read2_b32 v[22:23], v14 offset0:56 offset1:121
	v_lshl_add_u64 v[20:21], v[20:21], 1, s[60:61]
	v_lshl_add_u64 v[20:21], v[20:21], 0, s[4:5]
	v_lshl_add_u64 v[20:21], v[20:21], 0, v[8:9]
	global_store_dwordx4 v[20:21], v[16:19], off
	s_waitcnt lgkmcnt(0)
	v_mul_f32_e32 v4, v4, v22
	v_mul_f32_e32 v5, v5, v23
	v_cvt_pk_bf16_f32 v4, v4, v5
	ds_read2_b32 v[16:17], v14 offset0:186 offset1:251
	s_waitcnt lgkmcnt(0)
	v_mul_f32_e32 v5, v6, v16
	v_mul_f32_e32 v6, v7, v17
	v_cvt_pk_bf16_f32 v5, v5, v6
	ds_read2_b32 v[6:7], v15 offset0:60 offset1:125
	s_waitcnt lgkmcnt(0)
	v_mul_f32_e32 v0, v0, v6
	v_mul_f32_e32 v1, v1, v7
	v_cvt_pk_bf16_f32 v6, v0, v1
	ds_read2_b32 v[0:1], v15 offset0:190 offset1:255
	s_waitcnt lgkmcnt(0)
	v_mul_f32_e32 v0, v2, v0
	v_mul_f32_e32 v1, v3, v1
	v_cvt_pk_bf16_f32 v7, v0, v1
	v_add_u32_e32 v0, 56, v24
	v_ashrrev_i32_e32 v1, 31, v0
	v_mul_lo_u32 v2, s56, v1
	v_mul_lo_u32 v3, s57, v0
	v_mad_u64_u32 v[0:1], s[6:7], s56, v0, 0
	v_add3_u32 v1, v1, v2, v3
	v_lshl_add_u64 v[0:1], v[0:1], 1, s[60:61]
	v_lshl_add_u64 v[0:1], v[0:1], 0, s[4:5]
	v_lshl_add_u64 v[0:1], v[0:1], 0, v[8:9]
	global_store_dwordx4 v[0:1], v[4:7], off
	s_waitcnt lgkmcnt(0)
	s_cbranch_scc0 .Lcvp130_ret
